# MoE full-tile units: next unit's DMA prefetch issued after the epilogue's own loads (epilogue no longer waits for the prefetch); + helper n=4
# baseline (speedup 1.0000x reference)
; DI int lane_id_now() { int l; asm volatile("v_mbcnt_lo_u32_b32 %0, -1, 0\n\tv_mbcnt_hi_u32_b32 %0, -1, %0" : "=v"(l)); return l; }
; #define P_STAGE_A(slot, half, kt) do { _Pragma("unroll") for (int _i = 0; _i < 2; ++_i) { const unsigned _m0 = ldsw + (unsigned)((slot) + _i * 8192); const unsigned _so = (unsigned)(kt) * 128u; \
;     asm volatile("s_mov_b32 m0, %0\n\ts_nop 4\n\tbuffer_load_dwordx4 %1, %2, %3 offen lds" :: "s"(_m0), "v"(voffA[half][_i]), "s"(rsA), "s"(_so) : "m0", "memory"); } } while (0)
; #define P_STAGE_B(slot, half, kt) do { _Pragma("unroll") for (int _i = 0; _i < 2; ++_i) { const unsigned _m0 = ldsw + (unsigned)((slot) + _i * 8192); const unsigned _so = (unsigned)(kt) * 128u + (half) * bt_half + _i * bt_piece; \
;     asm volatile("s_mov_b32 m0, %0\n\ts_nop 4\n\tbuffer_load_dwordx4 %1, %2, %3 offen lds" :: "s"(_m0), "v"(voffB0), "s"(rsB), "s"(_so) : "m0", "memory"); } } while (0)
; #define P_STAGE_A(slot, half, kt) do { _Pragma("unroll") for (int _i = 0; _i < 2; ++_i) { const unsigned _m0 = ldsw + (unsigned)((slot) + _i * 8192); const unsigned _so = (unsigned)(kt) * 128u; \
;     asm volatile("s_mov_b32 m0, %0\n\ts_nop 4\n\tbuffer_load_dwordx4 %1, %2, %3 offen lds" :: "s"(_m0), "v"(voffA[half][_i]), "s"(rsA), "s"(_so) : "m0", "memory"); } } while (0)
; template <class Cfg>
; DI void f8dma_issue_prologue_st(LDS_AS unsigned char* lds, const Cfg& cfg) {
;     ...
;   P_STAGE_B(G_SB(0, 0), 0, 0); P_STAGE_A(G_SA(0, 0), 0, 0); P_STAGE_B(G_SB(0, 1), 1, 0); P_STAGE_A(G_SA(0, 1), 1, 0);
;   P_STAGE_B(G_SB(1, 0), 0, 1); P_STAGE_A(G_SA(1, 0), 0, 1); P_STAGE_B(G_SB(1, 1), 1, 1);
;     ...
;   if (has_nxt) f8dma_issue_prologue_st(lds, nxt);
;   {
;     const int wid2 = wid, ln2 = lane_id_now(), wr2 = wid2 >> 2, wc2 = wid2 & 3, fr2 = ln2 & 15, fq2 = ln2 >> 4;
;     if (PMODE == 0 && EPI_HOIST) {
;       typename Cfg::RowTok tok[2][4];
; #pragma unroll
;       for (int ai = 0; ai < 2; ++ai)
; #pragma unroll
;         for (int m = 0; m < 4; ++m) tok[ai][m] = cfg.row_tok(ai * 128 + wr2 * 64 + m * 16 + fr2);
;       typename Cfg::ColCtx cc[2];
; #pragma unroll
;       for (int bj = 0; bj < 2; ++bj) cc[bj] = cfg.col_ctx(bj, wc2, fq2);
.LBB0_1418:
	s_mov_b64 s[100:101], s[2:3]
	v_readlane_b32 s87, v255, 12
.LBB0_1420:
	s_lshl_b32 s2, s22, 6
	v_mbcnt_lo_u32_b32 v124, -1, 0
	v_mbcnt_hi_u32_b32 v124, -1, v124
	s_add_i32 s2, s2, s65
	v_and_b32_e32 v72, 15, v124
	v_add_u32_e32 v144, s2, v72
	v_min_i32_e32 v72, s28, v144
	v_add_u32_e32 v163, 16, v144
	v_add_u32_e32 v161, 32, v144
	v_add_u32_e32 v159, 48, v144
	v_add_u32_e32 v157, 0x80, v144
	v_add_u32_e32 v155, 0x90, v144
	v_add_u32_e32 v153, 0xa0, v144
	v_add_u32_e32 v151, 0xb0, v144
	v_add_u32_e32 v72, s29, v72
	v_min_i32_e32 v74, s28, v163
	v_min_i32_e32 v76, s28, v161
	v_min_i32_e32 v78, s28, v159
	v_min_i32_e32 v80, s28, v157
	v_min_i32_e32 v82, s28, v155
	v_min_i32_e32 v120, s28, v153
	v_min_i32_e32 v122, s28, v151
	v_ashrrev_i32_e32 v73, 31, v72
	v_add_u32_e32 v74, s29, v74
	v_add_u32_e32 v76, s29, v76
	v_add_u32_e32 v78, s29, v78
	v_add_u32_e32 v80, s29, v80
	v_add_u32_e32 v82, s29, v82
	v_add_u32_e32 v120, s29, v120
	v_add_u32_e32 v122, s29, v122
	v_lshl_add_u64 v[72:73], v[72:73], 2, s[92:93]
	v_ashrrev_i32_e32 v75, 31, v74
	v_ashrrev_i32_e32 v77, 31, v76
	v_ashrrev_i32_e32 v79, 31, v78
	v_ashrrev_i32_e32 v81, 31, v80
	v_ashrrev_i32_e32 v83, 31, v82
	v_ashrrev_i32_e32 v121, 31, v120
	v_ashrrev_i32_e32 v123, 31, v122
	v_lshl_add_u64 v[74:75], v[74:75], 2, s[92:93]
	v_lshl_add_u64 v[76:77], v[76:77], 2, s[92:93]
	v_lshl_add_u64 v[78:79], v[78:79], 2, s[92:93]
	v_lshl_add_u64 v[80:81], v[80:81], 2, s[92:93]
	v_lshl_add_u64 v[82:83], v[82:83], 2, s[92:93]
	v_lshl_add_u64 v[120:121], v[120:121], 2, s[92:93]
	v_lshl_add_u64 v[122:123], v[122:123], 2, s[92:93]
	global_load_dword v145, v[72:73], off
	global_load_dword v164, v[74:75], off
	global_load_dword v162, v[76:77], off
	global_load_dword v160, v[78:79], off
	global_load_dword v158, v[80:81], off
	global_load_dword v156, v[82:83], off
	global_load_dword v154, v[120:121], off
	global_load_dword v152, v[122:123], off
	s_lshl_b32 s2, s64, 7
	s_lshl_b32 s3, s17, 5
	v_ashrrev_i32_e32 v72, 1, v124
	v_and_b32_e32 v72, -8, v72
	s_or_b32 s2, s3, s2
	v_add_u32_e32 v146, s2, v72
	s_lshl_b32 s2, s16, 12
	v_readlane_b32 s68, v254, 6
	s_ashr_i32 s3, s2, 31
	v_readlane_b32 s70, v254, 8
	v_readlane_b32 s71, v254, 9
	s_lshl_b64 s[2:3], s[2:3], 2
	s_mov_b64 s[62:63], s[70:71]
	s_add_u32 s2, s62, s2
	s_addc_u32 s3, s63, s3
	v_ashrrev_i32_e32 v147, 31, v146
	v_lshl_add_u64 v[72:73], v[146:147], 2, s[2:3]
	global_load_dwordx4 v[128:131], v[72:73], off
	global_load_dwordx4 v[120:123], v[72:73], off offset:16
	v_lshl_add_u64 v[74:75], v[72:73], 0, s[0:1]
	v_add_co_u32_e32 v72, vcc, s37, v72
	v_readlane_b32 s69, v254, 7
	s_nop 0
	v_addc_co_u32_e32 v73, vcc, 0, v73, vcc
	global_load_dwordx4 v[132:135], v[72:73], off
	global_load_dwordx4 v[124:127], v[74:75], off offset:16
	s_and_b64 vcc, exec, s[100:101]
	s_cbranch_vccnz .Lpfm0_none
	v_mbcnt_lo_u32_b32 v76, -1, 0
	v_mbcnt_hi_u32_b32 v76, -1, v76
	s_ashr_i32 s15, s14, 31
	v_or_b32_e32 v72, s87, v76
	v_lshrrev_b32_e32 v77, 3, v76
	v_readfirstlane_b32 s2, v72
	s_ashr_i32 s23, s2, 6
	s_lshl_b32 s2, s23, 3
	s_and_b32 s3, s2, 16
	v_and_or_b32 v78, v77, 4, s2
	s_add_i32 s3, s3, s48
	s_lshl_b32 s3, s3, 7
	s_and_b32 s2, s2, 0x1fffe0
	v_lshlrev_b32_e32 v78, 1, v78
	v_xor_b32_e32 v77, v77, v76
	s_add_i32 s3, s3, s2
	v_and_b32_e32 v78, 24, v78
	v_bfe_u32 v76, v76, 3, 2
	v_or3_b32 v76, s3, v78, v76
	s_lshl_b64 s[2:3], s[14:15], 23
	v_lshl_add_u32 v72, v72, 2, 0
	s_add_u32 s4, s50, s2
	v_add_u32_e32 v74, 0x22410, v72
	s_addc_u32 s2, s51, s3
	ds_read2st64_b32 v[72:73], v74 offset1:8
	ds_read2st64_b32 v[74:75], v74 offset0:16 offset1:24
	v_lshlrev_b32_e32 v77, 4, v77
	s_and_b32 s5, s2, 0xffff
	s_lshl_b32 s2, s23, 10
	v_and_b32_e32 v77, 0x70, v77
	s_add_i32 s2, s2, 0
	v_lshl_or_b32 v76, v76, 11, v77
	s_add_i32 s3, s2, 0x10010
	s_mov_b32 m0, s3
	s_nop 0
	buffer_load_dwordx4 v76, s[4:7], s34 offen lds
	s_add_i32 s3, s2, 0x12010
	s_mov_b32 m0, s3
	s_nop 0
	buffer_load_dwordx4 v76, s[4:7], s7 offen lds
	s_add_i32 s3, s2, 16
	s_waitcnt lgkmcnt(1)
	s_mov_b32 m0, s3
	s_nop 0
	buffer_load_dwordx4 v72, s[8:11], s34 offen lds
	s_add_i32 s3, s2, 0x2010
	s_mov_b32 m0, s3
	s_nop 0
	buffer_load_dwordx4 v73, s[8:11], s34 offen lds
	s_add_i32 s3, s2, 0x14010
	s_mov_b32 m0, s3
	s_nop 0
	buffer_load_dwordx4 v76, s[4:7], s37 offen lds
	s_add_i32 s3, s2, 0x16010
	s_mov_b32 m0, s3
	s_nop 0
	buffer_load_dwordx4 v76, s[4:7], s56 offen lds
	s_add_i32 s3, s2, 0x4010
	s_waitcnt lgkmcnt(0)
	s_mov_b32 m0, s3
	s_nop 0
	buffer_load_dwordx4 v74, s[8:11], s34 offen lds
	s_add_i32 s3, s2, 0x6010
	s_mov_b32 m0, s3
	s_nop 0
	buffer_load_dwordx4 v75, s[8:11], s34 offen lds
	s_add_i32 s3, s2, 0x18010
	s_mov_b32 m0, s3
	s_nop 0
	buffer_load_dwordx4 v76, s[4:7], s35 offen lds
	s_add_i32 s3, s2, 0x1a010
	s_mov_b32 m0, s3
	s_nop 0
	buffer_load_dwordx4 v76, s[4:7], s43 offen lds
	s_add_i32 s3, s2, 0x8010
	s_mov_b32 m0, s3
	s_nop 0
	buffer_load_dwordx4 v72, s[8:11], s35 offen lds
	s_add_i32 s3, s2, 0xa010
	s_mov_b32 m0, s3
	s_nop 0
	buffer_load_dwordx4 v73, s[8:11], s35 offen lds
	s_add_i32 s3, s2, 0x1c010
	s_mov_b32 m0, s3
	s_nop 0
	buffer_load_dwordx4 v76, s[4:7], s44 offen lds
	s_add_i32 s2, s2, 0x1e010
	s_mov_b32 m0, s2
	s_nop 0
	buffer_load_dwordx4 v76, s[4:7], s45 offen lds
	s_branch .Lpfm0_done

;     ...
;       if constexpr (Cfg::PAIR_BJ) {
; #pragma unroll
;         for (int ai = 0; ai < 2; ++ai)
; #pragma unroll
;           for (int m = 0; m < 4; ++m) cfg.epi_pair(tok[ai][m], cc[0], cc[1], acc[ai][0][m][0], acc[ai][0][m][1], acc[ai][1][m][0], acc[ai][1][m][1]);
;   DI int glu4(const ColCtx& c, const f32x4& v0, const f32x4& v1) const {
;     float o[4];
; #pragma unroll
;     for (int i = 0; i < 4; ++i) {
;       const float g = fminf(v0[i] + c.bg[i], 7.f);
;       const float up = __builtin_amdgcn_fmed3f(v1[i] + c.bu[i], -7.f, 7.f);
;       const float sg = __builtin_amdgcn_rcpf(1.f + __builtin_amdgcn_exp2f(g * (-1.702f * 1.44269504088896f)));
;       o[i] = fmaf(up, 4.f, 4.f) * (g * sg);
;     }
;     return pack4_fp8(o[0], o[1], o[2], o[3]);
;   }
;   DI void epi_pair(RowTok a, const ColCtx& c0, const ColCtx& c1, const f32x4& g0, const f32x4& u0, const f32x4& g1, const f32x4& u1) const {
;     if (a < 0) return;
;     u32x2 pk; pk.x = (unsigned)glu4(c0, g0, u0); pk.y = (unsigned)glu4(c1, g1, u1);
;     *(u32x2*)(p.actq + (size_t)a * 2048 + c0.j0) = pk;
.Lpfm0_done:
	v_cmp_gt_i32_e32 vcc, s55, v144
	v_readlane_b32 s72, v254, 10
	v_readlane_b32 s73, v254, 11
	v_readlane_b32 s74, v254, 12
	v_readlane_b32 s75, v254, 13
	s_waitcnt vmcnt(25)
	v_cndmask_b32_e32 v252, -1, v145, vcc
	v_cmp_lt_i32_e32 vcc, -1, v252
	s_and_saveexec_b64 s[2:3], vcc
	v_readlane_b32 s68, v254, 47
	v_readlane_b32 s70, v254, 49
	v_readlane_b32 s71, v254, 50
	v_readlane_b32 s69, v254, 48
	s_cbranch_execz .LBB0_1422
	s_waitcnt vmcnt(17)
	v_add_f32_e32 v72, v140, v128
	v_min_f32_e32 v72, 0x40e00000, v72
	v_mul_f32_e32 v73, 0xc01d265f, v72
	v_exp_f32_e32 v73, v73
	v_add_f32_e32 v75, v141, v129
	v_min_f32_e32 v75, 0x40e00000, v75
	v_mul_f32_e32 v76, 0xc01d265f, v75
	v_add_f32_e32 v73, 1.0, v73
	v_rcp_f32_e32 v73, v73
	s_waitcnt vmcnt(15)
	v_add_f32_e32 v74, v136, v132
	v_med3_f32 v74, v74, s46, v150
	v_fma_f32 v74, v74, 4.0, 4.0
	v_mul_f32_e32 v72, v72, v73
	v_exp_f32_e32 v73, v76
	v_add_f32_e32 v76, v142, v130
	v_min_f32_e32 v76, 0x40e00000, v76
	v_mul_f32_e32 v77, 0xc01d265f, v76
	v_add_f32_e32 v73, 1.0, v73
	v_rcp_f32_e32 v73, v73
	v_exp_f32_e32 v77, v77
	v_mul_f32_e32 v74, v74, v72
	v_add_f32_e32 v72, v137, v133
	v_med3_f32 v72, v72, s46, v150
	v_fma_f32 v72, v72, 4.0, 4.0
	v_mul_f32_e32 v73, v75, v73
	v_mul_f32_e32 v73, v72, v73
	v_add_f32_e32 v72, 1.0, v77
	v_rcp_f32_e32 v72, v72
	v_add_f32_e32 v75, v138, v134
	v_med3_f32 v75, v75, s46, v150
	v_fma_f32 v75, v75, 4.0, 4.0
	v_mul_f32_e32 v72, v76, v72
	v_mul_f32_e32 v75, v75, v72
	v_add_f32_e32 v72, v139, v135
	v_med3_f32 v72, v72, s46, v150
	v_fma_f32 v78, v72, 4.0, 4.0
	v_mov_b32_e32 v72, v253
	v_add_f32_e32 v76, v143, v131
	v_cvt_pk_fp8_f32 v72, v74, v73
	v_add_f32_e32 v73, v116, v120
	v_min_f32_e32 v76, 0x40e00000, v76
	v_min_f32_e32 v73, 0x40e00000, v73
	v_mul_f32_e32 v77, 0xc01d265f, v76
	v_mul_f32_e32 v74, 0xc01d265f, v73
	v_exp_f32_e32 v77, v77
	v_exp_f32_e32 v74, v74
	v_add_f32_e32 v77, 1.0, v77
	v_add_f32_e32 v74, 1.0, v74
	v_rcp_f32_e32 v77, v77
	v_rcp_f32_e32 v74, v74
	v_mul_f32_e32 v76, v76, v77
	v_mul_f32_e32 v73, v73, v74
	v_add_f32_e32 v74, v117, v121
	v_mul_f32_e32 v76, v78, v76
	v_min_f32_e32 v74, 0x40e00000, v74
	v_cvt_pk_fp8_f32 v72, v75, v76 op_sel:[0,0,1]
	v_mul_f32_e32 v76, 0xc01d265f, v74
	v_exp_f32_e32 v76, v76
	v_add_f32_e32 v77, v118, v122
	s_waitcnt vmcnt(14)
	v_add_f32_e32 v75, v112, v124
	v_min_f32_e32 v77, 0x40e00000, v77
	v_add_f32_e32 v76, 1.0, v76
	v_med3_f32 v75, v75, s46, v150
	v_rcp_f32_e32 v76, v76
	v_mul_f32_e32 v78, 0xc01d265f, v77
	v_fma_f32 v75, v75, 4.0, 4.0
	v_exp_f32_e32 v78, v78
	v_mul_f32_e32 v75, v75, v73
	v_add_f32_e32 v73, v113, v125
	v_med3_f32 v73, v73, s46, v150
	v_fma_f32 v73, v73, 4.0, 4.0
	v_mul_f32_e32 v74, v74, v76
	v_mul_f32_e32 v74, v73, v74
	v_add_f32_e32 v73, 1.0, v78
	v_rcp_f32_e32 v73, v73
	v_add_f32_e32 v76, v114, v126
	v_med3_f32 v76, v76, s46, v150
	v_fma_f32 v76, v76, 4.0, 4.0
	v_mul_f32_e32 v73, v77, v73
	v_add_f32_e32 v77, v119, v123
	v_min_f32_e32 v77, 0x40e00000, v77
	v_mul_f32_e32 v78, 0xc01d265f, v77
	v_exp_f32_e32 v78, v78
	v_mul_f32_e32 v76, v76, v73
	v_add_f32_e32 v73, v115, v127
	v_med3_f32 v79, v73, s46, v150
	v_add_f32_e32 v73, 1.0, v78
	v_rcp_f32_e32 v78, v73
	v_mov_b32_e32 v73, v253
	v_cvt_pk_fp8_f32 v73, v75, v74
	v_fma_f32 v74, v79, 4.0, 4.0
	v_mul_f32_e32 v75, v77, v78
	v_mul_f32_e32 v74, v74, v75
	v_cvt_pk_fp8_f32 v73, v76, v74 op_sel:[0,0,1]
	v_lshlrev_b64 v[74:75], 11, v[252:253]
	v_lshl_add_u64 v[74:75], s[70:71], 0, v[74:75]
	v_lshl_add_u64 v[74:75], v[74:75], 0, v[146:147]
	global_store_dwordx2 v[74:75], v[72:73], off
.LBB0_1422:
	s_or_b64 exec, exec, s[2:3]
	v_cmp_gt_i32_e32 vcc, s55, v163
	s_waitcnt vmcnt(24)
	s_nop 0
	v_cndmask_b32_e32 v252, -1, v164, vcc
	v_cmp_lt_i32_e32 vcc, -1, v252
	s_and_saveexec_b64 s[2:3], vcc
	s_mov_b32 s97, s42
	v_readlane_b32 s96, v255, 8
	s_cbranch_execz .LBB0_1424
	s_waitcnt vmcnt(17)
	v_add_f32_e32 v72, v108, v128
	v_min_f32_e32 v72, 0x40e00000, v72
	v_mul_f32_e32 v73, 0xc01d265f, v72
	v_exp_f32_e32 v73, v73
	v_add_f32_e32 v75, v109, v129
	v_min_f32_e32 v75, 0x40e00000, v75
	v_mul_f32_e32 v76, 0xc01d265f, v75
	v_add_f32_e32 v73, 1.0, v73
	v_rcp_f32_e32 v73, v73
	s_waitcnt vmcnt(15)
	v_add_f32_e32 v74, v104, v132
	v_med3_f32 v74, v74, s46, v150
	v_fma_f32 v74, v74, 4.0, 4.0
	v_mul_f32_e32 v72, v72, v73
	v_exp_f32_e32 v73, v76
	v_add_f32_e32 v76, v110, v130
	v_min_f32_e32 v76, 0x40e00000, v76
	v_mul_f32_e32 v77, 0xc01d265f, v76
	v_add_f32_e32 v73, 1.0, v73
	v_rcp_f32_e32 v73, v73
	v_exp_f32_e32 v77, v77
	v_mul_f32_e32 v74, v74, v72
	v_add_f32_e32 v72, v105, v133
	v_med3_f32 v72, v72, s46, v150
	v_fma_f32 v72, v72, 4.0, 4.0
	v_mul_f32_e32 v73, v75, v73
	v_mul_f32_e32 v73, v72, v73
	v_add_f32_e32 v72, 1.0, v77
	v_rcp_f32_e32 v72, v72
	v_add_f32_e32 v75, v106, v134
	v_med3_f32 v75, v75, s46, v150
	v_fma_f32 v75, v75, 4.0, 4.0
	v_mul_f32_e32 v72, v76, v72
	v_mul_f32_e32 v75, v75, v72
	v_add_f32_e32 v72, v107, v135
	v_med3_f32 v72, v72, s46, v150
	v_fma_f32 v78, v72, 4.0, 4.0
	v_mov_b32_e32 v72, v253
	v_add_f32_e32 v76, v111, v131
	v_cvt_pk_fp8_f32 v72, v74, v73
	v_add_f32_e32 v73, v100, v120
	v_min_f32_e32 v76, 0x40e00000, v76
	v_min_f32_e32 v73, 0x40e00000, v73
	v_mul_f32_e32 v77, 0xc01d265f, v76
	v_mul_f32_e32 v74, 0xc01d265f, v73
	v_exp_f32_e32 v77, v77
	v_exp_f32_e32 v74, v74
	v_add_f32_e32 v77, 1.0, v77
	v_add_f32_e32 v74, 1.0, v74
	v_rcp_f32_e32 v77, v77
	v_rcp_f32_e32 v74, v74
	v_mul_f32_e32 v76, v76, v77
	v_mul_f32_e32 v73, v73, v74
	v_add_f32_e32 v74, v101, v121
	v_mul_f32_e32 v76, v78, v76
	v_min_f32_e32 v74, 0x40e00000, v74
	v_cvt_pk_fp8_f32 v72, v75, v76 op_sel:[0,0,1]
	v_mul_f32_e32 v76, 0xc01d265f, v74
	v_exp_f32_e32 v76, v76
	v_add_f32_e32 v77, v102, v122
	s_waitcnt vmcnt(14)
	v_add_f32_e32 v75, v96, v124
	v_min_f32_e32 v77, 0x40e00000, v77
	v_add_f32_e32 v76, 1.0, v76
	v_med3_f32 v75, v75, s46, v150
	v_rcp_f32_e32 v76, v76
	v_mul_f32_e32 v78, 0xc01d265f, v77
	v_fma_f32 v75, v75, 4.0, 4.0
	v_exp_f32_e32 v78, v78
	v_mul_f32_e32 v75, v75, v73
	v_add_f32_e32 v73, v97, v125
	v_med3_f32 v73, v73, s46, v150
	v_fma_f32 v73, v73, 4.0, 4.0
	v_mul_f32_e32 v74, v74, v76
	v_mul_f32_e32 v74, v73, v74
	v_add_f32_e32 v73, 1.0, v78
	v_rcp_f32_e32 v73, v73
	v_add_f32_e32 v76, v98, v126
	v_med3_f32 v76, v76, s46, v150
	v_fma_f32 v76, v76, 4.0, 4.0
	v_mul_f32_e32 v73, v77, v73
	v_add_f32_e32 v77, v103, v123
	v_min_f32_e32 v77, 0x40e00000, v77
	v_mul_f32_e32 v78, 0xc01d265f, v77
	v_exp_f32_e32 v78, v78
	v_mul_f32_e32 v76, v76, v73
	v_add_f32_e32 v73, v99, v127
	v_med3_f32 v79, v73, s46, v150
	v_add_f32_e32 v73, 1.0, v78
	v_rcp_f32_e32 v78, v73
	v_mov_b32_e32 v73, v253
	v_cvt_pk_fp8_f32 v73, v75, v74
	v_fma_f32 v74, v79, 4.0, 4.0
	v_mul_f32_e32 v75, v77, v78
	v_mul_f32_e32 v74, v74, v75
	v_cvt_pk_fp8_f32 v73, v76, v74 op_sel:[0,0,1]
	v_lshlrev_b64 v[74:75], 11, v[252:253]
	v_lshl_add_u64 v[74:75], s[70:71], 0, v[74:75]
	v_lshl_add_u64 v[74:75], v[74:75], 0, v[146:147]
	global_store_dwordx2 v[74:75], v[72:73], off
;   DI int glu4(const ColCtx& c, const f32x4& v0, const f32x4& v1) const {
;     float o[4];
; #pragma unroll
;     for (int i = 0; i < 4; ++i) {
;       const float g = fminf(v0[i] + c.bg[i], 7.f);
;       const float up = __builtin_amdgcn_fmed3f(v1[i] + c.bu[i], -7.f, 7.f);
;       const float sg = __builtin_amdgcn_rcpf(1.f + __builtin_amdgcn_exp2f(g * (-1.702f * 1.44269504088896f)));
;       o[i] = fmaf(up, 4.f, 4.f) * (g * sg);
;     }
;     return pack4_fp8(o[0], o[1], o[2], o[3]);
;   }
;   DI void epi_pair(RowTok a, const ColCtx& c0, const ColCtx& c1, const f32x4& g0, const f32x4& u0, const f32x4& g1, const f32x4& u1) const {
;     if (a < 0) return;
;     u32x2 pk; pk.x = (unsigned)glu4(c0, g0, u0); pk.y = (unsigned)glu4(c1, g1, u1);
;     *(u32x2*)(p.actq + (size_t)a * 2048 + c0.j0) = pk;
;   }
.LBB0_1424:
	s_or_b64 exec, exec, s[2:3]
	v_cmp_gt_i32_e32 vcc, s55, v161
	s_waitcnt vmcnt(23)
	s_nop 0
	v_cndmask_b32_e32 v252, -1, v162, vcc
	v_cmp_lt_i32_e32 vcc, -1, v252
	s_and_saveexec_b64 s[2:3], vcc
	s_cbranch_execz .LBB0_1426
	s_waitcnt vmcnt(17)
	v_add_f32_e32 v72, v92, v128
	v_min_f32_e32 v72, 0x40e00000, v72
	v_mul_f32_e32 v73, 0xc01d265f, v72
	v_exp_f32_e32 v73, v73
	v_add_f32_e32 v75, v93, v129
	v_min_f32_e32 v75, 0x40e00000, v75
	v_mul_f32_e32 v76, 0xc01d265f, v75
	v_add_f32_e32 v73, 1.0, v73
	v_rcp_f32_e32 v73, v73
	s_waitcnt vmcnt(15)
	v_add_f32_e32 v74, v88, v132
	v_med3_f32 v74, v74, s46, v150
	v_fma_f32 v74, v74, 4.0, 4.0
	v_mul_f32_e32 v72, v72, v73
	v_exp_f32_e32 v73, v76
	v_add_f32_e32 v76, v94, v130
	v_min_f32_e32 v76, 0x40e00000, v76
	v_mul_f32_e32 v77, 0xc01d265f, v76
	v_add_f32_e32 v73, 1.0, v73
	v_rcp_f32_e32 v73, v73
	v_exp_f32_e32 v77, v77
	v_mul_f32_e32 v74, v74, v72
	v_add_f32_e32 v72, v89, v133
	v_med3_f32 v72, v72, s46, v150
	v_fma_f32 v72, v72, 4.0, 4.0
	v_mul_f32_e32 v73, v75, v73
	v_mul_f32_e32 v73, v72, v73
	v_add_f32_e32 v72, 1.0, v77
	v_rcp_f32_e32 v72, v72
	v_add_f32_e32 v75, v90, v134
	v_med3_f32 v75, v75, s46, v150
	v_fma_f32 v75, v75, 4.0, 4.0
	v_mul_f32_e32 v72, v76, v72
	v_mul_f32_e32 v75, v75, v72
	v_add_f32_e32 v72, v91, v135
	v_med3_f32 v72, v72, s46, v150
	v_fma_f32 v78, v72, 4.0, 4.0
	v_mov_b32_e32 v72, v253
	v_add_f32_e32 v76, v95, v131
	v_cvt_pk_fp8_f32 v72, v74, v73
	v_add_f32_e32 v73, v84, v120
	v_min_f32_e32 v76, 0x40e00000, v76
	v_min_f32_e32 v73, 0x40e00000, v73
	v_mul_f32_e32 v77, 0xc01d265f, v76
	v_mul_f32_e32 v74, 0xc01d265f, v73
	v_exp_f32_e32 v77, v77
	v_exp_f32_e32 v74, v74
	s_waitcnt vmcnt(14)
	v_add_f32_e32 v8, v8, v124
	v_med3_f32 v8, v8, s46, v150
	v_add_f32_e32 v77, 1.0, v77
	v_add_f32_e32 v74, 1.0, v74
	v_rcp_f32_e32 v77, v77
	v_rcp_f32_e32 v74, v74
	v_fma_f32 v8, v8, 4.0, 4.0
	v_add_f32_e32 v9, v9, v125
	v_mul_f32_e32 v76, v76, v77
	v_mul_f32_e32 v73, v73, v74
	v_add_f32_e32 v74, v85, v121
	v_mul_f32_e32 v76, v78, v76
	v_min_f32_e32 v74, 0x40e00000, v74
	v_cvt_pk_fp8_f32 v72, v75, v76 op_sel:[0,0,1]
	v_mul_f32_e32 v75, 0xc01d265f, v74
	v_exp_f32_e32 v75, v75
	v_mul_f32_e32 v8, v8, v73
	v_med3_f32 v9, v9, s46, v150
	v_fma_f32 v9, v9, 4.0, 4.0
	v_add_f32_e32 v73, 1.0, v75
	v_add_f32_e32 v75, v86, v122
	v_min_f32_e32 v75, 0x40e00000, v75
	v_rcp_f32_e32 v73, v73
	v_mul_f32_e32 v76, 0xc01d265f, v75
	v_exp_f32_e32 v76, v76
	v_add_f32_e32 v10, v10, v126
	v_mul_f32_e32 v73, v74, v73
	v_mul_f32_e32 v9, v9, v73
	v_add_f32_e32 v73, 1.0, v76
	v_rcp_f32_e32 v73, v73
	v_add_f32_e32 v74, v87, v123
	v_min_f32_e32 v74, 0x40e00000, v74
	v_med3_f32 v10, v10, s46, v150
	v_mul_f32_e32 v73, v75, v73
	v_mul_f32_e32 v75, 0xc01d265f, v74
	v_exp_f32_e32 v75, v75
	v_fma_f32 v10, v10, 4.0, 4.0
	v_mul_f32_e32 v10, v10, v73
	v_add_f32_e32 v11, v11, v127
	v_add_f32_e32 v73, 1.0, v75
	v_rcp_f32_e32 v75, v73
	v_mov_b32_e32 v73, v253
	v_cvt_pk_fp8_f32 v73, v8, v9
	v_med3_f32 v11, v11, s46, v150
	v_fma_f32 v8, v11, 4.0, 4.0
	v_mul_f32_e32 v9, v74, v75
	v_mul_f32_e32 v8, v8, v9
	v_cvt_pk_fp8_f32 v73, v10, v8 op_sel:[0,0,1]
	v_lshlrev_b64 v[8:9], 11, v[252:253]
	v_lshl_add_u64 v[8:9], s[70:71], 0, v[8:9]
	v_lshl_add_u64 v[8:9], v[8:9], 0, v[146:147]
	global_store_dwordx2 v[8:9], v[72:73], off
.LBB0_1426:
	s_or_b64 exec, exec, s[2:3]
	v_cmp_gt_i32_e32 vcc, s55, v159
	s_waitcnt vmcnt(22)
	s_nop 0
	v_cndmask_b32_e32 v252, -1, v160, vcc
	v_cmp_lt_i32_e32 vcc, -1, v252
	s_and_saveexec_b64 s[2:3], vcc
	s_cbranch_execz .LBB0_1428
	s_waitcnt vmcnt(17)
	v_add_f32_e32 v8, v212, v128
	v_min_f32_e32 v8, 0x40e00000, v8
	v_mul_f32_e32 v9, 0xc01d265f, v8
	v_exp_f32_e32 v9, v9
	v_add_f32_e32 v11, v213, v129
	v_min_f32_e32 v11, 0x40e00000, v11
	v_mul_f32_e32 v72, 0xc01d265f, v11
	v_add_f32_e32 v9, 1.0, v9
	v_rcp_f32_e32 v9, v9
	s_waitcnt vmcnt(15)
	v_add_f32_e32 v10, v216, v132
	v_med3_f32 v10, v10, s46, v150
	v_fma_f32 v10, v10, 4.0, 4.0
	v_mul_f32_e32 v8, v8, v9
	v_exp_f32_e32 v9, v72
	v_add_f32_e32 v72, v214, v130
	v_min_f32_e32 v72, 0x40e00000, v72
	v_mul_f32_e32 v73, 0xc01d265f, v72
	v_add_f32_e32 v9, 1.0, v9
	v_rcp_f32_e32 v9, v9
	v_exp_f32_e32 v73, v73
	v_mul_f32_e32 v10, v10, v8
	v_add_f32_e32 v8, v217, v133
	v_med3_f32 v8, v8, s46, v150
	v_fma_f32 v8, v8, 4.0, 4.0
	v_mul_f32_e32 v9, v11, v9
	v_mul_f32_e32 v9, v8, v9
	v_add_f32_e32 v8, 1.0, v73
	v_rcp_f32_e32 v8, v8
	v_add_f32_e32 v11, v218, v134
	v_med3_f32 v11, v11, s46, v150
	v_fma_f32 v11, v11, 4.0, 4.0
	v_mul_f32_e32 v8, v72, v8
	v_mul_f32_e32 v11, v11, v8
	v_add_f32_e32 v8, v219, v135
	v_med3_f32 v8, v8, s46, v150
	v_fma_f32 v74, v8, 4.0, 4.0
	v_mov_b32_e32 v8, v253
	v_add_f32_e32 v72, v215, v131
	v_cvt_pk_fp8_f32 v8, v10, v9
	v_add_f32_e32 v9, v68, v120
	v_min_f32_e32 v72, 0x40e00000, v72
	v_min_f32_e32 v9, 0x40e00000, v9
	v_mul_f32_e32 v73, 0xc01d265f, v72
	v_mul_f32_e32 v10, 0xc01d265f, v9
	v_exp_f32_e32 v73, v73
	v_exp_f32_e32 v10, v10
	v_add_f32_e32 v73, 1.0, v73
	v_add_f32_e32 v10, 1.0, v10
	v_rcp_f32_e32 v73, v73
	v_rcp_f32_e32 v10, v10
	v_mul_f32_e32 v68, v72, v73
	v_mul_f32_e32 v9, v9, v10
	v_add_f32_e32 v10, v69, v121
	v_mul_f32_e32 v68, v74, v68
	v_min_f32_e32 v10, 0x40e00000, v10
	v_cvt_pk_fp8_f32 v8, v11, v68 op_sel:[0,0,1]
	s_waitcnt vmcnt(14)
	v_add_f32_e32 v11, v56, v124
	v_mul_f32_e32 v56, 0xc01d265f, v10
	v_exp_f32_e32 v56, v56
	v_med3_f32 v11, v11, s46, v150
	v_fma_f32 v11, v11, 4.0, 4.0
	v_mul_f32_e32 v11, v11, v9
	v_add_f32_e32 v9, v57, v125
	v_add_f32_e32 v57, v70, v122
	v_add_f32_e32 v56, 1.0, v56
	v_min_f32_e32 v57, 0x40e00000, v57
	v_rcp_f32_e32 v56, v56
	v_mul_f32_e32 v68, 0xc01d265f, v57
	v_exp_f32_e32 v68, v68
	v_med3_f32 v9, v9, s46, v150
	v_fma_f32 v9, v9, 4.0, 4.0
	v_mul_f32_e32 v10, v10, v56
	v_mul_f32_e32 v10, v9, v10
	v_add_f32_e32 v9, 1.0, v68
	v_rcp_f32_e32 v9, v9
	v_add_f32_e32 v56, v58, v126
	v_med3_f32 v56, v56, s46, v150
	v_fma_f32 v56, v56, 4.0, 4.0
	v_mul_f32_e32 v9, v57, v9
	v_add_f32_e32 v57, v71, v123
	v_min_f32_e32 v57, 0x40e00000, v57
	v_mul_f32_e32 v58, 0xc01d265f, v57
	v_exp_f32_e32 v58, v58
	v_mul_f32_e32 v56, v56, v9
	v_add_f32_e32 v9, v59, v127
	v_med3_f32 v59, v9, s46, v150
	v_add_f32_e32 v9, 1.0, v58
	v_rcp_f32_e32 v58, v9
	v_mov_b32_e32 v9, v253
	v_cvt_pk_fp8_f32 v9, v11, v10
	v_fma_f32 v10, v59, 4.0, 4.0
	v_mul_f32_e32 v11, v57, v58
	v_mul_f32_e32 v10, v10, v11
	v_cvt_pk_fp8_f32 v9, v56, v10 op_sel:[0,0,1]
	v_lshlrev_b64 v[10:11], 11, v[252:253]
	v_lshl_add_u64 v[10:11], s[70:71], 0, v[10:11]
	v_lshl_add_u64 v[10:11], v[10:11], 0, v[146:147]
	global_store_dwordx2 v[10:11], v[8:9], off
;   DI int glu4(const ColCtx& c, const f32x4& v0, const f32x4& v1) const {
;     float o[4];
; #pragma unroll
;     for (int i = 0; i < 4; ++i) {
;       const float g = fminf(v0[i] + c.bg[i], 7.f);
;       const float up = __builtin_amdgcn_fmed3f(v1[i] + c.bu[i], -7.f, 7.f);
;       const float sg = __builtin_amdgcn_rcpf(1.f + __builtin_amdgcn_exp2f(g * (-1.702f * 1.44269504088896f)));
;       o[i] = fmaf(up, 4.f, 4.f) * (g * sg);
;     }
;     return pack4_fp8(o[0], o[1], o[2], o[3]);
;   }
;   DI void epi_pair(RowTok a, const ColCtx& c0, const ColCtx& c1, const f32x4& g0, const f32x4& u0, const f32x4& g1, const f32x4& u1) const {
;     if (a < 0) return;
;     u32x2 pk; pk.x = (unsigned)glu4(c0, g0, u0); pk.y = (unsigned)glu4(c1, g1, u1);
;     *(u32x2*)(p.actq + (size_t)a * 2048 + c0.j0) = pk;
;   }
.LBB0_1428:
	s_or_b64 exec, exec, s[2:3]
	v_cmp_gt_i32_e32 vcc, s55, v157
	s_waitcnt vmcnt(21)
	s_nop 0
	v_cndmask_b32_e32 v252, -1, v158, vcc
	v_cmp_lt_i32_e32 vcc, -1, v252
	s_and_saveexec_b64 s[2:3], vcc
	s_cbranch_execz .LBB0_1430
	s_waitcnt vmcnt(17)
	v_add_f32_e32 v8, v64, v128
	v_min_f32_e32 v8, 0x40e00000, v8
	v_mul_f32_e32 v9, 0xc01d265f, v8
	v_exp_f32_e32 v9, v9
	v_add_f32_e32 v11, v65, v129
	v_min_f32_e32 v11, 0x40e00000, v11
	v_mul_f32_e32 v56, 0xc01d265f, v11
	v_add_f32_e32 v9, 1.0, v9
	v_rcp_f32_e32 v9, v9
	s_waitcnt vmcnt(15)
	v_add_f32_e32 v10, v60, v132
	v_med3_f32 v10, v10, s46, v150
	v_fma_f32 v10, v10, 4.0, 4.0
	v_mul_f32_e32 v8, v8, v9
	v_exp_f32_e32 v9, v56
	v_add_f32_e32 v56, v66, v130
	v_min_f32_e32 v56, 0x40e00000, v56
	v_mul_f32_e32 v57, 0xc01d265f, v56
	v_add_f32_e32 v9, 1.0, v9
	v_rcp_f32_e32 v9, v9
	v_exp_f32_e32 v57, v57
	v_mul_f32_e32 v10, v10, v8
	v_add_f32_e32 v8, v61, v133
	v_med3_f32 v8, v8, s46, v150
	v_fma_f32 v8, v8, 4.0, 4.0
	v_mul_f32_e32 v9, v11, v9
	v_mul_f32_e32 v9, v8, v9
	v_add_f32_e32 v8, 1.0, v57
	v_rcp_f32_e32 v8, v8
	v_add_f32_e32 v11, v62, v134
	v_med3_f32 v11, v11, s46, v150
	v_fma_f32 v11, v11, 4.0, 4.0
	v_mul_f32_e32 v8, v56, v8
	v_mul_f32_e32 v11, v11, v8
	v_add_f32_e32 v8, v63, v135
	v_med3_f32 v8, v8, s46, v150
	v_fma_f32 v58, v8, 4.0, 4.0
	v_mov_b32_e32 v8, v253
	v_add_f32_e32 v56, v67, v131
	v_cvt_pk_fp8_f32 v8, v10, v9
	v_add_f32_e32 v9, v52, v120
	v_min_f32_e32 v56, 0x40e00000, v56
	v_min_f32_e32 v9, 0x40e00000, v9
	v_mul_f32_e32 v57, 0xc01d265f, v56
	v_mul_f32_e32 v10, 0xc01d265f, v9
	v_exp_f32_e32 v57, v57
	v_exp_f32_e32 v10, v10
	v_add_f32_e32 v57, 1.0, v57
	v_add_f32_e32 v10, 1.0, v10
	v_rcp_f32_e32 v57, v57
	v_rcp_f32_e32 v10, v10
	v_mul_f32_e32 v52, v56, v57
	v_mul_f32_e32 v9, v9, v10
	v_add_f32_e32 v10, v53, v121
	v_mul_f32_e32 v52, v58, v52
	v_min_f32_e32 v10, 0x40e00000, v10
	v_cvt_pk_fp8_f32 v8, v11, v52 op_sel:[0,0,1]
	s_waitcnt vmcnt(14)
	v_add_f32_e32 v11, v48, v124
	v_mul_f32_e32 v48, 0xc01d265f, v10
	v_exp_f32_e32 v48, v48
	v_med3_f32 v11, v11, s46, v150
	v_fma_f32 v11, v11, 4.0, 4.0
	v_mul_f32_e32 v11, v11, v9
	v_add_f32_e32 v9, v49, v125
	v_add_f32_e32 v49, v54, v122
	v_add_f32_e32 v48, 1.0, v48
	v_min_f32_e32 v49, 0x40e00000, v49
	v_rcp_f32_e32 v48, v48
	v_mul_f32_e32 v52, 0xc01d265f, v49
	v_exp_f32_e32 v52, v52
	v_med3_f32 v9, v9, s46, v150
	v_fma_f32 v9, v9, 4.0, 4.0
	v_mul_f32_e32 v10, v10, v48
	v_mul_f32_e32 v10, v9, v10
	v_add_f32_e32 v9, 1.0, v52
	v_rcp_f32_e32 v9, v9
	v_add_f32_e32 v48, v50, v126
	v_med3_f32 v48, v48, s46, v150
	v_fma_f32 v48, v48, 4.0, 4.0
	v_mul_f32_e32 v9, v49, v9
	v_add_f32_e32 v49, v55, v123
	v_min_f32_e32 v49, 0x40e00000, v49
	v_mul_f32_e32 v50, 0xc01d265f, v49
	v_exp_f32_e32 v50, v50
	v_mul_f32_e32 v48, v48, v9
	v_add_f32_e32 v9, v51, v127
	v_med3_f32 v51, v9, s46, v150
	v_add_f32_e32 v9, 1.0, v50
	v_rcp_f32_e32 v50, v9
	v_mov_b32_e32 v9, v253
	v_cvt_pk_fp8_f32 v9, v11, v10
	v_fma_f32 v10, v51, 4.0, 4.0
	v_mul_f32_e32 v11, v49, v50
	v_mul_f32_e32 v10, v10, v11
	v_cvt_pk_fp8_f32 v9, v48, v10 op_sel:[0,0,1]
	v_lshlrev_b64 v[10:11], 11, v[252:253]
	v_lshl_add_u64 v[10:11], s[70:71], 0, v[10:11]
	v_lshl_add_u64 v[10:11], v[10:11], 0, v[146:147]
	global_store_dwordx2 v[10:11], v[8:9], off
.LBB0_1430:
	s_or_b64 exec, exec, s[2:3]
	v_cmp_gt_i32_e32 vcc, s55, v155
	s_waitcnt vmcnt(20)
	s_nop 0
	v_cndmask_b32_e32 v252, -1, v156, vcc
	v_cmp_lt_i32_e32 vcc, -1, v252
	s_and_saveexec_b64 s[2:3], vcc
	s_cbranch_execz .LBB0_1432
	s_waitcnt vmcnt(17)
	v_add_f32_e32 v8, v44, v128
	v_min_f32_e32 v8, 0x40e00000, v8
	v_mul_f32_e32 v9, 0xc01d265f, v8
	v_exp_f32_e32 v9, v9
	v_add_f32_e32 v11, v45, v129
	v_min_f32_e32 v11, 0x40e00000, v11
	s_waitcnt vmcnt(15)
	v_add_f32_e32 v10, v40, v132
	v_add_f32_e32 v9, 1.0, v9
	v_rcp_f32_e32 v9, v9
	v_mul_f32_e32 v40, 0xc01d265f, v11
	v_med3_f32 v10, v10, s46, v150
	v_fma_f32 v10, v10, 4.0, 4.0
	v_mul_f32_e32 v8, v8, v9
	v_exp_f32_e32 v9, v40
	v_add_f32_e32 v40, v46, v130
	v_min_f32_e32 v40, 0x40e00000, v40
	v_mul_f32_e32 v10, v10, v8
	v_add_f32_e32 v9, 1.0, v9
	v_add_f32_e32 v8, v41, v133
	v_rcp_f32_e32 v9, v9
	v_mul_f32_e32 v41, 0xc01d265f, v40
	v_exp_f32_e32 v41, v41
	v_med3_f32 v8, v8, s46, v150
	v_fma_f32 v8, v8, 4.0, 4.0
	v_mul_f32_e32 v9, v11, v9
	v_mul_f32_e32 v9, v8, v9
	v_add_f32_e32 v8, 1.0, v41
	v_rcp_f32_e32 v8, v8
	v_add_f32_e32 v11, v42, v134
	v_med3_f32 v11, v11, s46, v150
	v_fma_f32 v11, v11, 4.0, 4.0
	v_mul_f32_e32 v8, v40, v8
	v_mul_f32_e32 v11, v11, v8
	v_add_f32_e32 v8, v43, v135
	v_med3_f32 v8, v8, s46, v150
	v_fma_f32 v42, v8, 4.0, 4.0
	v_mov_b32_e32 v8, v253
	v_add_f32_e32 v40, v47, v131
	v_cvt_pk_fp8_f32 v8, v10, v9
	v_add_f32_e32 v9, v36, v120
	v_min_f32_e32 v40, 0x40e00000, v40
	v_min_f32_e32 v9, 0x40e00000, v9
	v_mul_f32_e32 v41, 0xc01d265f, v40
	v_mul_f32_e32 v10, 0xc01d265f, v9
	v_exp_f32_e32 v41, v41
	v_exp_f32_e32 v10, v10
	v_add_f32_e32 v41, 1.0, v41
	v_add_f32_e32 v10, 1.0, v10
	v_rcp_f32_e32 v41, v41
	v_rcp_f32_e32 v10, v10
	v_mul_f32_e32 v36, v40, v41
	v_mul_f32_e32 v9, v9, v10
	v_add_f32_e32 v10, v37, v121
	v_mul_f32_e32 v36, v42, v36
	v_min_f32_e32 v10, 0x40e00000, v10
	v_cvt_pk_fp8_f32 v8, v11, v36 op_sel:[0,0,1]
	s_waitcnt vmcnt(14)
	v_add_f32_e32 v11, v32, v124
	v_mul_f32_e32 v32, 0xc01d265f, v10
	v_exp_f32_e32 v32, v32
	v_med3_f32 v11, v11, s46, v150
	v_fma_f32 v11, v11, 4.0, 4.0
	v_mul_f32_e32 v11, v11, v9
	v_add_f32_e32 v9, v33, v125
	v_add_f32_e32 v33, v38, v122
	v_add_f32_e32 v32, 1.0, v32
	v_min_f32_e32 v33, 0x40e00000, v33
	v_rcp_f32_e32 v32, v32
	v_mul_f32_e32 v36, 0xc01d265f, v33
	v_exp_f32_e32 v36, v36
	v_med3_f32 v9, v9, s46, v150
	v_fma_f32 v9, v9, 4.0, 4.0
	v_mul_f32_e32 v10, v10, v32
	v_mul_f32_e32 v10, v9, v10
	v_add_f32_e32 v9, 1.0, v36
	v_rcp_f32_e32 v9, v9
	v_add_f32_e32 v32, v34, v126
	v_med3_f32 v32, v32, s46, v150
	v_fma_f32 v32, v32, 4.0, 4.0
	v_mul_f32_e32 v9, v33, v9
	v_add_f32_e32 v33, v39, v123
	v_min_f32_e32 v33, 0x40e00000, v33
	v_mul_f32_e32 v34, 0xc01d265f, v33
	v_exp_f32_e32 v34, v34
	v_mul_f32_e32 v32, v32, v9
	v_add_f32_e32 v9, v35, v127
	v_med3_f32 v35, v9, s46, v150
	v_add_f32_e32 v9, 1.0, v34
	v_rcp_f32_e32 v34, v9
	v_mov_b32_e32 v9, v253
	v_cvt_pk_fp8_f32 v9, v11, v10
	v_fma_f32 v10, v35, 4.0, 4.0
	v_mul_f32_e32 v11, v33, v34
	v_mul_f32_e32 v10, v10, v11
	v_cvt_pk_fp8_f32 v9, v32, v10 op_sel:[0,0,1]
	v_lshlrev_b64 v[10:11], 11, v[252:253]
	v_lshl_add_u64 v[10:11], s[70:71], 0, v[10:11]
	v_lshl_add_u64 v[10:11], v[10:11], 0, v[146:147]
	global_store_dwordx2 v[10:11], v[8:9], off
;   DI int glu4(const ColCtx& c, const f32x4& v0, const f32x4& v1) const {
;     float o[4];
; #pragma unroll
;     for (int i = 0; i < 4; ++i) {
;       const float g = fminf(v0[i] + c.bg[i], 7.f);
;       const float up = __builtin_amdgcn_fmed3f(v1[i] + c.bu[i], -7.f, 7.f);
;       const float sg = __builtin_amdgcn_rcpf(1.f + __builtin_amdgcn_exp2f(g * (-1.702f * 1.44269504088896f)));
;       o[i] = fmaf(up, 4.f, 4.f) * (g * sg);
;     }
;     return pack4_fp8(o[0], o[1], o[2], o[3]);
;   }
;   DI void epi_pair(RowTok a, const ColCtx& c0, const ColCtx& c1, const f32x4& g0, const f32x4& u0, const f32x4& g1, const f32x4& u1) const {
;     if (a < 0) return;
;     u32x2 pk; pk.x = (unsigned)glu4(c0, g0, u0); pk.y = (unsigned)glu4(c1, g1, u1);
;     *(u32x2*)(p.actq + (size_t)a * 2048 + c0.j0) = pk;
;   }
.LBB0_1432:
	s_or_b64 exec, exec, s[2:3]
	v_cmp_gt_i32_e32 vcc, s55, v153
	s_waitcnt vmcnt(19)
	s_nop 0
	v_cndmask_b32_e32 v252, -1, v154, vcc
	v_cmp_lt_i32_e32 vcc, -1, v252
	s_and_saveexec_b64 s[2:3], vcc
	s_cbranch_execz .LBB0_1434
	s_waitcnt vmcnt(17)
	v_add_f32_e32 v8, v28, v128
	v_min_f32_e32 v8, 0x40e00000, v8
	v_mul_f32_e32 v9, 0xc01d265f, v8
	v_exp_f32_e32 v9, v9
	v_add_f32_e32 v11, v29, v129
	v_min_f32_e32 v11, 0x40e00000, v11
	s_waitcnt vmcnt(15)
	v_add_f32_e32 v10, v24, v132
	v_add_f32_e32 v9, 1.0, v9
	v_rcp_f32_e32 v9, v9
	v_mul_f32_e32 v24, 0xc01d265f, v11
	v_med3_f32 v10, v10, s46, v150
	v_fma_f32 v10, v10, 4.0, 4.0
	v_mul_f32_e32 v8, v8, v9
	v_exp_f32_e32 v9, v24
	v_add_f32_e32 v24, v30, v130
	v_min_f32_e32 v24, 0x40e00000, v24
	v_mul_f32_e32 v10, v10, v8
	v_add_f32_e32 v9, 1.0, v9
	v_add_f32_e32 v8, v25, v133
	v_rcp_f32_e32 v9, v9
	v_mul_f32_e32 v25, 0xc01d265f, v24
	v_exp_f32_e32 v25, v25
	v_med3_f32 v8, v8, s46, v150
	v_fma_f32 v8, v8, 4.0, 4.0
	v_mul_f32_e32 v9, v11, v9
	v_mul_f32_e32 v9, v8, v9
	v_add_f32_e32 v8, 1.0, v25
	v_rcp_f32_e32 v8, v8
	v_add_f32_e32 v11, v26, v134
	v_med3_f32 v11, v11, s46, v150
	v_fma_f32 v11, v11, 4.0, 4.0
	v_mul_f32_e32 v8, v24, v8
	v_mul_f32_e32 v11, v11, v8
	v_add_f32_e32 v8, v27, v135
	v_med3_f32 v8, v8, s46, v150
	v_fma_f32 v26, v8, 4.0, 4.0
	v_mov_b32_e32 v8, v253
	v_add_f32_e32 v24, v31, v131
	v_cvt_pk_fp8_f32 v8, v10, v9
	v_add_f32_e32 v9, v20, v120
	v_min_f32_e32 v24, 0x40e00000, v24
	v_min_f32_e32 v9, 0x40e00000, v9
	v_mul_f32_e32 v25, 0xc01d265f, v24
	v_mul_f32_e32 v10, 0xc01d265f, v9
	v_exp_f32_e32 v25, v25
	v_exp_f32_e32 v10, v10
	v_add_f32_e32 v25, 1.0, v25
	v_add_f32_e32 v10, 1.0, v10
	v_rcp_f32_e32 v25, v25
	v_rcp_f32_e32 v10, v10
	v_mul_f32_e32 v20, v24, v25
	v_mul_f32_e32 v9, v9, v10
	v_add_f32_e32 v10, v21, v121
	v_mul_f32_e32 v20, v26, v20
	v_min_f32_e32 v10, 0x40e00000, v10
	v_cvt_pk_fp8_f32 v8, v11, v20 op_sel:[0,0,1]
	s_waitcnt vmcnt(14)
	v_add_f32_e32 v11, v16, v124
	v_mul_f32_e32 v16, 0xc01d265f, v10
	v_exp_f32_e32 v16, v16
	v_med3_f32 v11, v11, s46, v150
	v_fma_f32 v11, v11, 4.0, 4.0
	v_mul_f32_e32 v11, v11, v9
	v_add_f32_e32 v9, v17, v125
	v_add_f32_e32 v17, v22, v122
	v_add_f32_e32 v16, 1.0, v16
	v_min_f32_e32 v17, 0x40e00000, v17
	v_rcp_f32_e32 v16, v16
	v_mul_f32_e32 v20, 0xc01d265f, v17
	v_exp_f32_e32 v20, v20
	v_med3_f32 v9, v9, s46, v150
	v_fma_f32 v9, v9, 4.0, 4.0
	v_mul_f32_e32 v10, v10, v16
	v_mul_f32_e32 v10, v9, v10
	v_add_f32_e32 v9, 1.0, v20
	v_rcp_f32_e32 v9, v9
	v_add_f32_e32 v16, v18, v126
	v_med3_f32 v16, v16, s46, v150
	v_fma_f32 v16, v16, 4.0, 4.0
	v_mul_f32_e32 v9, v17, v9
	v_add_f32_e32 v17, v23, v123
	v_min_f32_e32 v17, 0x40e00000, v17
	v_mul_f32_e32 v18, 0xc01d265f, v17
	v_exp_f32_e32 v18, v18
	v_mul_f32_e32 v16, v16, v9
	v_add_f32_e32 v9, v19, v127
	v_med3_f32 v19, v9, s46, v150
	v_add_f32_e32 v9, 1.0, v18
	v_rcp_f32_e32 v18, v9
	v_mov_b32_e32 v9, v253
	v_cvt_pk_fp8_f32 v9, v11, v10
	v_fma_f32 v10, v19, 4.0, 4.0
	v_mul_f32_e32 v11, v17, v18
	v_mul_f32_e32 v10, v10, v11
	v_cvt_pk_fp8_f32 v9, v16, v10 op_sel:[0,0,1]
	v_lshlrev_b64 v[10:11], 11, v[252:253]
	v_lshl_add_u64 v[10:11], s[70:71], 0, v[10:11]
	v_lshl_add_u64 v[10:11], v[10:11], 0, v[146:147]
	global_store_dwordx2 v[10:11], v[8:9], off
.LBB0_1434:
	s_or_b64 exec, exec, s[2:3]
	v_cmp_gt_i32_e32 vcc, s55, v151
	s_waitcnt vmcnt(18)
	s_nop 0
	v_cndmask_b32_e32 v252, -1, v152, vcc
	v_cmp_lt_i32_e32 vcc, -1, v252
	s_and_saveexec_b64 s[2:3], vcc
	s_cbranch_execz .LBB0_1436
	s_waitcnt vmcnt(17)
	v_add_f32_e32 v8, v12, v128
	v_min_f32_e32 v8, 0x40e00000, v8
	v_mul_f32_e32 v9, 0xc01d265f, v8
	v_exp_f32_e32 v9, v9
	v_add_f32_e32 v11, v13, v129
	v_min_f32_e32 v11, 0x40e00000, v11
	v_mul_f32_e32 v12, 0xc01d265f, v11
	v_add_f32_e32 v9, 1.0, v9
	v_rcp_f32_e32 v9, v9
	s_waitcnt vmcnt(15)
	v_add_f32_e32 v10, v236, v132
	v_med3_f32 v10, v10, s46, v150
	v_fma_f32 v10, v10, 4.0, 4.0
	v_mul_f32_e32 v8, v8, v9
	v_exp_f32_e32 v9, v12
	v_add_f32_e32 v12, v14, v130
	v_min_f32_e32 v12, 0x40e00000, v12
	v_mul_f32_e32 v13, 0xc01d265f, v12
	v_add_f32_e32 v9, 1.0, v9
	v_rcp_f32_e32 v9, v9
	v_exp_f32_e32 v13, v13
	v_mul_f32_e32 v10, v10, v8
	v_add_f32_e32 v8, v237, v133
	v_med3_f32 v8, v8, s46, v150
	v_fma_f32 v8, v8, 4.0, 4.0
	v_mul_f32_e32 v9, v11, v9
	v_mul_f32_e32 v9, v8, v9
	v_add_f32_e32 v8, 1.0, v13
	v_rcp_f32_e32 v8, v8
	v_add_f32_e32 v11, v238, v134
	v_med3_f32 v11, v11, s46, v150
	v_fma_f32 v11, v11, 4.0, 4.0
	v_mul_f32_e32 v8, v12, v8
	v_mul_f32_e32 v11, v11, v8
	v_add_f32_e32 v8, v239, v135
	v_med3_f32 v8, v8, s46, v150
	v_add_f32_e32 v4, v4, v120
	v_fma_f32 v14, v8, 4.0, 4.0
	v_mov_b32_e32 v8, v253
	v_min_f32_e32 v4, 0x40e00000, v4
	v_cvt_pk_fp8_f32 v8, v10, v9
	v_mul_f32_e32 v9, 0xc01d265f, v4
	v_exp_f32_e32 v9, v9
	v_add_f32_e32 v5, v5, v121
	v_min_f32_e32 v5, 0x40e00000, v5
	s_waitcnt vmcnt(14)
	v_add_f32_e32 v0, v0, v124
	v_add_f32_e32 v9, 1.0, v9
	v_rcp_f32_e32 v9, v9
	v_med3_f32 v0, v0, s46, v150
	v_fma_f32 v0, v0, 4.0, 4.0
	v_add_f32_e32 v6, v6, v122
	v_mul_f32_e32 v4, v4, v9
	v_mul_f32_e32 v9, 0xc01d265f, v5
	v_exp_f32_e32 v9, v9
	v_mul_f32_e32 v0, v0, v4
	v_min_f32_e32 v6, 0x40e00000, v6
	v_add_f32_e32 v1, v1, v125
	v_add_f32_e32 v4, 1.0, v9
	v_rcp_f32_e32 v4, v4
	v_mul_f32_e32 v9, 0xc01d265f, v6
	v_exp_f32_e32 v9, v9
	v_med3_f32 v1, v1, s46, v150
	v_fma_f32 v1, v1, 4.0, 4.0
	v_mul_f32_e32 v4, v5, v4
	v_mul_f32_e32 v1, v1, v4
	v_add_f32_e32 v4, 1.0, v9
	v_rcp_f32_e32 v4, v4
	v_add_f32_e32 v12, v15, v131
	v_add_f32_e32 v5, v7, v123
	v_min_f32_e32 v12, 0x40e00000, v12
	v_min_f32_e32 v5, 0x40e00000, v5
	v_mul_f32_e32 v13, 0xc01d265f, v12
	v_mul_f32_e32 v4, v6, v4
	v_mul_f32_e32 v6, 0xc01d265f, v5
	v_exp_f32_e32 v13, v13
	v_exp_f32_e32 v6, v6
	v_add_f32_e32 v2, v2, v126
	v_med3_f32 v2, v2, s46, v150
	v_fma_f32 v2, v2, 4.0, 4.0
	v_add_f32_e32 v13, 1.0, v13
	v_mul_f32_e32 v2, v2, v4
	v_add_f32_e32 v4, 1.0, v6
	v_rcp_f32_e32 v13, v13
	v_rcp_f32_e32 v4, v4
	v_mov_b32_e32 v9, v253
	v_add_f32_e32 v3, v3, v127
	v_cvt_pk_fp8_f32 v9, v0, v1
	v_med3_f32 v3, v3, s46, v150
	v_mul_f32_e32 v10, v12, v13
	v_fma_f32 v0, v3, 4.0, 4.0
	v_mul_f32_e32 v1, v5, v4
	v_mul_f32_e32 v10, v14, v10
	v_mul_f32_e32 v0, v0, v1
	v_cvt_pk_fp8_f32 v8, v11, v10 op_sel:[0,0,1]
	v_cvt_pk_fp8_f32 v9, v2, v0 op_sel:[0,0,1]
	v_lshlrev_b64 v[0:1], 11, v[252:253]
	v_lshl_add_u64 v[0:1], s[70:71], 0, v[0:1]
	v_lshl_add_u64 v[0:1], v[0:1], 0, v[146:147]
	global_store_dwordx2 v[0:1], v[8:9], off

; #define LDS_AS __attribute__((address_space(3)))
; #define OPAQUE_TID(P) (((P).wid0 << 6) | lane_id_now())
; #define P_STAGE_A(slot, half, kt) do { _Pragma("unroll") for (int _i = 0; _i < 2; ++_i) { const unsigned _m0 = ldsw + (unsigned)((slot) + _i * 8192); const unsigned _so = (unsigned)(kt) * 128u; \
;     asm volatile("s_mov_b32 m0, %0\n\ts_nop 4\n\tbuffer_load_dwordx4 %1, %2, %3 offen lds" :: "s"(_m0), "v"(voffA[half][_i]), "s"(rsA), "s"(_so) : "m0", "memory"); } } while (0)
; #define P_STAGE_B(slot, half, kt) do { _Pragma("unroll") for (int _i = 0; _i < 2; ++_i) { const unsigned _m0 = ldsw + (unsigned)((slot) + _i * 8192); const unsigned _so = (unsigned)(kt) * 128u + (half) * bt_half + _i * bt_piece; \
;     asm volatile("s_mov_b32 m0, %0\n\ts_nop 4\n\tbuffer_load_dwordx4 %1, %2, %3 offen lds" :: "s"(_m0), "v"(voffB0), "s"(rsB), "s"(_so) : "m0", "memory"); } } while (0)
;   DI unsigned bt_rowoff(int h, int R) const { return (unsigned)(pn * 256 + 128 * h + (pn < 15 ? tcol_adj(R) : tcol_p64(R))) * 4096u; }
; template <class Cfg>
; DI void f8dma_issue_prologue_st(LDS_AS unsigned char* lds, const Cfg& cfg) {
;   const int tid = OPAQUE_TID(cfg.p), wid = __builtin_amdgcn_readfirstlane(tid >> 6), lane = tid & 63;
;   const LDS_AS unsigned* stash = (const LDS_AS unsigned*)(lds + F8_STASH);
;   unsigned voffA[2][2], voffB0;
;   voffA[0][0] = stash[tid]; voffA[0][1] = stash[512 + tid]; voffA[1][0] = stash[1024 + tid]; voffA[1][1] = stash[1536 + tid];
;   {
;     const int r = 8 * wid + (lane >> 3);
;     const unsigned cofs = 16u * (((unsigned)lane & 7u) ^ (((unsigned)lane >> 3) & 7u));
;     voffB0 = cfg.bt_rowoff(0, r) + cofs;
;   }
;   const unsigned bt_half = cfg.bt_rowoff(1, 0) - cfg.bt_rowoff(0, 0), bt_piece = cfg.bt_rowoff(0, 64) - cfg.bt_rowoff(0, 0);
;   const __amdgpu_buffer_rsrc_t rsA = __builtin_amdgcn_make_buffer_rsrc((void*)cfg.a_base(), 0, cfg.a_bytes(), 0x00020000);
;   const __amdgpu_buffer_rsrc_t rsB = __builtin_amdgcn_make_buffer_rsrc((void*)cfg.bt_base(), 0, cfg.bt_bytes(), 0x00020000);
;   const unsigned ldsw = (unsigned)__builtin_amdgcn_readfirstlane((int)(unsigned)(size_t)lds) + (unsigned)wid * 1024u;
;     ...
;   P_STAGE_B(G_SB(0, 0), 0, 0); P_STAGE_A(G_SA(0, 0), 0, 0); P_STAGE_B(G_SB(0, 1), 1, 0); P_STAGE_A(G_SA(0, 1), 1, 0);
;   P_STAGE_B(G_SB(1, 0), 0, 1); P_STAGE_A(G_SA(1, 0), 0, 1); P_STAGE_B(G_SB(1, 1), 1, 1);
.LBB0_1486:
	s_mov_b64 s[100:101], s[2:3]
.LBB0_1488:
	s_lshl_b32 s4, s25, 6
	v_mbcnt_lo_u32_b32 v124, -1, 0
	v_mbcnt_hi_u32_b32 v124, -1, v124
	s_add_i32 s4, s4, s65
	v_and_b32_e32 v72, 15, v124
	v_add_u32_e32 v144, s4, v72
	s_add_i32 s4, s55, -1
	s_lshl_b32 s5, s16, 13
	v_min_i32_e32 v72, s4, v144
	v_add_u32_e32 v163, 16, v144
	v_add_u32_e32 v161, 32, v144
	v_add_u32_e32 v159, 48, v144
	v_add_u32_e32 v157, 0x80, v144
	v_add_u32_e32 v155, 0x90, v144
	v_add_u32_e32 v153, 0xa0, v144
	v_add_u32_e32 v151, 0xb0, v144
	v_add_u32_e32 v72, s5, v72
	v_min_i32_e32 v74, s4, v163
	v_min_i32_e32 v76, s4, v161
	v_min_i32_e32 v78, s4, v159
	v_min_i32_e32 v80, s4, v157
	v_min_i32_e32 v82, s4, v155
	v_min_i32_e32 v120, s4, v153
	v_min_i32_e32 v122, s4, v151
	v_ashrrev_i32_e32 v73, 31, v72
	v_add_u32_e32 v74, s5, v74
	v_add_u32_e32 v76, s5, v76
	v_add_u32_e32 v78, s5, v78
	v_add_u32_e32 v80, s5, v80
	v_add_u32_e32 v82, s5, v82
	v_add_u32_e32 v120, s5, v120
	v_add_u32_e32 v122, s5, v122
	v_lshl_add_u64 v[72:73], v[72:73], 2, s[92:93]
	v_ashrrev_i32_e32 v75, 31, v74
	v_ashrrev_i32_e32 v77, 31, v76
	v_ashrrev_i32_e32 v79, 31, v78
	v_ashrrev_i32_e32 v81, 31, v80
	v_ashrrev_i32_e32 v83, 31, v82
	v_ashrrev_i32_e32 v121, 31, v120
	v_ashrrev_i32_e32 v123, 31, v122
	v_lshl_add_u64 v[74:75], v[74:75], 2, s[92:93]
	v_lshl_add_u64 v[76:77], v[76:77], 2, s[92:93]
	v_lshl_add_u64 v[78:79], v[78:79], 2, s[92:93]
	v_lshl_add_u64 v[80:81], v[80:81], 2, s[92:93]
	v_lshl_add_u64 v[82:83], v[82:83], 2, s[92:93]
	v_lshl_add_u64 v[120:121], v[120:121], 2, s[92:93]
	v_lshl_add_u64 v[122:123], v[122:123], 2, s[92:93]
	global_load_dword v145, v[72:73], off
	global_load_dword v164, v[74:75], off
	global_load_dword v162, v[76:77], off
	global_load_dword v160, v[78:79], off
	global_load_dword v158, v[80:81], off
	global_load_dword v156, v[82:83], off
	global_load_dword v154, v[120:121], off
	global_load_dword v152, v[122:123], off
	s_lshl_b32 s4, s64, 7
	s_lshl_b32 s5, s24, 5
	v_ashrrev_i32_e32 v72, 1, v124
	v_and_b32_e32 v72, -8, v72
	s_or_b32 s4, s5, s4
	v_add_u32_e32 v146, s4, v72
	s_lshl_b32 s4, s16, 12
	v_readlane_b32 s68, v254, 6
	s_ashr_i32 s5, s4, 31
	v_readlane_b32 s70, v254, 8
	v_readlane_b32 s71, v254, 9
	s_lshl_b64 s[4:5], s[4:5], 2
	s_mov_b64 s[62:63], s[70:71]
	s_add_u32 s4, s62, s4
	s_addc_u32 s5, s63, s5
	v_ashrrev_i32_e32 v147, 31, v146
	v_lshl_add_u64 v[72:73], v[146:147], 2, s[4:5]
	global_load_dwordx4 v[128:131], v[72:73], off
	global_load_dwordx4 v[120:123], v[72:73], off offset:16
	v_lshl_add_u64 v[74:75], v[72:73], 0, s[0:1]
	v_add_co_u32_e32 v72, vcc, s37, v72
	v_readlane_b32 s69, v254, 7
	s_nop 0
	v_addc_co_u32_e32 v73, vcc, 0, v73, vcc
	global_load_dwordx4 v[132:135], v[72:73], off
	global_load_dwordx4 v[124:127], v[74:75], off offset:16
	s_and_b64 vcc, exec, s[100:101]
	s_cbranch_vccnz .Lpfm1_none
	v_mbcnt_lo_u32_b32 v76, -1, 0
	v_mbcnt_hi_u32_b32 v76, -1, v76
	s_ashr_i32 s15, s14, 31
	v_or_b32_e32 v72, s87, v76
	v_lshrrev_b32_e32 v77, 3, v76
	v_readfirstlane_b32 s4, v72
	s_ashr_i32 s17, s4, 6
	s_lshl_b32 s4, s17, 3
	s_and_b32 s5, s4, 16
	v_and_or_b32 v78, v77, 4, s4
	s_add_i32 s5, s5, s48
	s_lshl_b32 s5, s5, 7
	s_and_b32 s4, s4, 0x1fffe0
	v_lshlrev_b32_e32 v78, 1, v78
	v_xor_b32_e32 v77, v77, v76
	s_add_i32 s5, s5, s4
	v_and_b32_e32 v78, 24, v78
	v_bfe_u32 v76, v76, 3, 2
	v_lshl_add_u32 v72, v72, 2, 0
	v_or3_b32 v76, s5, v78, v76
	s_lshl_b64 s[4:5], s[14:15], 23
	v_add_u32_e32 v74, 0x22410, v72
	s_add_u32 s4, s50, s4
	ds_read2st64_b32 v[72:73], v74 offset1:8
	ds_read2st64_b32 v[74:75], v74 offset0:16 offset1:24
	v_lshlrev_b32_e32 v77, 4, v77
	s_addc_u32 s5, s51, s5
	s_lshl_b32 s15, s17, 10
	v_and_b32_e32 v77, 0x70, v77
	s_add_i32 s15, s15, 0
	v_lshl_or_b32 v76, v76, 11, v77
	s_and_b32 s5, s5, 0xffff
	s_add_i32 s17, s15, 0x10010
	s_mov_b32 m0, s17
	s_nop 0
	buffer_load_dwordx4 v76, s[4:7], s34 offen lds
	s_add_i32 s17, s15, 0x12010
	s_mov_b32 m0, s17
	s_nop 0
	buffer_load_dwordx4 v76, s[4:7], s7 offen lds
	s_add_i32 s17, s15, 16
	s_waitcnt lgkmcnt(1)
	s_mov_b32 m0, s17
	s_nop 0
	buffer_load_dwordx4 v72, s[8:11], s34 offen lds
	s_add_i32 s17, s15, 0x2010
	s_mov_b32 m0, s17
	s_nop 0
	buffer_load_dwordx4 v73, s[8:11], s34 offen lds
	s_add_i32 s17, s15, 0x14010
	s_mov_b32 m0, s17
	s_nop 0
	buffer_load_dwordx4 v76, s[4:7], s37 offen lds
	s_add_i32 s17, s15, 0x16010
	s_mov_b32 m0, s17
	s_nop 0
	buffer_load_dwordx4 v76, s[4:7], s56 offen lds
	s_add_i32 s17, s15, 0x4010
	s_waitcnt lgkmcnt(0)
	s_mov_b32 m0, s17
	s_nop 0
	buffer_load_dwordx4 v74, s[8:11], s34 offen lds
	s_add_i32 s17, s15, 0x6010
	s_mov_b32 m0, s17
	s_nop 0
	buffer_load_dwordx4 v75, s[8:11], s34 offen lds
	s_add_i32 s17, s15, 0x18010
	s_mov_b32 m0, s17
	s_nop 0
	buffer_load_dwordx4 v76, s[4:7], s35 offen lds
	s_add_i32 s17, s15, 0x1a010
	s_mov_b32 m0, s17
	s_nop 0
	buffer_load_dwordx4 v76, s[4:7], s43 offen lds
	s_add_i32 s17, s15, 0x8010
	s_mov_b32 m0, s17
	s_nop 0
	buffer_load_dwordx4 v72, s[8:11], s35 offen lds
	s_add_i32 s17, s15, 0xa010
	s_mov_b32 m0, s17
	s_nop 0
	buffer_load_dwordx4 v73, s[8:11], s35 offen lds
	s_add_i32 s17, s15, 0x1c010
	s_mov_b32 m0, s17
	s_nop 0
	buffer_load_dwordx4 v76, s[4:7], s44 offen lds
	s_add_i32 s15, s15, 0x1e010
	s_mov_b32 m0, s15
	s_nop 0
	buffer_load_dwordx4 v76, s[4:7], s45 offen lds
	s_branch .Lpfm1_done

;   DI int glu4(const ColCtx& c, const f32x4& v0, const f32x4& v1) const {
;     float o[4];
; #pragma unroll
;     for (int i = 0; i < 4; ++i) {
;       const float g = fminf(v0[i] + c.bg[i], 7.f);
;       const float up = __builtin_amdgcn_fmed3f(v1[i] + c.bu[i], -7.f, 7.f);
;       const float sg = __builtin_amdgcn_rcpf(1.f + __builtin_amdgcn_exp2f(g * (-1.702f * 1.44269504088896f)));
;       o[i] = fmaf(up, 4.f, 4.f) * (g * sg);
;     }
;     return pack4_fp8(o[0], o[1], o[2], o[3]);
;   }
;   DI void epi_pair(RowTok a, const ColCtx& c0, const ColCtx& c1, const f32x4& g0, const f32x4& u0, const f32x4& g1, const f32x4& u1) const {
;     if (a < 0) return;
;     u32x2 pk; pk.x = (unsigned)glu4(c0, g0, u0); pk.y = (unsigned)glu4(c1, g1, u1);
;     *(u32x2*)(p.actq + (size_t)a * 2048 + c0.j0) = pk;
;   }
.Lpfm1_done:
	v_cmp_gt_i32_e32 vcc, s55, v144
	v_readlane_b32 s72, v254, 10
	v_readlane_b32 s73, v254, 11
	v_readlane_b32 s74, v254, 12
	v_readlane_b32 s75, v254, 13
	s_waitcnt vmcnt(25)
	v_cndmask_b32_e32 v252, -1, v145, vcc
	v_cmp_lt_i32_e32 vcc, -1, v252
	s_and_saveexec_b64 s[4:5], vcc
	v_readlane_b32 s68, v254, 47
	v_readlane_b32 s70, v254, 49
	v_readlane_b32 s71, v254, 50
	v_readlane_b32 s69, v254, 48
	s_cbranch_execz .LBB0_1490
	s_waitcnt vmcnt(17)
	v_add_f32_e32 v72, v140, v128
	v_min_f32_e32 v72, 0x40e00000, v72
	v_mul_f32_e32 v73, 0xc01d265f, v72
	v_exp_f32_e32 v73, v73
	v_add_f32_e32 v75, v141, v129
	v_min_f32_e32 v75, 0x40e00000, v75
	v_mul_f32_e32 v76, 0xc01d265f, v75
	v_add_f32_e32 v73, 1.0, v73
	v_rcp_f32_e32 v73, v73
	s_waitcnt vmcnt(15)
	v_add_f32_e32 v74, v136, v132
	v_med3_f32 v74, v74, s46, v150
	v_fma_f32 v74, v74, 4.0, 4.0
	v_mul_f32_e32 v72, v72, v73
	v_exp_f32_e32 v73, v76
	v_add_f32_e32 v76, v142, v130
	v_min_f32_e32 v76, 0x40e00000, v76
	v_mul_f32_e32 v77, 0xc01d265f, v76
	v_add_f32_e32 v73, 1.0, v73
	v_rcp_f32_e32 v73, v73
	v_exp_f32_e32 v77, v77
	v_mul_f32_e32 v74, v74, v72
	v_add_f32_e32 v72, v137, v133
	v_med3_f32 v72, v72, s46, v150
	v_fma_f32 v72, v72, 4.0, 4.0
	v_mul_f32_e32 v73, v75, v73
	v_mul_f32_e32 v73, v72, v73
	v_add_f32_e32 v72, 1.0, v77
	v_rcp_f32_e32 v72, v72
	v_add_f32_e32 v75, v138, v134
	v_med3_f32 v75, v75, s46, v150
	v_fma_f32 v75, v75, 4.0, 4.0
	v_mul_f32_e32 v72, v76, v72
	v_mul_f32_e32 v75, v75, v72
	v_add_f32_e32 v72, v139, v135
	v_med3_f32 v72, v72, s46, v150
	v_fma_f32 v78, v72, 4.0, 4.0
	v_mov_b32_e32 v72, v253
	v_add_f32_e32 v76, v143, v131
	v_cvt_pk_fp8_f32 v72, v74, v73
	v_add_f32_e32 v73, v116, v120
	v_min_f32_e32 v76, 0x40e00000, v76
	v_min_f32_e32 v73, 0x40e00000, v73
	v_mul_f32_e32 v77, 0xc01d265f, v76
	v_mul_f32_e32 v74, 0xc01d265f, v73
	v_exp_f32_e32 v77, v77
	v_exp_f32_e32 v74, v74
	v_add_f32_e32 v77, 1.0, v77
	v_add_f32_e32 v74, 1.0, v74
	v_rcp_f32_e32 v77, v77
	v_rcp_f32_e32 v74, v74
	v_mul_f32_e32 v76, v76, v77
	v_mul_f32_e32 v73, v73, v74
	v_add_f32_e32 v74, v117, v121
	v_mul_f32_e32 v76, v78, v76
	v_min_f32_e32 v74, 0x40e00000, v74
	v_cvt_pk_fp8_f32 v72, v75, v76 op_sel:[0,0,1]
	v_mul_f32_e32 v76, 0xc01d265f, v74
	v_exp_f32_e32 v76, v76
	v_add_f32_e32 v77, v118, v122
	s_waitcnt vmcnt(14)
	v_add_f32_e32 v75, v112, v124
	v_min_f32_e32 v77, 0x40e00000, v77
	v_add_f32_e32 v76, 1.0, v76
	v_med3_f32 v75, v75, s46, v150
	v_rcp_f32_e32 v76, v76
	v_mul_f32_e32 v78, 0xc01d265f, v77
	v_fma_f32 v75, v75, 4.0, 4.0
	v_exp_f32_e32 v78, v78
	v_mul_f32_e32 v75, v75, v73
	v_add_f32_e32 v73, v113, v125
	v_med3_f32 v73, v73, s46, v150
	v_fma_f32 v73, v73, 4.0, 4.0
	v_mul_f32_e32 v74, v74, v76
	v_mul_f32_e32 v74, v73, v74
	v_add_f32_e32 v73, 1.0, v78
	v_rcp_f32_e32 v73, v73
	v_add_f32_e32 v76, v114, v126
	v_med3_f32 v76, v76, s46, v150
	v_fma_f32 v76, v76, 4.0, 4.0
	v_mul_f32_e32 v73, v77, v73
	v_add_f32_e32 v77, v119, v123
	v_min_f32_e32 v77, 0x40e00000, v77
	v_mul_f32_e32 v78, 0xc01d265f, v77
	v_exp_f32_e32 v78, v78
	v_mul_f32_e32 v76, v76, v73
	v_add_f32_e32 v73, v115, v127
	v_med3_f32 v79, v73, s46, v150
	v_add_f32_e32 v73, 1.0, v78
	v_rcp_f32_e32 v78, v73
	v_mov_b32_e32 v73, v253
	v_cvt_pk_fp8_f32 v73, v75, v74
	v_fma_f32 v74, v79, 4.0, 4.0
	v_mul_f32_e32 v75, v77, v78
	v_mul_f32_e32 v74, v74, v75
	v_cvt_pk_fp8_f32 v73, v76, v74 op_sel:[0,0,1]
	v_lshlrev_b64 v[74:75], 11, v[252:253]
	v_lshl_add_u64 v[74:75], s[70:71], 0, v[74:75]
	v_lshl_add_u64 v[74:75], v[74:75], 0, v[146:147]
	global_store_dwordx2 v[74:75], v[72:73], off
.LBB0_1490:
	s_or_b64 exec, exec, s[4:5]
	v_cmp_gt_i32_e32 vcc, s55, v163
	s_waitcnt vmcnt(24)
	s_nop 0
	v_cndmask_b32_e32 v252, -1, v164, vcc
	v_cmp_lt_i32_e32 vcc, -1, v252
	s_and_saveexec_b64 s[4:5], vcc
	s_cbranch_execz .LBB0_1492
	s_waitcnt vmcnt(17)
	v_add_f32_e32 v72, v108, v128
	v_min_f32_e32 v72, 0x40e00000, v72
	v_mul_f32_e32 v73, 0xc01d265f, v72
	v_exp_f32_e32 v73, v73
	v_add_f32_e32 v75, v109, v129
	v_min_f32_e32 v75, 0x40e00000, v75
	v_mul_f32_e32 v76, 0xc01d265f, v75
	v_add_f32_e32 v73, 1.0, v73
	v_rcp_f32_e32 v73, v73
	s_waitcnt vmcnt(15)
	v_add_f32_e32 v74, v104, v132
	v_med3_f32 v74, v74, s46, v150
	v_fma_f32 v74, v74, 4.0, 4.0
	v_mul_f32_e32 v72, v72, v73
	v_exp_f32_e32 v73, v76
	v_add_f32_e32 v76, v110, v130
	v_min_f32_e32 v76, 0x40e00000, v76
	v_mul_f32_e32 v77, 0xc01d265f, v76
	v_add_f32_e32 v73, 1.0, v73
	v_rcp_f32_e32 v73, v73
	v_exp_f32_e32 v77, v77
	v_mul_f32_e32 v74, v74, v72
	v_add_f32_e32 v72, v105, v133
	v_med3_f32 v72, v72, s46, v150
	v_fma_f32 v72, v72, 4.0, 4.0
	v_mul_f32_e32 v73, v75, v73
	v_mul_f32_e32 v73, v72, v73
	v_add_f32_e32 v72, 1.0, v77
	v_rcp_f32_e32 v72, v72
	v_add_f32_e32 v75, v106, v134
	v_med3_f32 v75, v75, s46, v150
	v_fma_f32 v75, v75, 4.0, 4.0
	v_mul_f32_e32 v72, v76, v72
	v_mul_f32_e32 v75, v75, v72
	v_add_f32_e32 v72, v107, v135
	v_med3_f32 v72, v72, s46, v150
	v_fma_f32 v78, v72, 4.0, 4.0
	v_mov_b32_e32 v72, v253
	v_add_f32_e32 v76, v111, v131
	v_cvt_pk_fp8_f32 v72, v74, v73
	v_add_f32_e32 v73, v100, v120
	v_min_f32_e32 v76, 0x40e00000, v76
	v_min_f32_e32 v73, 0x40e00000, v73
	v_mul_f32_e32 v77, 0xc01d265f, v76
	v_mul_f32_e32 v74, 0xc01d265f, v73
	v_exp_f32_e32 v77, v77
	v_exp_f32_e32 v74, v74
	v_add_f32_e32 v77, 1.0, v77
	v_add_f32_e32 v74, 1.0, v74
	v_rcp_f32_e32 v77, v77
	v_rcp_f32_e32 v74, v74
	v_mul_f32_e32 v76, v76, v77
	v_mul_f32_e32 v73, v73, v74
	v_add_f32_e32 v74, v101, v121
	v_mul_f32_e32 v76, v78, v76
	v_min_f32_e32 v74, 0x40e00000, v74
	v_cvt_pk_fp8_f32 v72, v75, v76 op_sel:[0,0,1]
	v_mul_f32_e32 v76, 0xc01d265f, v74
	v_exp_f32_e32 v76, v76
	v_add_f32_e32 v77, v102, v122
	s_waitcnt vmcnt(14)
	v_add_f32_e32 v75, v96, v124
	v_min_f32_e32 v77, 0x40e00000, v77
	v_add_f32_e32 v76, 1.0, v76
	v_med3_f32 v75, v75, s46, v150
	v_rcp_f32_e32 v76, v76
	v_mul_f32_e32 v78, 0xc01d265f, v77
	v_fma_f32 v75, v75, 4.0, 4.0
	v_exp_f32_e32 v78, v78
	v_mul_f32_e32 v75, v75, v73
	v_add_f32_e32 v73, v97, v125
	v_med3_f32 v73, v73, s46, v150
	v_fma_f32 v73, v73, 4.0, 4.0
	v_mul_f32_e32 v74, v74, v76
	v_mul_f32_e32 v74, v73, v74
	v_add_f32_e32 v73, 1.0, v78
	v_rcp_f32_e32 v73, v73
	v_add_f32_e32 v76, v98, v126
	v_med3_f32 v76, v76, s46, v150
	v_fma_f32 v76, v76, 4.0, 4.0
	v_mul_f32_e32 v73, v77, v73
	v_add_f32_e32 v77, v103, v123
	v_min_f32_e32 v77, 0x40e00000, v77
	v_mul_f32_e32 v78, 0xc01d265f, v77
	v_exp_f32_e32 v78, v78
	v_mul_f32_e32 v76, v76, v73
	v_add_f32_e32 v73, v99, v127
	v_med3_f32 v79, v73, s46, v150
	v_add_f32_e32 v73, 1.0, v78
	v_rcp_f32_e32 v78, v73
	v_mov_b32_e32 v73, v253
	v_cvt_pk_fp8_f32 v73, v75, v74
	v_fma_f32 v74, v79, 4.0, 4.0
	v_mul_f32_e32 v75, v77, v78
	v_mul_f32_e32 v74, v74, v75
	v_cvt_pk_fp8_f32 v73, v76, v74 op_sel:[0,0,1]
	v_lshlrev_b64 v[74:75], 11, v[252:253]
	v_lshl_add_u64 v[74:75], s[70:71], 0, v[74:75]
	v_lshl_add_u64 v[74:75], v[74:75], 0, v[146:147]
	global_store_dwordx2 v[74:75], v[72:73], off
;   DI int glu4(const ColCtx& c, const f32x4& v0, const f32x4& v1) const {
;     float o[4];
; #pragma unroll
;     for (int i = 0; i < 4; ++i) {
;       const float g = fminf(v0[i] + c.bg[i], 7.f);
;       const float up = __builtin_amdgcn_fmed3f(v1[i] + c.bu[i], -7.f, 7.f);
;       const float sg = __builtin_amdgcn_rcpf(1.f + __builtin_amdgcn_exp2f(g * (-1.702f * 1.44269504088896f)));
;       o[i] = fmaf(up, 4.f, 4.f) * (g * sg);
;     }
;     return pack4_fp8(o[0], o[1], o[2], o[3]);
;   }
;   DI void epi_pair(RowTok a, const ColCtx& c0, const ColCtx& c1, const f32x4& g0, const f32x4& u0, const f32x4& g1, const f32x4& u1) const {
;     if (a < 0) return;
;     u32x2 pk; pk.x = (unsigned)glu4(c0, g0, u0); pk.y = (unsigned)glu4(c1, g1, u1);
;     *(u32x2*)(p.actq + (size_t)a * 2048 + c0.j0) = pk;
;   }
.LBB0_1492:
	s_or_b64 exec, exec, s[4:5]
	v_cmp_gt_i32_e32 vcc, s55, v161
	s_waitcnt vmcnt(23)
	s_nop 0
	v_cndmask_b32_e32 v252, -1, v162, vcc
	v_cmp_lt_i32_e32 vcc, -1, v252
	s_and_saveexec_b64 s[4:5], vcc
	s_cbranch_execz .LBB0_1494
	s_waitcnt vmcnt(17)
	v_add_f32_e32 v72, v92, v128
	v_min_f32_e32 v72, 0x40e00000, v72
	v_mul_f32_e32 v73, 0xc01d265f, v72
	v_exp_f32_e32 v73, v73
	v_add_f32_e32 v75, v93, v129
	v_min_f32_e32 v75, 0x40e00000, v75
	v_mul_f32_e32 v76, 0xc01d265f, v75
	v_add_f32_e32 v73, 1.0, v73
	v_rcp_f32_e32 v73, v73
	s_waitcnt vmcnt(15)
	v_add_f32_e32 v74, v88, v132
	v_med3_f32 v74, v74, s46, v150
	v_fma_f32 v74, v74, 4.0, 4.0
	v_mul_f32_e32 v72, v72, v73
	v_exp_f32_e32 v73, v76
	v_add_f32_e32 v76, v94, v130
	v_min_f32_e32 v76, 0x40e00000, v76
	v_mul_f32_e32 v77, 0xc01d265f, v76
	v_add_f32_e32 v73, 1.0, v73
	v_rcp_f32_e32 v73, v73
	v_exp_f32_e32 v77, v77
	v_mul_f32_e32 v74, v74, v72
	v_add_f32_e32 v72, v89, v133
	v_med3_f32 v72, v72, s46, v150
	v_fma_f32 v72, v72, 4.0, 4.0
	v_mul_f32_e32 v73, v75, v73
	v_mul_f32_e32 v73, v72, v73
	v_add_f32_e32 v72, 1.0, v77
	v_rcp_f32_e32 v72, v72
	v_add_f32_e32 v75, v90, v134
	v_med3_f32 v75, v75, s46, v150
	v_fma_f32 v75, v75, 4.0, 4.0
	v_mul_f32_e32 v72, v76, v72
	v_mul_f32_e32 v75, v75, v72
	v_add_f32_e32 v72, v91, v135
	v_med3_f32 v72, v72, s46, v150
	v_fma_f32 v78, v72, 4.0, 4.0
	v_mov_b32_e32 v72, v253
	v_add_f32_e32 v76, v95, v131
	v_cvt_pk_fp8_f32 v72, v74, v73
	v_add_f32_e32 v73, v84, v120
	v_min_f32_e32 v76, 0x40e00000, v76
	v_min_f32_e32 v73, 0x40e00000, v73
	v_mul_f32_e32 v77, 0xc01d265f, v76
	v_mul_f32_e32 v74, 0xc01d265f, v73
	v_exp_f32_e32 v77, v77
	v_exp_f32_e32 v74, v74
	s_waitcnt vmcnt(14)
	v_add_f32_e32 v8, v8, v124
	v_med3_f32 v8, v8, s46, v150
	v_add_f32_e32 v77, 1.0, v77
	v_add_f32_e32 v74, 1.0, v74
	v_rcp_f32_e32 v77, v77
	v_rcp_f32_e32 v74, v74
	v_fma_f32 v8, v8, 4.0, 4.0
	v_add_f32_e32 v9, v9, v125
	v_mul_f32_e32 v76, v76, v77
	v_mul_f32_e32 v73, v73, v74
	v_add_f32_e32 v74, v85, v121
	v_mul_f32_e32 v76, v78, v76
	v_min_f32_e32 v74, 0x40e00000, v74
	v_cvt_pk_fp8_f32 v72, v75, v76 op_sel:[0,0,1]
	v_mul_f32_e32 v75, 0xc01d265f, v74
	v_exp_f32_e32 v75, v75
	v_mul_f32_e32 v8, v8, v73
	v_med3_f32 v9, v9, s46, v150
	v_fma_f32 v9, v9, 4.0, 4.0
	v_add_f32_e32 v73, 1.0, v75
	v_add_f32_e32 v75, v86, v122
	v_min_f32_e32 v75, 0x40e00000, v75
	v_rcp_f32_e32 v73, v73
	v_mul_f32_e32 v76, 0xc01d265f, v75
	v_exp_f32_e32 v76, v76
	v_add_f32_e32 v10, v10, v126
	v_mul_f32_e32 v73, v74, v73
	v_mul_f32_e32 v9, v9, v73
	v_add_f32_e32 v73, 1.0, v76
	v_rcp_f32_e32 v73, v73
	v_add_f32_e32 v74, v87, v123
	v_min_f32_e32 v74, 0x40e00000, v74
	v_med3_f32 v10, v10, s46, v150
	v_mul_f32_e32 v73, v75, v73
	v_mul_f32_e32 v75, 0xc01d265f, v74
	v_exp_f32_e32 v75, v75
	v_fma_f32 v10, v10, 4.0, 4.0
	v_mul_f32_e32 v10, v10, v73
	v_add_f32_e32 v11, v11, v127
	v_add_f32_e32 v73, 1.0, v75
	v_rcp_f32_e32 v75, v73
	v_mov_b32_e32 v73, v253
	v_cvt_pk_fp8_f32 v73, v8, v9
	v_med3_f32 v11, v11, s46, v150
	v_fma_f32 v8, v11, 4.0, 4.0
	v_mul_f32_e32 v9, v74, v75
	v_mul_f32_e32 v8, v8, v9
	v_cvt_pk_fp8_f32 v73, v10, v8 op_sel:[0,0,1]
	v_lshlrev_b64 v[8:9], 11, v[252:253]
	v_lshl_add_u64 v[8:9], s[70:71], 0, v[8:9]
	v_lshl_add_u64 v[8:9], v[8:9], 0, v[146:147]
	global_store_dwordx2 v[8:9], v[72:73], off
.LBB0_1494:
	s_or_b64 exec, exec, s[4:5]
	v_cmp_gt_i32_e32 vcc, s55, v159
	s_waitcnt vmcnt(22)
	s_nop 0
	v_cndmask_b32_e32 v252, -1, v160, vcc
	v_cmp_lt_i32_e32 vcc, -1, v252
	s_and_saveexec_b64 s[4:5], vcc
	s_cbranch_execz .LBB0_1496
	s_waitcnt vmcnt(17)
	v_add_f32_e32 v8, v220, v128
	v_min_f32_e32 v8, 0x40e00000, v8
	v_mul_f32_e32 v9, 0xc01d265f, v8
	v_exp_f32_e32 v9, v9
	v_add_f32_e32 v11, v221, v129
	v_min_f32_e32 v11, 0x40e00000, v11
	v_mul_f32_e32 v72, 0xc01d265f, v11
	v_add_f32_e32 v9, 1.0, v9
	v_rcp_f32_e32 v9, v9
	s_waitcnt vmcnt(15)
	v_add_f32_e32 v10, v224, v132
	v_med3_f32 v10, v10, s46, v150
	v_fma_f32 v10, v10, 4.0, 4.0
	v_mul_f32_e32 v8, v8, v9
	v_exp_f32_e32 v9, v72
	v_add_f32_e32 v72, v222, v130
	v_min_f32_e32 v72, 0x40e00000, v72
	v_mul_f32_e32 v73, 0xc01d265f, v72
	v_add_f32_e32 v9, 1.0, v9
	v_rcp_f32_e32 v9, v9
	v_exp_f32_e32 v73, v73
	v_mul_f32_e32 v10, v10, v8
	v_add_f32_e32 v8, v225, v133
	v_med3_f32 v8, v8, s46, v150
	v_fma_f32 v8, v8, 4.0, 4.0
	v_mul_f32_e32 v9, v11, v9
	v_mul_f32_e32 v9, v8, v9
	v_add_f32_e32 v8, 1.0, v73
	v_rcp_f32_e32 v8, v8
	v_add_f32_e32 v11, v226, v134
	v_med3_f32 v11, v11, s46, v150
	v_fma_f32 v11, v11, 4.0, 4.0
	v_mul_f32_e32 v8, v72, v8
	v_mul_f32_e32 v11, v11, v8
	v_add_f32_e32 v8, v227, v135
	v_med3_f32 v8, v8, s46, v150
	v_fma_f32 v74, v8, 4.0, 4.0
	v_mov_b32_e32 v8, v253
	v_add_f32_e32 v72, v223, v131
	v_cvt_pk_fp8_f32 v8, v10, v9
	v_add_f32_e32 v9, v68, v120
	v_min_f32_e32 v72, 0x40e00000, v72
	v_min_f32_e32 v9, 0x40e00000, v9
	v_mul_f32_e32 v73, 0xc01d265f, v72
	v_mul_f32_e32 v10, 0xc01d265f, v9
	v_exp_f32_e32 v73, v73
	v_exp_f32_e32 v10, v10
	v_add_f32_e32 v73, 1.0, v73
	v_add_f32_e32 v10, 1.0, v10
	v_rcp_f32_e32 v73, v73
	v_rcp_f32_e32 v10, v10
	v_mul_f32_e32 v68, v72, v73
	v_mul_f32_e32 v9, v9, v10
	v_add_f32_e32 v10, v69, v121
	v_mul_f32_e32 v68, v74, v68
	v_min_f32_e32 v10, 0x40e00000, v10
	v_cvt_pk_fp8_f32 v8, v11, v68 op_sel:[0,0,1]
	s_waitcnt vmcnt(14)
	v_add_f32_e32 v11, v56, v124
	v_mul_f32_e32 v56, 0xc01d265f, v10
	v_exp_f32_e32 v56, v56
	v_med3_f32 v11, v11, s46, v150
	v_fma_f32 v11, v11, 4.0, 4.0
	v_mul_f32_e32 v11, v11, v9
	v_add_f32_e32 v9, v57, v125
	v_add_f32_e32 v57, v70, v122
	v_add_f32_e32 v56, 1.0, v56
	v_min_f32_e32 v57, 0x40e00000, v57
	v_rcp_f32_e32 v56, v56
	v_mul_f32_e32 v68, 0xc01d265f, v57
	v_exp_f32_e32 v68, v68
	v_med3_f32 v9, v9, s46, v150
	v_fma_f32 v9, v9, 4.0, 4.0
	v_mul_f32_e32 v10, v10, v56
	v_mul_f32_e32 v10, v9, v10
	v_add_f32_e32 v9, 1.0, v68
	v_rcp_f32_e32 v9, v9
	v_add_f32_e32 v56, v58, v126
	v_med3_f32 v56, v56, s46, v150
	v_fma_f32 v56, v56, 4.0, 4.0
	v_mul_f32_e32 v9, v57, v9
	v_add_f32_e32 v57, v71, v123
	v_min_f32_e32 v57, 0x40e00000, v57
	v_mul_f32_e32 v58, 0xc01d265f, v57
	v_exp_f32_e32 v58, v58
	v_mul_f32_e32 v56, v56, v9
	v_add_f32_e32 v9, v59, v127
	v_med3_f32 v59, v9, s46, v150
	v_add_f32_e32 v9, 1.0, v58
	v_rcp_f32_e32 v58, v9
	v_mov_b32_e32 v9, v253
	v_cvt_pk_fp8_f32 v9, v11, v10
	v_fma_f32 v10, v59, 4.0, 4.0
	v_mul_f32_e32 v11, v57, v58
	v_mul_f32_e32 v10, v10, v11
	v_cvt_pk_fp8_f32 v9, v56, v10 op_sel:[0,0,1]
	v_lshlrev_b64 v[10:11], 11, v[252:253]
	v_lshl_add_u64 v[10:11], s[70:71], 0, v[10:11]
	v_lshl_add_u64 v[10:11], v[10:11], 0, v[146:147]
	global_store_dwordx2 v[10:11], v[8:9], off
;   DI int glu4(const ColCtx& c, const f32x4& v0, const f32x4& v1) const {
;     float o[4];
; #pragma unroll
;     for (int i = 0; i < 4; ++i) {
;       const float g = fminf(v0[i] + c.bg[i], 7.f);
;       const float up = __builtin_amdgcn_fmed3f(v1[i] + c.bu[i], -7.f, 7.f);
;       const float sg = __builtin_amdgcn_rcpf(1.f + __builtin_amdgcn_exp2f(g * (-1.702f * 1.44269504088896f)));
;       o[i] = fmaf(up, 4.f, 4.f) * (g * sg);
;     }
;     return pack4_fp8(o[0], o[1], o[2], o[3]);
;   }
;   DI void epi_pair(RowTok a, const ColCtx& c0, const ColCtx& c1, const f32x4& g0, const f32x4& u0, const f32x4& g1, const f32x4& u1) const {
;     if (a < 0) return;
;     u32x2 pk; pk.x = (unsigned)glu4(c0, g0, u0); pk.y = (unsigned)glu4(c1, g1, u1);
;     *(u32x2*)(p.actq + (size_t)a * 2048 + c0.j0) = pk;
;   }
.LBB0_1496:
	s_or_b64 exec, exec, s[4:5]
	v_cmp_gt_i32_e32 vcc, s55, v157
	s_waitcnt vmcnt(21)
	s_nop 0
	v_cndmask_b32_e32 v252, -1, v158, vcc
	v_cmp_lt_i32_e32 vcc, -1, v252
	s_and_saveexec_b64 s[4:5], vcc
	s_cbranch_execz .LBB0_1498
	s_waitcnt vmcnt(17)
	v_add_f32_e32 v8, v64, v128
	v_min_f32_e32 v8, 0x40e00000, v8
	v_mul_f32_e32 v9, 0xc01d265f, v8
	v_exp_f32_e32 v9, v9
	v_add_f32_e32 v11, v65, v129
	v_min_f32_e32 v11, 0x40e00000, v11
	v_mul_f32_e32 v56, 0xc01d265f, v11
	v_add_f32_e32 v9, 1.0, v9
	v_rcp_f32_e32 v9, v9
	s_waitcnt vmcnt(15)
	v_add_f32_e32 v10, v60, v132
	v_med3_f32 v10, v10, s46, v150
	v_fma_f32 v10, v10, 4.0, 4.0
	v_mul_f32_e32 v8, v8, v9
	v_exp_f32_e32 v9, v56
	v_add_f32_e32 v56, v66, v130
	v_min_f32_e32 v56, 0x40e00000, v56
	v_mul_f32_e32 v57, 0xc01d265f, v56
	v_add_f32_e32 v9, 1.0, v9
	v_rcp_f32_e32 v9, v9
	v_exp_f32_e32 v57, v57
	v_mul_f32_e32 v10, v10, v8
	v_add_f32_e32 v8, v61, v133
	v_med3_f32 v8, v8, s46, v150
	v_fma_f32 v8, v8, 4.0, 4.0
	v_mul_f32_e32 v9, v11, v9
	v_mul_f32_e32 v9, v8, v9
	v_add_f32_e32 v8, 1.0, v57
	v_rcp_f32_e32 v8, v8
	v_add_f32_e32 v11, v62, v134
	v_med3_f32 v11, v11, s46, v150
	v_fma_f32 v11, v11, 4.0, 4.0
	v_mul_f32_e32 v8, v56, v8
	v_mul_f32_e32 v11, v11, v8
	v_add_f32_e32 v8, v63, v135
	v_med3_f32 v8, v8, s46, v150
	v_fma_f32 v58, v8, 4.0, 4.0
	v_mov_b32_e32 v8, v253
	v_add_f32_e32 v56, v67, v131
	v_cvt_pk_fp8_f32 v8, v10, v9
	v_add_f32_e32 v9, v52, v120
	v_min_f32_e32 v56, 0x40e00000, v56
	v_min_f32_e32 v9, 0x40e00000, v9
	v_mul_f32_e32 v57, 0xc01d265f, v56
	v_mul_f32_e32 v10, 0xc01d265f, v9
	v_exp_f32_e32 v57, v57
	v_exp_f32_e32 v10, v10
	v_add_f32_e32 v57, 1.0, v57
	v_add_f32_e32 v10, 1.0, v10
	v_rcp_f32_e32 v57, v57
	v_rcp_f32_e32 v10, v10
	v_mul_f32_e32 v52, v56, v57
	v_mul_f32_e32 v9, v9, v10
	v_add_f32_e32 v10, v53, v121
	v_mul_f32_e32 v52, v58, v52
	v_min_f32_e32 v10, 0x40e00000, v10
	v_cvt_pk_fp8_f32 v8, v11, v52 op_sel:[0,0,1]
	s_waitcnt vmcnt(14)
	v_add_f32_e32 v11, v48, v124
	v_mul_f32_e32 v48, 0xc01d265f, v10
	v_exp_f32_e32 v48, v48
	v_med3_f32 v11, v11, s46, v150
	v_fma_f32 v11, v11, 4.0, 4.0
	v_mul_f32_e32 v11, v11, v9
	v_add_f32_e32 v9, v49, v125
	v_add_f32_e32 v49, v54, v122
	v_add_f32_e32 v48, 1.0, v48
	v_min_f32_e32 v49, 0x40e00000, v49
	v_rcp_f32_e32 v48, v48
	v_mul_f32_e32 v52, 0xc01d265f, v49
	v_exp_f32_e32 v52, v52
	v_med3_f32 v9, v9, s46, v150
	v_fma_f32 v9, v9, 4.0, 4.0
	v_mul_f32_e32 v10, v10, v48
	v_mul_f32_e32 v10, v9, v10
	v_add_f32_e32 v9, 1.0, v52
	v_rcp_f32_e32 v9, v9
	v_add_f32_e32 v48, v50, v126
	v_med3_f32 v48, v48, s46, v150
	v_fma_f32 v48, v48, 4.0, 4.0
	v_mul_f32_e32 v9, v49, v9
	v_add_f32_e32 v49, v55, v123
	v_min_f32_e32 v49, 0x40e00000, v49
	v_mul_f32_e32 v50, 0xc01d265f, v49
	v_exp_f32_e32 v50, v50
	v_mul_f32_e32 v48, v48, v9
	v_add_f32_e32 v9, v51, v127
	v_med3_f32 v51, v9, s46, v150
	v_add_f32_e32 v9, 1.0, v50
	v_rcp_f32_e32 v50, v9
	v_mov_b32_e32 v9, v253
	v_cvt_pk_fp8_f32 v9, v11, v10
	v_fma_f32 v10, v51, 4.0, 4.0
	v_mul_f32_e32 v11, v49, v50
	v_mul_f32_e32 v10, v10, v11
	v_cvt_pk_fp8_f32 v9, v48, v10 op_sel:[0,0,1]
	v_lshlrev_b64 v[10:11], 11, v[252:253]
	v_lshl_add_u64 v[10:11], s[70:71], 0, v[10:11]
	v_lshl_add_u64 v[10:11], v[10:11], 0, v[146:147]
	global_store_dwordx2 v[10:11], v[8:9], off
.LBB0_1498:
	s_or_b64 exec, exec, s[4:5]
	v_cmp_gt_i32_e32 vcc, s55, v155
	s_waitcnt vmcnt(20)
	s_nop 0
	v_cndmask_b32_e32 v252, -1, v156, vcc
	v_cmp_lt_i32_e32 vcc, -1, v252
	s_and_saveexec_b64 s[4:5], vcc
	s_cbranch_execz .LBB0_1500
	s_waitcnt vmcnt(17)
	v_add_f32_e32 v8, v44, v128
	v_min_f32_e32 v8, 0x40e00000, v8
	v_mul_f32_e32 v9, 0xc01d265f, v8
	v_exp_f32_e32 v9, v9
	v_add_f32_e32 v11, v45, v129
	v_min_f32_e32 v11, 0x40e00000, v11
	s_waitcnt vmcnt(15)
	v_add_f32_e32 v10, v40, v132
	v_add_f32_e32 v9, 1.0, v9
	v_rcp_f32_e32 v9, v9
	v_mul_f32_e32 v40, 0xc01d265f, v11
	v_med3_f32 v10, v10, s46, v150
	v_fma_f32 v10, v10, 4.0, 4.0
	v_mul_f32_e32 v8, v8, v9
	v_exp_f32_e32 v9, v40
	v_add_f32_e32 v40, v46, v130
	v_min_f32_e32 v40, 0x40e00000, v40
	v_mul_f32_e32 v10, v10, v8
	v_add_f32_e32 v9, 1.0, v9
	v_add_f32_e32 v8, v41, v133
	v_rcp_f32_e32 v9, v9
	v_mul_f32_e32 v41, 0xc01d265f, v40
	v_exp_f32_e32 v41, v41
	v_med3_f32 v8, v8, s46, v150
	v_fma_f32 v8, v8, 4.0, 4.0
	v_mul_f32_e32 v9, v11, v9
	v_mul_f32_e32 v9, v8, v9
	v_add_f32_e32 v8, 1.0, v41
	v_rcp_f32_e32 v8, v8
	v_add_f32_e32 v11, v42, v134
	v_med3_f32 v11, v11, s46, v150
	v_fma_f32 v11, v11, 4.0, 4.0
	v_mul_f32_e32 v8, v40, v8
	v_mul_f32_e32 v11, v11, v8
	v_add_f32_e32 v8, v43, v135
	v_med3_f32 v8, v8, s46, v150
	v_fma_f32 v42, v8, 4.0, 4.0
	v_mov_b32_e32 v8, v253
	v_add_f32_e32 v40, v47, v131
	v_cvt_pk_fp8_f32 v8, v10, v9
	v_add_f32_e32 v9, v36, v120
	v_min_f32_e32 v40, 0x40e00000, v40
	v_min_f32_e32 v9, 0x40e00000, v9
	v_mul_f32_e32 v41, 0xc01d265f, v40
	v_mul_f32_e32 v10, 0xc01d265f, v9
	v_exp_f32_e32 v41, v41
	v_exp_f32_e32 v10, v10
	v_add_f32_e32 v41, 1.0, v41
	v_add_f32_e32 v10, 1.0, v10
	v_rcp_f32_e32 v41, v41
	v_rcp_f32_e32 v10, v10
	v_mul_f32_e32 v36, v40, v41
	v_mul_f32_e32 v9, v9, v10
	v_add_f32_e32 v10, v37, v121
	v_mul_f32_e32 v36, v42, v36
	v_min_f32_e32 v10, 0x40e00000, v10
	v_cvt_pk_fp8_f32 v8, v11, v36 op_sel:[0,0,1]
	s_waitcnt vmcnt(14)
	v_add_f32_e32 v11, v32, v124
	v_mul_f32_e32 v32, 0xc01d265f, v10
	v_exp_f32_e32 v32, v32
	v_med3_f32 v11, v11, s46, v150
	v_fma_f32 v11, v11, 4.0, 4.0
	v_mul_f32_e32 v11, v11, v9
	v_add_f32_e32 v9, v33, v125
	v_add_f32_e32 v33, v38, v122
	v_add_f32_e32 v32, 1.0, v32
	v_min_f32_e32 v33, 0x40e00000, v33
	v_rcp_f32_e32 v32, v32
	v_mul_f32_e32 v36, 0xc01d265f, v33
	v_exp_f32_e32 v36, v36
	v_med3_f32 v9, v9, s46, v150
	v_fma_f32 v9, v9, 4.0, 4.0
	v_mul_f32_e32 v10, v10, v32
	v_mul_f32_e32 v10, v9, v10
	v_add_f32_e32 v9, 1.0, v36
	v_rcp_f32_e32 v9, v9
	v_add_f32_e32 v32, v34, v126
	v_med3_f32 v32, v32, s46, v150
	v_fma_f32 v32, v32, 4.0, 4.0
	v_mul_f32_e32 v9, v33, v9
	v_add_f32_e32 v33, v39, v123
	v_min_f32_e32 v33, 0x40e00000, v33
	v_mul_f32_e32 v34, 0xc01d265f, v33
	v_exp_f32_e32 v34, v34
	v_mul_f32_e32 v32, v32, v9
	v_add_f32_e32 v9, v35, v127
	v_med3_f32 v35, v9, s46, v150
	v_add_f32_e32 v9, 1.0, v34
	v_rcp_f32_e32 v34, v9
	v_mov_b32_e32 v9, v253
	v_cvt_pk_fp8_f32 v9, v11, v10
	v_fma_f32 v10, v35, 4.0, 4.0
	v_mul_f32_e32 v11, v33, v34
	v_mul_f32_e32 v10, v10, v11
	v_cvt_pk_fp8_f32 v9, v32, v10 op_sel:[0,0,1]
	v_lshlrev_b64 v[10:11], 11, v[252:253]
	v_lshl_add_u64 v[10:11], s[70:71], 0, v[10:11]
	v_lshl_add_u64 v[10:11], v[10:11], 0, v[146:147]
	global_store_dwordx2 v[10:11], v[8:9], off
;   DI int glu4(const ColCtx& c, const f32x4& v0, const f32x4& v1) const {
;     float o[4];
; #pragma unroll
;     for (int i = 0; i < 4; ++i) {
;       const float g = fminf(v0[i] + c.bg[i], 7.f);
;       const float up = __builtin_amdgcn_fmed3f(v1[i] + c.bu[i], -7.f, 7.f);
;       const float sg = __builtin_amdgcn_rcpf(1.f + __builtin_amdgcn_exp2f(g * (-1.702f * 1.44269504088896f)));
;       o[i] = fmaf(up, 4.f, 4.f) * (g * sg);
;     }
;     return pack4_fp8(o[0], o[1], o[2], o[3]);
;   }
;   DI void epi_pair(RowTok a, const ColCtx& c0, const ColCtx& c1, const f32x4& g0, const f32x4& u0, const f32x4& g1, const f32x4& u1) const {
;     if (a < 0) return;
;     u32x2 pk; pk.x = (unsigned)glu4(c0, g0, u0); pk.y = (unsigned)glu4(c1, g1, u1);
;     *(u32x2*)(p.actq + (size_t)a * 2048 + c0.j0) = pk;
;   }
.LBB0_1500:
	s_or_b64 exec, exec, s[4:5]
	v_cmp_gt_i32_e32 vcc, s55, v153
	s_waitcnt vmcnt(19)
	s_nop 0
	v_cndmask_b32_e32 v252, -1, v154, vcc
	v_cmp_lt_i32_e32 vcc, -1, v252
	s_and_saveexec_b64 s[4:5], vcc
	s_cbranch_execz .LBB0_1502
	s_waitcnt vmcnt(17)
	v_add_f32_e32 v8, v28, v128
	v_min_f32_e32 v8, 0x40e00000, v8
	v_mul_f32_e32 v9, 0xc01d265f, v8
	v_exp_f32_e32 v9, v9
	v_add_f32_e32 v11, v29, v129
	v_min_f32_e32 v11, 0x40e00000, v11
	s_waitcnt vmcnt(15)
	v_add_f32_e32 v10, v24, v132
	v_add_f32_e32 v9, 1.0, v9
	v_rcp_f32_e32 v9, v9
	v_mul_f32_e32 v24, 0xc01d265f, v11
	v_med3_f32 v10, v10, s46, v150
	v_fma_f32 v10, v10, 4.0, 4.0
	v_mul_f32_e32 v8, v8, v9
	v_exp_f32_e32 v9, v24
	v_add_f32_e32 v24, v30, v130
	v_min_f32_e32 v24, 0x40e00000, v24
	v_mul_f32_e32 v10, v10, v8
	v_add_f32_e32 v9, 1.0, v9
	v_add_f32_e32 v8, v25, v133
	v_rcp_f32_e32 v9, v9
	v_mul_f32_e32 v25, 0xc01d265f, v24
	v_exp_f32_e32 v25, v25
	v_med3_f32 v8, v8, s46, v150
	v_fma_f32 v8, v8, 4.0, 4.0
	v_mul_f32_e32 v9, v11, v9
	v_mul_f32_e32 v9, v8, v9
	v_add_f32_e32 v8, 1.0, v25
	v_rcp_f32_e32 v8, v8
	v_add_f32_e32 v11, v26, v134
	v_med3_f32 v11, v11, s46, v150
	v_fma_f32 v11, v11, 4.0, 4.0
	v_mul_f32_e32 v8, v24, v8
	v_mul_f32_e32 v11, v11, v8
	v_add_f32_e32 v8, v27, v135
	v_med3_f32 v8, v8, s46, v150
	v_fma_f32 v26, v8, 4.0, 4.0
	v_mov_b32_e32 v8, v253
	v_add_f32_e32 v24, v31, v131
	v_cvt_pk_fp8_f32 v8, v10, v9
	v_add_f32_e32 v9, v20, v120
	v_min_f32_e32 v24, 0x40e00000, v24
	v_min_f32_e32 v9, 0x40e00000, v9
	v_mul_f32_e32 v25, 0xc01d265f, v24
	v_mul_f32_e32 v10, 0xc01d265f, v9
	v_exp_f32_e32 v25, v25
	v_exp_f32_e32 v10, v10
	v_add_f32_e32 v25, 1.0, v25
	v_add_f32_e32 v10, 1.0, v10
	v_rcp_f32_e32 v25, v25
	v_rcp_f32_e32 v10, v10
	v_mul_f32_e32 v20, v24, v25
	v_mul_f32_e32 v9, v9, v10
	v_add_f32_e32 v10, v21, v121
	v_mul_f32_e32 v20, v26, v20
	v_min_f32_e32 v10, 0x40e00000, v10
	v_cvt_pk_fp8_f32 v8, v11, v20 op_sel:[0,0,1]
	s_waitcnt vmcnt(14)
	v_add_f32_e32 v11, v16, v124
	v_mul_f32_e32 v16, 0xc01d265f, v10
	v_exp_f32_e32 v16, v16
	v_med3_f32 v11, v11, s46, v150
	v_fma_f32 v11, v11, 4.0, 4.0
	v_mul_f32_e32 v11, v11, v9
	v_add_f32_e32 v9, v17, v125
	v_add_f32_e32 v17, v22, v122
	v_add_f32_e32 v16, 1.0, v16
	v_min_f32_e32 v17, 0x40e00000, v17
	v_rcp_f32_e32 v16, v16
	v_mul_f32_e32 v20, 0xc01d265f, v17
	v_exp_f32_e32 v20, v20
	v_med3_f32 v9, v9, s46, v150
	v_fma_f32 v9, v9, 4.0, 4.0
	v_mul_f32_e32 v10, v10, v16
	v_mul_f32_e32 v10, v9, v10
	v_add_f32_e32 v9, 1.0, v20
	v_rcp_f32_e32 v9, v9
	v_add_f32_e32 v16, v18, v126
	v_med3_f32 v16, v16, s46, v150
	v_fma_f32 v16, v16, 4.0, 4.0
	v_mul_f32_e32 v9, v17, v9
	v_add_f32_e32 v17, v23, v123
	v_min_f32_e32 v17, 0x40e00000, v17
	v_mul_f32_e32 v18, 0xc01d265f, v17
	v_exp_f32_e32 v18, v18
	v_mul_f32_e32 v16, v16, v9
	v_add_f32_e32 v9, v19, v127
	v_med3_f32 v19, v9, s46, v150
	v_add_f32_e32 v9, 1.0, v18
	v_rcp_f32_e32 v18, v9
	v_mov_b32_e32 v9, v253
	v_cvt_pk_fp8_f32 v9, v11, v10
	v_fma_f32 v10, v19, 4.0, 4.0
	v_mul_f32_e32 v11, v17, v18
	v_mul_f32_e32 v10, v10, v11
	v_cvt_pk_fp8_f32 v9, v16, v10 op_sel:[0,0,1]
	v_lshlrev_b64 v[10:11], 11, v[252:253]
	v_lshl_add_u64 v[10:11], s[70:71], 0, v[10:11]
	v_lshl_add_u64 v[10:11], v[10:11], 0, v[146:147]
	global_store_dwordx2 v[10:11], v[8:9], off
.LBB0_1502:
	s_or_b64 exec, exec, s[4:5]
	v_cmp_gt_i32_e32 vcc, s55, v151
	s_waitcnt vmcnt(18)
	s_nop 0
	v_cndmask_b32_e32 v252, -1, v152, vcc
	v_cmp_lt_i32_e32 vcc, -1, v252
	s_and_saveexec_b64 s[4:5], vcc
	s_cbranch_execz .LBB0_1504
	s_waitcnt vmcnt(17)
	v_add_f32_e32 v8, v12, v128
	v_min_f32_e32 v8, 0x40e00000, v8
	v_mul_f32_e32 v9, 0xc01d265f, v8
	v_exp_f32_e32 v9, v9
	v_add_f32_e32 v11, v13, v129
	v_min_f32_e32 v11, 0x40e00000, v11
	v_mul_f32_e32 v12, 0xc01d265f, v11
	v_add_f32_e32 v9, 1.0, v9
	v_rcp_f32_e32 v9, v9
	s_waitcnt vmcnt(15)
	v_add_f32_e32 v10, v244, v132
	v_med3_f32 v10, v10, s46, v150
	v_fma_f32 v10, v10, 4.0, 4.0
	v_mul_f32_e32 v8, v8, v9
	v_exp_f32_e32 v9, v12
	v_add_f32_e32 v12, v14, v130
	v_min_f32_e32 v12, 0x40e00000, v12
	v_mul_f32_e32 v13, 0xc01d265f, v12
	v_add_f32_e32 v9, 1.0, v9
	v_rcp_f32_e32 v9, v9
	v_exp_f32_e32 v13, v13
	v_mul_f32_e32 v10, v10, v8
	v_add_f32_e32 v8, v245, v133
	v_med3_f32 v8, v8, s46, v150
	v_fma_f32 v8, v8, 4.0, 4.0
	v_mul_f32_e32 v9, v11, v9
	v_mul_f32_e32 v9, v8, v9
	v_add_f32_e32 v8, 1.0, v13
	v_rcp_f32_e32 v8, v8
	v_add_f32_e32 v11, v246, v134
	v_med3_f32 v11, v11, s46, v150
	v_fma_f32 v11, v11, 4.0, 4.0
	v_mul_f32_e32 v8, v12, v8
	v_mul_f32_e32 v11, v11, v8
	v_add_f32_e32 v8, v247, v135
	v_med3_f32 v8, v8, s46, v150
	v_add_f32_e32 v4, v4, v120
	v_fma_f32 v14, v8, 4.0, 4.0
	v_mov_b32_e32 v8, v253
	v_min_f32_e32 v4, 0x40e00000, v4
	v_cvt_pk_fp8_f32 v8, v10, v9
	v_mul_f32_e32 v9, 0xc01d265f, v4
	v_exp_f32_e32 v9, v9
	v_add_f32_e32 v5, v5, v121
	v_min_f32_e32 v5, 0x40e00000, v5
	s_waitcnt vmcnt(14)
	v_add_f32_e32 v0, v0, v124
	v_add_f32_e32 v9, 1.0, v9
	v_rcp_f32_e32 v9, v9
	v_med3_f32 v0, v0, s46, v150
	v_fma_f32 v0, v0, 4.0, 4.0
	v_add_f32_e32 v6, v6, v122
	v_mul_f32_e32 v4, v4, v9
	v_mul_f32_e32 v9, 0xc01d265f, v5
	v_exp_f32_e32 v9, v9
	v_mul_f32_e32 v0, v0, v4
	v_min_f32_e32 v6, 0x40e00000, v6
	v_add_f32_e32 v1, v1, v125
	v_add_f32_e32 v4, 1.0, v9
	v_rcp_f32_e32 v4, v4
	v_mul_f32_e32 v9, 0xc01d265f, v6
	v_exp_f32_e32 v9, v9
	v_med3_f32 v1, v1, s46, v150
	v_fma_f32 v1, v1, 4.0, 4.0
	v_mul_f32_e32 v4, v5, v4
	v_mul_f32_e32 v1, v1, v4
	v_add_f32_e32 v4, 1.0, v9
	v_rcp_f32_e32 v4, v4
	v_add_f32_e32 v12, v15, v131
	v_add_f32_e32 v5, v7, v123
	v_min_f32_e32 v12, 0x40e00000, v12
	v_min_f32_e32 v5, 0x40e00000, v5
	v_mul_f32_e32 v13, 0xc01d265f, v12
	v_mul_f32_e32 v4, v6, v4
	v_mul_f32_e32 v6, 0xc01d265f, v5
	v_exp_f32_e32 v13, v13
	v_exp_f32_e32 v6, v6
	v_add_f32_e32 v2, v2, v126
	v_med3_f32 v2, v2, s46, v150
	v_fma_f32 v2, v2, 4.0, 4.0
	v_add_f32_e32 v13, 1.0, v13
	v_mul_f32_e32 v2, v2, v4
	v_add_f32_e32 v4, 1.0, v6
	v_rcp_f32_e32 v13, v13
	v_rcp_f32_e32 v4, v4
	v_mov_b32_e32 v9, v253
	v_add_f32_e32 v3, v3, v127
	v_cvt_pk_fp8_f32 v9, v0, v1
	v_med3_f32 v3, v3, s46, v150
	v_mul_f32_e32 v10, v12, v13
	v_fma_f32 v0, v3, 4.0, 4.0
	v_mul_f32_e32 v1, v5, v4
	v_mul_f32_e32 v10, v14, v10
	v_mul_f32_e32 v0, v0, v1
	v_cvt_pk_fp8_f32 v8, v11, v10 op_sel:[0,0,1]
	v_cvt_pk_fp8_f32 v9, v2, v0 op_sel:[0,0,1]
	v_lshlrev_b64 v[0:1], 11, v[252:253]
	v_lshl_add_u64 v[0:1], s[70:71], 0, v[0:1]
	v_lshl_add_u64 v[0:1], v[0:1], 0, v[146:147]
	global_store_dwordx2 v[0:1], v[8:9], off

; #define LDS_AS __attribute__((address_space(3)))
; #define OPAQUE_TID(P) (((P).wid0 << 6) | lane_id_now())
; #define P_STAGE_A(slot, half, kt) do { _Pragma("unroll") for (int _i = 0; _i < 2; ++_i) { const unsigned _m0 = ldsw + (unsigned)((slot) + _i * 8192); const unsigned _so = (unsigned)(kt) * 128u; \
;     asm volatile("s_mov_b32 m0, %0\n\ts_nop 4\n\tbuffer_load_dwordx4 %1, %2, %3 offen lds" :: "s"(_m0), "v"(voffA[half][_i]), "s"(rsA), "s"(_so) : "m0", "memory"); } } while (0)
;   DI unsigned bt_rowoff(int h, int R) const { return (unsigned)(pn * 256 + 128 * h + (pn < 15 ? tcol_adj(R) : tcol_p64(R))) * 4096u; }
;   DI unsigned a_bytes() const { return (unsigned)NTOK * 4096u; }
;   DI unsigned a_bytes() const { return (unsigned)NTOK * 1024u; }
; template <class Cfg>
; DI void f8dma_issue_prologue_st(LDS_AS unsigned char* lds, const Cfg& cfg) {
;   const int tid = OPAQUE_TID(cfg.p), wid = __builtin_amdgcn_readfirstlane(tid >> 6), lane = tid & 63;
;   const LDS_AS unsigned* stash = (const LDS_AS unsigned*)(lds + F8_STASH);
;   unsigned voffA[2][2], voffB0;
;   voffA[0][0] = stash[tid]; voffA[0][1] = stash[512 + tid]; voffA[1][0] = stash[1024 + tid]; voffA[1][1] = stash[1536 + tid];
;   {
;     const int r = 8 * wid + (lane >> 3);
;     const unsigned cofs = 16u * (((unsigned)lane & 7u) ^ (((unsigned)lane >> 3) & 7u));
;     voffB0 = cfg.bt_rowoff(0, r) + cofs;
;   }
;   const unsigned bt_half = cfg.bt_rowoff(1, 0) - cfg.bt_rowoff(0, 0), bt_piece = cfg.bt_rowoff(0, 64) - cfg.bt_rowoff(0, 0);
;   const __amdgpu_buffer_rsrc_t rsA = __builtin_amdgcn_make_buffer_rsrc((void*)cfg.a_base(), 0, cfg.a_bytes(), 0x00020000);
;   const __amdgpu_buffer_rsrc_t rsB = __builtin_amdgcn_make_buffer_rsrc((void*)cfg.bt_base(), 0, cfg.bt_bytes(), 0x00020000);
;   const unsigned ldsw = (unsigned)__builtin_amdgcn_readfirstlane((int)(unsigned)(size_t)lds) + (unsigned)wid * 1024u;
;     ...
;   P_STAGE_B(G_SB(0, 0), 0, 0); P_STAGE_A(G_SA(0, 0), 0, 0); P_STAGE_B(G_SB(0, 1), 1, 0); P_STAGE_A(G_SA(0, 1), 1, 0);
;   P_STAGE_B(G_SB(1, 0), 0, 1); P_STAGE_A(G_SA(1, 0), 0, 1); P_STAGE_B(G_SB(1, 1), 1, 1);
;   DI RowTok row_tok(int r) const {
;     const int rr = m0 + r; const unsigned long long pr = p.rowpair[e * 8192 + (rr < cnt ? rr : cnt - 1)];
;     RowTok t; t.a = rr < cnt ? (int)(unsigned)pr : -1; t.gt = __uint_as_float((unsigned)(pr >> 32)); return t;
;   }
.LBB0_1611:
	s_lshl_b32 s2, s21, 6
	v_mbcnt_lo_u32_b32 v128, -1, 0
	v_mbcnt_hi_u32_b32 v128, -1, v128
	s_add_i32 s2, s2, s47
	v_and_b32_e32 v68, 15, v128
	v_add_u32_e32 v144, s2, v68
	v_min_i32_e32 v68, s27, v144
	v_add_u32_e32 v173, 16, v144
	v_add_u32_e32 v172, 32, v144
	v_add_u32_e32 v171, 48, v144
	v_add_u32_e32 v68, s48, v68
	v_min_i32_e32 v70, s27, v173
	v_min_i32_e32 v72, s27, v172
	v_min_i32_e32 v74, s27, v171
	v_ashrrev_i32_e32 v69, 31, v68
	v_add_u32_e32 v70, s48, v70
	v_add_u32_e32 v72, s48, v72
	v_add_u32_e32 v74, s48, v74
	v_lshl_add_u64 v[68:69], v[68:69], 3, s[94:95]
	v_ashrrev_i32_e32 v71, 31, v70
	v_ashrrev_i32_e32 v73, 31, v72
	v_ashrrev_i32_e32 v75, 31, v74
	v_add_u32_e32 v170, 0x80, v144
	v_lshl_add_u64 v[70:71], v[70:71], 3, s[94:95]
	v_lshl_add_u64 v[72:73], v[72:73], 3, s[94:95]
	v_lshl_add_u64 v[74:75], v[74:75], 3, s[94:95]
	global_load_dwordx2 v[162:163], v[68:69], off
	global_load_dwordx2 v[160:161], v[70:71], off
	global_load_dwordx2 v[158:159], v[72:73], off
	global_load_dwordx2 v[156:157], v[74:75], off
	v_min_i32_e32 v68, s27, v170
	v_add_u32_e32 v169, 0x90, v144
	v_add_u32_e32 v168, 0xa0, v144
	v_add_u32_e32 v167, 0xb0, v144
	v_add_u32_e32 v68, s48, v68
	v_min_i32_e32 v70, s27, v169
	v_min_i32_e32 v72, s27, v168
	v_min_i32_e32 v74, s27, v167
	v_ashrrev_i32_e32 v69, 31, v68
	v_add_u32_e32 v70, s48, v70
	v_add_u32_e32 v72, s48, v72
	v_add_u32_e32 v74, s48, v74
	v_lshl_add_u64 v[68:69], v[68:69], 3, s[94:95]
	v_ashrrev_i32_e32 v71, 31, v70
	v_ashrrev_i32_e32 v73, 31, v72
	v_ashrrev_i32_e32 v75, 31, v74
	v_lshl_add_u64 v[70:71], v[70:71], 3, s[94:95]
	v_lshl_add_u64 v[72:73], v[72:73], 3, s[94:95]
	v_lshl_add_u64 v[74:75], v[74:75], 3, s[94:95]
	global_load_dwordx2 v[154:155], v[68:69], off
	global_load_dwordx2 v[152:153], v[70:71], off
	global_load_dwordx2 v[150:151], v[72:73], off
	global_load_dwordx2 v[146:147], v[74:75], off
	s_lshl_b32 s2, s15, 5
	v_ashrrev_i32_e32 v68, 1, v128
	v_and_b32_e32 v68, -8, v68
	s_or_b32 s2, s2, s20
	v_add_u32_e32 v148, s2, v68
	s_lshl_b32 s2, s14, 11
	v_readlane_b32 s60, v254, 6
	s_ashr_i32 s3, s2, 31
	v_readlane_b32 s66, v254, 12
	v_readlane_b32 s67, v254, 13
	s_lshl_b64 s[2:3], s[2:3], 2
	s_mov_b64 s[50:51], s[66:67]
	s_add_u32 s2, s50, s2
	s_addc_u32 s3, s51, s3
	v_ashrrev_i32_e32 v149, 31, v148
	v_lshl_add_u64 v[68:69], v[148:149], 2, s[2:3]
	global_load_dwordx4 v[136:139], v[68:69], off offset:16
	global_load_dwordx4 v[140:143], v[68:69], off
	global_load_dwordx4 v[128:131], v[68:69], off offset:528
	global_load_dwordx4 v[132:135], v[68:69], off offset:512
	s_and_b64 vcc, exec, s[100:101]
	s_cbranch_vccnz .Lpfm2_none
	v_mbcnt_lo_u32_b32 v72, -1, 0
	v_mbcnt_hi_u32_b32 v72, -1, v72
	s_ashr_i32 s13, s12, 31
	v_or_b32_e32 v68, s87, v72
	v_bfe_u32 v74, v72, 3, 3
	v_readfirstlane_b32 s2, v68
	s_ashr_i32 s38, s2, 6
	s_lshl_b32 s2, s38, 3
	v_lshrrev_b32_e32 v73, 3, v72
	v_or_b32_e32 v75, s2, v74
	v_xor_b32_e32 v72, v73, v72
	s_lshl_b32 s3, s38, 1
	v_lshlrev_b32_e32 v73, 1, v75
	v_mov_b32_e32 v75, 0x63
	s_and_b32 s3, s3, 4
	v_and_b32_e32 v73, 24, v73
	v_bitop3_b32 v74, s2, v75, v74 bitop3:0xc8
	v_lshlrev_b32_e32 v72, 4, v72
	v_or3_b32 v73, s3, v74, v73
	v_and_b32_e32 v72, 0x70, v72
	s_lshl_b32 s2, s44, 19
	v_lshlrev_b32_e32 v73, 11, v73
	v_or3_b32 v72, v73, s2, v72
	s_lshl_b64 s[2:3], s[12:13], 22
	v_lshl_add_u32 v68, v68, 2, 0
	s_add_u32 s4, s52, s2
	v_add_u32_e32 v70, 0x22410, v68
	s_addc_u32 s2, s53, s3
	ds_read2st64_b32 v[68:69], v70 offset1:8
	ds_read2st64_b32 v[70:71], v70 offset0:16 offset1:24
	s_and_b32 s5, s2, 0xffff
	s_lshl_b32 s2, s38, 10
	s_add_i32 s2, s2, 0
	s_add_i32 s3, s2, 0x10010
	s_mov_b32 m0, s3
	s_nop 0
	buffer_load_dwordx4 v72, s[4:7], s31 offen lds
	s_add_i32 s3, s2, 0x12010
	s_mov_b32 m0, s3
	s_nop 0
	buffer_load_dwordx4 v72, s[4:7], s7 offen lds
	s_add_i32 s3, s2, 16
	s_waitcnt lgkmcnt(1)
	s_mov_b32 m0, s3
	s_nop 0
	buffer_load_dwordx4 v68, s[8:11], s31 offen lds
	s_add_i32 s3, s2, 0x2010
	s_mov_b32 m0, s3
	s_nop 0
	buffer_load_dwordx4 v69, s[8:11], s31 offen lds
	s_add_i32 s3, s2, 0x14010
	s_mov_b32 m0, s3
	s_nop 0
	buffer_load_dwordx4 v72, s[4:7], s34 offen lds
	s_add_i32 s3, s2, 0x16010
	s_mov_b32 m0, s3
	s_nop 0
	buffer_load_dwordx4 v72, s[4:7], s35 offen lds
	s_add_i32 s3, s2, 0x4010
	s_waitcnt lgkmcnt(0)
	s_mov_b32 m0, s3
	s_nop 0
	buffer_load_dwordx4 v70, s[8:11], s31 offen lds
	s_add_i32 s3, s2, 0x6010
	s_mov_b32 m0, s3
	s_nop 0
	buffer_load_dwordx4 v71, s[8:11], s31 offen lds
	s_add_i32 s3, s2, 0x18010
	s_mov_b32 m0, s3
	s_nop 0
	buffer_load_dwordx4 v72, s[4:7], s33 offen lds
	s_add_i32 s3, s2, 0x1a010
	s_mov_b32 m0, s3
	s_nop 0
	buffer_load_dwordx4 v72, s[4:7], s36 offen lds
	s_add_i32 s3, s2, 0x8010
	s_mov_b32 m0, s3
	s_nop 0
	buffer_load_dwordx4 v68, s[8:11], s33 offen lds
	s_add_i32 s3, s2, 0xa010
	s_mov_b32 m0, s3
	s_nop 0
	buffer_load_dwordx4 v69, s[8:11], s33 offen lds
	s_add_i32 s3, s2, 0x1c010
	s_mov_b32 m0, s3
	s_nop 0
	buffer_load_dwordx4 v72, s[4:7], s37 offen lds
	s_add_i32 s2, s2, 0x1e010
	s_mov_b32 m0, s2
	s_nop 0
	buffer_load_dwordx4 v72, s[4:7], s42 offen lds
	s_branch .Lpfm2_done

;   DI void epi_t(const RowTok& t, const ColCtx& c, const f32x4& v0, const f32x4& v1) const {
;     if (t.a < 0) return;
;     const f32x4 x0 = (v0 + c.b0) * t.gt, x1 = (v1 + c.b1) * t.gt;
;     u32x4 pk; pk.x = pack2(x0[0], x0[1]); pk.y = pack2(x0[2], x0[3]); pk.z = pack2(x1[0], x1[1]); pk.w = pack2(x1[2], x1[3]);
;     *(u32x4*)(p.yb + (size_t)t.a * 2048 + c.gc) = pk;
;   }
.Lpfm2_done:
	v_cmp_gt_i32_e32 vcc, s43, v144
	v_readlane_b32 s61, v254, 7
	v_readlane_b32 s62, v254, 8
	v_readlane_b32 s63, v254, 9
	v_readlane_b32 s64, v254, 10
	v_readlane_b32 s65, v254, 11
	s_waitcnt vmcnt(25)
	v_cndmask_b32_e32 v252, -1, v162, vcc
	v_cmp_lt_i32_e32 vcc, -1, v252
	s_and_saveexec_b64 s[2:3], vcc
	s_cbranch_execz .LBB0_1613
	s_waitcnt vmcnt(16)
	v_pk_add_f32 v[68:69], v[126:127], v[142:143]
	v_pk_add_f32 v[70:71], v[124:125], v[140:141]
	v_lshlrev_b64 v[72:73], 12, v[252:253]
	v_pk_mul_f32 v[74:75], v[162:163], v[68:69] op_sel:[1,0]
	v_pk_mul_f32 v[68:69], v[162:163], v[70:71] op_sel:[1,0]
	v_pk_add_f32 v[70:71], v[122:123], v[138:139]
	v_pk_add_f32 v[120:121], v[120:121], v[136:137]
	v_pk_mul_f32 v[122:123], v[162:163], v[70:71] op_sel:[1,0]
	v_pk_mul_f32 v[70:71], v[162:163], v[120:121] op_sel:[1,0]
	v_lshl_add_u64 v[72:73], s[40:41], 0, v[72:73]
	v_cvt_pk_bf16_f32 v68, v68, v69
	v_cvt_pk_bf16_f32 v69, v74, v75
	v_cvt_pk_bf16_f32 v70, v70, v71
	v_cvt_pk_bf16_f32 v71, v122, v123
	v_lshl_add_u64 v[72:73], v[148:149], 1, v[72:73]
	global_store_dwordx4 v[72:73], v[68:71], off
	s_waitcnt vmcnt(16)
	v_pk_add_f32 v[112:113], v[112:113], v[128:129]
	s_waitcnt vmcnt(15)
	v_pk_add_f32 v[68:69], v[118:119], v[134:135]
	v_pk_add_f32 v[70:71], v[116:117], v[132:133]
	v_pk_mul_f32 v[74:75], v[162:163], v[68:69] op_sel:[1,0]
	v_pk_mul_f32 v[68:69], v[162:163], v[70:71] op_sel:[1,0]
	v_pk_add_f32 v[70:71], v[114:115], v[130:131]
	v_cvt_pk_bf16_f32 v68, v68, v69
	v_pk_mul_f32 v[114:115], v[162:163], v[70:71] op_sel:[1,0]
	v_pk_mul_f32 v[70:71], v[162:163], v[112:113] op_sel:[1,0]
	v_cvt_pk_bf16_f32 v69, v74, v75
	v_cvt_pk_bf16_f32 v70, v70, v71
	v_cvt_pk_bf16_f32 v71, v114, v115
	global_store_dwordx4 v[72:73], v[68:71], off offset:256
.LBB0_1613:
	s_or_b64 exec, exec, s[2:3]
	v_cmp_gt_i32_e32 vcc, s43, v173
	s_waitcnt vmcnt(24)
	s_nop 0
	v_cndmask_b32_e32 v252, -1, v160, vcc
	v_cmp_lt_i32_e32 vcc, -1, v252
	s_and_saveexec_b64 s[2:3], vcc
	s_cbranch_execz .LBB0_1615
	s_waitcnt vmcnt(16)
	v_pk_add_f32 v[68:69], v[110:111], v[142:143]
	v_pk_add_f32 v[70:71], v[108:109], v[140:141]
	v_lshlrev_b64 v[72:73], 12, v[252:253]
	v_pk_mul_f32 v[74:75], v[160:161], v[68:69] op_sel:[1,0]
	v_pk_mul_f32 v[68:69], v[160:161], v[70:71] op_sel:[1,0]
	v_pk_add_f32 v[70:71], v[102:103], v[138:139]
	v_pk_add_f32 v[100:101], v[100:101], v[136:137]
	v_pk_mul_f32 v[102:103], v[160:161], v[70:71] op_sel:[1,0]
	v_pk_mul_f32 v[70:71], v[160:161], v[100:101] op_sel:[1,0]
	v_lshl_add_u64 v[72:73], s[40:41], 0, v[72:73]
	v_cvt_pk_bf16_f32 v68, v68, v69
	v_cvt_pk_bf16_f32 v69, v74, v75
	v_cvt_pk_bf16_f32 v70, v70, v71
	v_cvt_pk_bf16_f32 v71, v102, v103
	v_lshl_add_u64 v[72:73], v[148:149], 1, v[72:73]
	global_store_dwordx4 v[72:73], v[68:71], off
	s_waitcnt vmcnt(16)
	v_pk_add_f32 v[96:97], v[96:97], v[128:129]
	s_waitcnt vmcnt(15)
	v_pk_add_f32 v[68:69], v[106:107], v[134:135]
	v_pk_add_f32 v[70:71], v[104:105], v[132:133]
	v_pk_mul_f32 v[74:75], v[160:161], v[68:69] op_sel:[1,0]
	v_pk_mul_f32 v[68:69], v[160:161], v[70:71] op_sel:[1,0]
	v_pk_add_f32 v[70:71], v[98:99], v[130:131]
	v_cvt_pk_bf16_f32 v68, v68, v69
	v_pk_mul_f32 v[98:99], v[160:161], v[70:71] op_sel:[1,0]
	v_pk_mul_f32 v[70:71], v[160:161], v[96:97] op_sel:[1,0]
	v_cvt_pk_bf16_f32 v69, v74, v75
	v_cvt_pk_bf16_f32 v70, v70, v71
	v_cvt_pk_bf16_f32 v71, v98, v99
	global_store_dwordx4 v[72:73], v[68:71], off offset:256
.LBB0_1615:
	s_or_b64 exec, exec, s[2:3]
	v_cmp_gt_i32_e32 vcc, s43, v172
	s_waitcnt vmcnt(23)
	s_nop 0
	v_cndmask_b32_e32 v252, -1, v158, vcc
	v_cmp_lt_i32_e32 vcc, -1, v252
	s_and_saveexec_b64 s[2:3], vcc
	s_cbranch_execz .LBB0_1617
	s_waitcnt vmcnt(16)
	v_pk_add_f32 v[68:69], v[86:87], v[142:143]
	v_pk_add_f32 v[70:71], v[84:85], v[140:141]
	v_lshlrev_b64 v[72:73], 12, v[252:253]
	v_pk_mul_f32 v[74:75], v[158:159], v[68:69] op_sel:[1,0]
	v_pk_mul_f32 v[68:69], v[158:159], v[70:71] op_sel:[1,0]
	v_pk_add_f32 v[70:71], v[82:83], v[138:139]
	v_pk_add_f32 v[80:81], v[80:81], v[136:137]
	v_pk_mul_f32 v[82:83], v[158:159], v[70:71] op_sel:[1,0]
	v_pk_mul_f32 v[70:71], v[158:159], v[80:81] op_sel:[1,0]
	v_lshl_add_u64 v[72:73], s[40:41], 0, v[72:73]
	v_cvt_pk_bf16_f32 v68, v68, v69
	v_cvt_pk_bf16_f32 v69, v74, v75
	v_cvt_pk_bf16_f32 v70, v70, v71
	v_cvt_pk_bf16_f32 v71, v82, v83
	v_lshl_add_u64 v[72:73], v[148:149], 1, v[72:73]
	global_store_dwordx4 v[72:73], v[68:71], off
	s_waitcnt vmcnt(16)
	v_pk_add_f32 v[80:81], v[88:89], v[128:129]
	s_waitcnt vmcnt(15)
	v_pk_add_f32 v[68:69], v[94:95], v[134:135]
	v_pk_add_f32 v[70:71], v[92:93], v[132:133]
	v_pk_mul_f32 v[74:75], v[158:159], v[68:69] op_sel:[1,0]
	v_pk_mul_f32 v[68:69], v[158:159], v[70:71] op_sel:[1,0]
	v_pk_add_f32 v[70:71], v[90:91], v[130:131]
	v_cvt_pk_bf16_f32 v68, v68, v69
	v_pk_mul_f32 v[82:83], v[158:159], v[70:71] op_sel:[1,0]
	v_pk_mul_f32 v[70:71], v[158:159], v[80:81] op_sel:[1,0]
	v_cvt_pk_bf16_f32 v69, v74, v75
	v_cvt_pk_bf16_f32 v70, v70, v71
	v_cvt_pk_bf16_f32 v71, v82, v83
	global_store_dwordx4 v[72:73], v[68:71], off offset:256
;   DI void epi_t(const RowTok& t, const ColCtx& c, const f32x4& v0, const f32x4& v1) const {
;     if (t.a < 0) return;
;     const f32x4 x0 = (v0 + c.b0) * t.gt, x1 = (v1 + c.b1) * t.gt;
;     u32x4 pk; pk.x = pack2(x0[0], x0[1]); pk.y = pack2(x0[2], x0[3]); pk.z = pack2(x1[0], x1[1]); pk.w = pack2(x1[2], x1[3]);
;     *(u32x4*)(p.yb + (size_t)t.a * 2048 + c.gc) = pk;
;   }
.LBB0_1617:
	s_or_b64 exec, exec, s[2:3]
	v_cmp_gt_i32_e32 vcc, s43, v171
	s_waitcnt vmcnt(22)
	s_nop 0
	v_cndmask_b32_e32 v252, -1, v156, vcc
	v_cmp_lt_i32_e32 vcc, -1, v252
	s_and_saveexec_b64 s[2:3], vcc
	s_cbranch_execz .LBB0_1619
	v_lshlrev_b64 v[68:69], 12, v[252:253]
	s_waitcnt vmcnt(16)
	v_pk_add_f32 v[70:71], v[218:219], v[142:143]
	v_pk_add_f32 v[72:73], v[216:217], v[140:141]
	v_pk_add_f32 v[50:51], v[50:51], v[138:139]
	v_pk_add_f32 v[48:49], v[48:49], v[136:137]
	v_pk_mul_f32 v[70:71], v[156:157], v[70:71] op_sel:[1,0]
	v_pk_mul_f32 v[72:73], v[156:157], v[72:73] op_sel:[1,0]
	v_pk_mul_f32 v[74:75], v[156:157], v[50:51] op_sel:[1,0]
	v_pk_mul_f32 v[50:51], v[156:157], v[48:49] op_sel:[1,0]
	v_lshl_add_u64 v[68:69], s[40:41], 0, v[68:69]
	v_cvt_pk_bf16_f32 v48, v72, v73
	v_cvt_pk_bf16_f32 v49, v70, v71
	v_cvt_pk_bf16_f32 v50, v50, v51
	v_cvt_pk_bf16_f32 v51, v74, v75
	v_lshl_add_u64 v[68:69], v[148:149], 1, v[68:69]
	global_store_dwordx4 v[68:69], v[48:51], off
	s_waitcnt vmcnt(16)
	v_pk_add_f32 v[18:19], v[18:19], v[130:131]
	v_pk_add_f32 v[16:17], v[16:17], v[128:129]
	s_waitcnt vmcnt(15)
	v_pk_add_f32 v[48:49], v[78:79], v[134:135]
	v_pk_add_f32 v[50:51], v[76:77], v[132:133]
	v_pk_mul_f32 v[48:49], v[156:157], v[48:49] op_sel:[1,0]
	v_pk_mul_f32 v[50:51], v[156:157], v[50:51] op_sel:[1,0]
	v_pk_mul_f32 v[70:71], v[156:157], v[18:19] op_sel:[1,0]
	v_pk_mul_f32 v[18:19], v[156:157], v[16:17] op_sel:[1,0]
	v_cvt_pk_bf16_f32 v16, v50, v51
	v_cvt_pk_bf16_f32 v17, v48, v49
	v_cvt_pk_bf16_f32 v18, v18, v19
	v_cvt_pk_bf16_f32 v19, v70, v71
	global_store_dwordx4 v[68:69], v[16:19], off offset:256
.LBB0_1619:
	s_or_b64 exec, exec, s[2:3]
	v_cmp_gt_i32_e32 vcc, s43, v170
	s_waitcnt vmcnt(21)
	s_nop 0
	v_cndmask_b32_e32 v252, -1, v154, vcc
	v_cmp_lt_i32_e32 vcc, -1, v252
	s_and_saveexec_b64 s[2:3], vcc
	s_cbranch_execz .LBB0_1621
	s_waitcnt vmcnt(16)
	v_pk_add_f32 v[16:17], v[58:59], v[142:143]
	v_pk_add_f32 v[18:19], v[56:57], v[140:141]
	v_lshlrev_b64 v[48:49], 12, v[252:253]
	v_pk_mul_f32 v[50:51], v[154:155], v[16:17] op_sel:[1,0]
	v_pk_mul_f32 v[16:17], v[154:155], v[18:19] op_sel:[1,0]
	v_pk_add_f32 v[18:19], v[54:55], v[138:139]
	v_pk_add_f32 v[52:53], v[52:53], v[136:137]
	v_pk_mul_f32 v[54:55], v[154:155], v[18:19] op_sel:[1,0]
	v_pk_mul_f32 v[18:19], v[154:155], v[52:53] op_sel:[1,0]
	v_lshl_add_u64 v[48:49], s[40:41], 0, v[48:49]
	v_cvt_pk_bf16_f32 v16, v16, v17
	v_cvt_pk_bf16_f32 v17, v50, v51
	v_cvt_pk_bf16_f32 v18, v18, v19
	v_cvt_pk_bf16_f32 v19, v54, v55
	v_lshl_add_u64 v[48:49], v[148:149], 1, v[48:49]
	global_store_dwordx4 v[48:49], v[16:19], off
	s_waitcnt vmcnt(16)
	v_pk_add_f32 v[52:53], v[60:61], v[128:129]
	s_waitcnt vmcnt(15)
	v_pk_add_f32 v[16:17], v[66:67], v[134:135]
	v_pk_add_f32 v[18:19], v[64:65], v[132:133]
	v_pk_mul_f32 v[50:51], v[154:155], v[16:17] op_sel:[1,0]
	v_pk_mul_f32 v[16:17], v[154:155], v[18:19] op_sel:[1,0]
	v_pk_add_f32 v[18:19], v[62:63], v[130:131]
	v_cvt_pk_bf16_f32 v16, v16, v17
	v_pk_mul_f32 v[54:55], v[154:155], v[18:19] op_sel:[1,0]
	v_pk_mul_f32 v[18:19], v[154:155], v[52:53] op_sel:[1,0]
	v_cvt_pk_bf16_f32 v17, v50, v51
	v_cvt_pk_bf16_f32 v18, v18, v19
	v_cvt_pk_bf16_f32 v19, v54, v55
	global_store_dwordx4 v[48:49], v[16:19], off offset:256
;   DI void epi_t(const RowTok& t, const ColCtx& c, const f32x4& v0, const f32x4& v1) const {
;     if (t.a < 0) return;
;     const f32x4 x0 = (v0 + c.b0) * t.gt, x1 = (v1 + c.b1) * t.gt;
;     u32x4 pk; pk.x = pack2(x0[0], x0[1]); pk.y = pack2(x0[2], x0[3]); pk.z = pack2(x1[0], x1[1]); pk.w = pack2(x1[2], x1[3]);
;     *(u32x4*)(p.yb + (size_t)t.a * 2048 + c.gc) = pk;
;   }
.LBB0_1621:
	s_or_b64 exec, exec, s[2:3]
	v_cmp_gt_i32_e32 vcc, s43, v169
	s_waitcnt vmcnt(20)
	s_nop 0
	v_cndmask_b32_e32 v252, -1, v152, vcc
	v_cmp_lt_i32_e32 vcc, -1, v252
	s_and_saveexec_b64 s[2:3], vcc
	s_cbranch_execz .LBB0_1623
	s_waitcnt vmcnt(16)
	v_pk_add_f32 v[16:17], v[38:39], v[142:143]
	v_pk_add_f32 v[18:19], v[36:37], v[140:141]
	v_lshlrev_b64 v[48:49], 12, v[252:253]
	v_pk_mul_f32 v[36:37], v[16:17], v[152:153] op_sel:[0,1]
	v_pk_mul_f32 v[16:17], v[18:19], v[152:153] op_sel:[0,1]
	v_pk_add_f32 v[18:19], v[34:35], v[138:139]
	v_pk_add_f32 v[32:33], v[32:33], v[136:137]
	v_pk_mul_f32 v[34:35], v[152:153], v[18:19] op_sel:[1,0]
	v_pk_mul_f32 v[18:19], v[152:153], v[32:33] op_sel:[1,0]
	v_lshl_add_u64 v[32:33], s[40:41], 0, v[48:49]
	v_cvt_pk_bf16_f32 v16, v16, v17
	v_cvt_pk_bf16_f32 v17, v36, v37
	v_cvt_pk_bf16_f32 v18, v18, v19
	v_cvt_pk_bf16_f32 v19, v34, v35
	v_lshl_add_u64 v[32:33], v[148:149], 1, v[32:33]
	global_store_dwordx4 v[32:33], v[16:19], off
	s_waitcnt vmcnt(16)
	v_pk_add_f32 v[36:37], v[40:41], v[128:129]
	s_waitcnt vmcnt(15)
	v_pk_add_f32 v[16:17], v[46:47], v[134:135]
	v_pk_add_f32 v[18:19], v[44:45], v[132:133]
	v_pk_mul_f32 v[34:35], v[152:153], v[16:17] op_sel:[1,0]
	v_pk_mul_f32 v[16:17], v[152:153], v[18:19] op_sel:[1,0]
	v_pk_add_f32 v[18:19], v[42:43], v[130:131]
	v_cvt_pk_bf16_f32 v16, v16, v17
	v_pk_mul_f32 v[38:39], v[152:153], v[18:19] op_sel:[1,0]
	v_pk_mul_f32 v[18:19], v[152:153], v[36:37] op_sel:[1,0]
	v_cvt_pk_bf16_f32 v17, v34, v35
	v_cvt_pk_bf16_f32 v18, v18, v19
	v_cvt_pk_bf16_f32 v19, v38, v39
	global_store_dwordx4 v[32:33], v[16:19], off offset:256
.LBB0_1623:
	s_or_b64 exec, exec, s[2:3]
	v_cmp_gt_i32_e32 vcc, s43, v168
	s_waitcnt vmcnt(19)
	s_nop 0
	v_cndmask_b32_e32 v252, -1, v150, vcc
	v_cmp_lt_i32_e32 vcc, -1, v252
	s_and_saveexec_b64 s[2:3], vcc
	s_cbranch_execz .LBB0_1625
	s_waitcnt vmcnt(16)
	v_pk_add_f32 v[16:17], v[22:23], v[142:143]
	v_pk_add_f32 v[18:19], v[20:21], v[140:141]
	v_lshlrev_b64 v[32:33], 12, v[252:253]
	v_pk_mul_f32 v[20:21], v[16:17], v[150:151] op_sel:[0,1]
	v_pk_mul_f32 v[16:17], v[18:19], v[150:151] op_sel:[0,1]
	v_pk_add_f32 v[18:19], v[226:227], v[138:139]
	v_pk_add_f32 v[22:23], v[224:225], v[136:137]
	v_pk_mul_f32 v[34:35], v[18:19], v[150:151] op_sel:[0,1]
	v_pk_mul_f32 v[18:19], v[22:23], v[150:151] op_sel:[0,1]
	v_cvt_pk_bf16_f32 v16, v16, v17
	v_cvt_pk_bf16_f32 v17, v20, v21
	v_lshl_add_u64 v[20:21], s[40:41], 0, v[32:33]
	v_cvt_pk_bf16_f32 v18, v18, v19
	v_cvt_pk_bf16_f32 v19, v34, v35
	v_lshl_add_u64 v[20:21], v[148:149], 1, v[20:21]
	global_store_dwordx4 v[20:21], v[16:19], off
	s_waitcnt vmcnt(16)
	v_pk_add_f32 v[24:25], v[24:25], v[128:129]
	s_waitcnt vmcnt(15)
	v_pk_add_f32 v[16:17], v[30:31], v[134:135]
	v_pk_add_f32 v[18:19], v[28:29], v[132:133]
	v_pk_mul_f32 v[22:23], v[150:151], v[16:17] op_sel:[1,0]
	v_pk_mul_f32 v[16:17], v[150:151], v[18:19] op_sel:[1,0]
	v_pk_add_f32 v[18:19], v[26:27], v[130:131]
	v_cvt_pk_bf16_f32 v16, v16, v17
	v_pk_mul_f32 v[26:27], v[150:151], v[18:19] op_sel:[1,0]
	v_pk_mul_f32 v[18:19], v[150:151], v[24:25] op_sel:[1,0]
	v_cvt_pk_bf16_f32 v17, v22, v23
	v_cvt_pk_bf16_f32 v18, v18, v19
	v_cvt_pk_bf16_f32 v19, v26, v27
	global_store_dwordx4 v[20:21], v[16:19], off offset:256
.LBB0_1625:
	s_or_b64 exec, exec, s[2:3]
	v_cmp_gt_i32_e32 vcc, s43, v167
	s_waitcnt vmcnt(18)
	s_nop 0
	v_cndmask_b32_e32 v252, -1, v146, vcc
	v_cmp_lt_i32_e32 vcc, -1, v252
	s_and_saveexec_b64 s[2:3], vcc
	s_cbranch_execz .LBB0_1627
	s_waitcnt vmcnt(16)
	v_pk_add_f32 v[4:5], v[4:5], v[140:141]
	v_lshlrev_b64 v[16:17], 12, v[252:253]
	v_pk_add_f32 v[6:7], v[6:7], v[142:143]
	v_pk_mul_f32 v[4:5], v[4:5], v[146:147] op_sel:[0,1]
	v_pk_add_f32 v[2:3], v[2:3], v[138:139]
	v_pk_add_f32 v[0:1], v[0:1], v[136:137]
	v_pk_mul_f32 v[6:7], v[6:7], v[146:147] op_sel:[0,1]
	v_pk_mul_f32 v[18:19], v[2:3], v[146:147] op_sel:[0,1]
	v_pk_mul_f32 v[2:3], v[0:1], v[146:147] op_sel:[0,1]
	v_cvt_pk_bf16_f32 v0, v4, v5
	v_lshl_add_u64 v[4:5], s[40:41], 0, v[16:17]
	v_cvt_pk_bf16_f32 v1, v6, v7
	v_cvt_pk_bf16_f32 v2, v2, v3
	v_cvt_pk_bf16_f32 v3, v18, v19
	v_lshl_add_u64 v[4:5], v[148:149], 1, v[4:5]
	global_store_dwordx4 v[4:5], v[0:3], off
	s_waitcnt vmcnt(16)
	v_pk_add_f32 v[8:9], v[8:9], v[128:129]
	s_waitcnt vmcnt(15)
	v_pk_add_f32 v[0:1], v[14:15], v[134:135]
	v_pk_add_f32 v[2:3], v[12:13], v[132:133]
	v_pk_mul_f32 v[6:7], v[0:1], v[146:147] op_sel:[0,1]
	v_pk_mul_f32 v[0:1], v[2:3], v[146:147] op_sel:[0,1]
	v_pk_add_f32 v[2:3], v[10:11], v[130:131]
	v_cvt_pk_bf16_f32 v0, v0, v1
	v_pk_mul_f32 v[10:11], v[146:147], v[2:3] op_sel:[1,0]
	v_pk_mul_f32 v[2:3], v[146:147], v[8:9] op_sel:[1,0]
	v_cvt_pk_bf16_f32 v1, v6, v7
	v_cvt_pk_bf16_f32 v2, v2, v3
	v_cvt_pk_bf16_f32 v3, v10, v11
	global_store_dwordx4 v[4:5], v[0:3], off offset:256

; #define LDS_AS __attribute__((address_space(3)))
; #define OPAQUE_TID(P) (((P).wid0 << 6) | lane_id_now())
; #define P_STAGE_A(slot, half, kt) do { _Pragma("unroll") for (int _i = 0; _i < 2; ++_i) { const unsigned _m0 = ldsw + (unsigned)((slot) + _i * 8192); const unsigned _so = (unsigned)(kt) * 128u; \
;     asm volatile("s_mov_b32 m0, %0\n\ts_nop 4\n\tbuffer_load_dwordx4 %1, %2, %3 offen lds" :: "s"(_m0), "v"(voffA[half][_i]), "s"(rsA), "s"(_so) : "m0", "memory"); } } while (0)
;   DI unsigned bt_rowoff(int h, int R) const { return (unsigned)(pn * 256 + 128 * h + (pn < 15 ? tcol_adj(R) : tcol_p64(R))) * 4096u; }
;   DI unsigned a_bytes() const { return (unsigned)NTOK * 4096u; }
;   DI unsigned a_bytes() const { return (unsigned)NTOK * 1024u; }
; template <class Cfg>
; DI void f8dma_issue_prologue_st(LDS_AS unsigned char* lds, const Cfg& cfg) {
;   const int tid = OPAQUE_TID(cfg.p), wid = __builtin_amdgcn_readfirstlane(tid >> 6), lane = tid & 63;
;   const LDS_AS unsigned* stash = (const LDS_AS unsigned*)(lds + F8_STASH);
;   unsigned voffA[2][2], voffB0;
;   voffA[0][0] = stash[tid]; voffA[0][1] = stash[512 + tid]; voffA[1][0] = stash[1024 + tid]; voffA[1][1] = stash[1536 + tid];
;   {
;     const int r = 8 * wid + (lane >> 3);
;     const unsigned cofs = 16u * (((unsigned)lane & 7u) ^ (((unsigned)lane >> 3) & 7u));
;     voffB0 = cfg.bt_rowoff(0, r) + cofs;
;   }
;   const unsigned bt_half = cfg.bt_rowoff(1, 0) - cfg.bt_rowoff(0, 0), bt_piece = cfg.bt_rowoff(0, 64) - cfg.bt_rowoff(0, 0);
;   const __amdgpu_buffer_rsrc_t rsA = __builtin_amdgcn_make_buffer_rsrc((void*)cfg.a_base(), 0, cfg.a_bytes(), 0x00020000);
;   const __amdgpu_buffer_rsrc_t rsB = __builtin_amdgcn_make_buffer_rsrc((void*)cfg.bt_base(), 0, cfg.bt_bytes(), 0x00020000);
;   const unsigned ldsw = (unsigned)__builtin_amdgcn_readfirstlane((int)(unsigned)(size_t)lds) + (unsigned)wid * 1024u;
;     ...
;   P_STAGE_B(G_SB(0, 0), 0, 0); P_STAGE_A(G_SA(0, 0), 0, 0); P_STAGE_B(G_SB(0, 1), 1, 0); P_STAGE_A(G_SA(0, 1), 1, 0);
;   P_STAGE_B(G_SB(1, 0), 0, 1); P_STAGE_A(G_SA(1, 0), 0, 1); P_STAGE_B(G_SB(1, 1), 1, 1);
;   DI RowTok row_tok(int r) const {
;     const int rr = m0 + r; const unsigned long long pr = p.rowpair[e * 8192 + (rr < cnt ? rr : cnt - 1)];
;     RowTok t; t.a = rr < cnt ? (int)(unsigned)pr : -1; t.gt = __uint_as_float((unsigned)(pr >> 32)); return t;
;   }
.LBB0_1679:
	s_lshl_b32 s4, s23, 6
	v_mbcnt_lo_u32_b32 v132, -1, 0
	v_mbcnt_hi_u32_b32 v132, -1, v132
	s_add_i32 s4, s4, s47
	v_and_b32_e32 v68, 15, v132
	v_add_u32_e32 v144, s4, v68
	s_add_i32 s4, s43, -1
	s_lshl_b32 s5, s14, 13
	v_min_i32_e32 v68, s4, v144
	v_add_u32_e32 v173, 16, v144
	v_add_u32_e32 v172, 32, v144
	v_add_u32_e32 v171, 48, v144
	v_add_u32_e32 v68, s5, v68
	v_min_i32_e32 v70, s4, v173
	v_min_i32_e32 v128, s4, v172
	v_min_i32_e32 v130, s4, v171
	v_ashrrev_i32_e32 v69, 31, v68
	v_add_u32_e32 v70, s5, v70
	v_add_u32_e32 v128, s5, v128
	v_add_u32_e32 v130, s5, v130
	v_lshl_add_u64 v[68:69], v[68:69], 3, s[94:95]
	v_ashrrev_i32_e32 v71, 31, v70
	v_ashrrev_i32_e32 v129, 31, v128
	v_ashrrev_i32_e32 v131, 31, v130
	v_add_u32_e32 v170, 0x80, v144
	v_lshl_add_u64 v[70:71], v[70:71], 3, s[94:95]
	v_lshl_add_u64 v[128:129], v[128:129], 3, s[94:95]
	v_lshl_add_u64 v[130:131], v[130:131], 3, s[94:95]
	global_load_dwordx2 v[162:163], v[68:69], off
	global_load_dwordx2 v[160:161], v[70:71], off
	global_load_dwordx2 v[158:159], v[128:129], off
	global_load_dwordx2 v[156:157], v[130:131], off
	v_min_i32_e32 v68, s4, v170
	v_add_u32_e32 v169, 0x90, v144
	v_add_u32_e32 v168, 0xa0, v144
	v_add_u32_e32 v167, 0xb0, v144
	v_add_u32_e32 v68, s5, v68
	v_min_i32_e32 v70, s4, v169
	v_min_i32_e32 v128, s4, v168
	v_min_i32_e32 v130, s4, v167
	v_ashrrev_i32_e32 v69, 31, v68
	v_add_u32_e32 v70, s5, v70
	v_add_u32_e32 v128, s5, v128
	v_add_u32_e32 v130, s5, v130
	v_lshl_add_u64 v[68:69], v[68:69], 3, s[94:95]
	v_ashrrev_i32_e32 v71, 31, v70
	v_ashrrev_i32_e32 v129, 31, v128
	v_ashrrev_i32_e32 v131, 31, v130
	v_lshl_add_u64 v[70:71], v[70:71], 3, s[94:95]
	v_lshl_add_u64 v[128:129], v[128:129], 3, s[94:95]
	v_lshl_add_u64 v[130:131], v[130:131], 3, s[94:95]
	global_load_dwordx2 v[154:155], v[68:69], off
	global_load_dwordx2 v[152:153], v[70:71], off
	global_load_dwordx2 v[150:151], v[128:129], off
	global_load_dwordx2 v[146:147], v[130:131], off
	s_lshl_b32 s4, s22, 5
	v_ashrrev_i32_e32 v68, 1, v132
	v_and_b32_e32 v68, -8, v68
	s_or_b32 s4, s4, s48
	v_add_u32_e32 v148, s4, v68
	s_lshl_b32 s4, s14, 11
	v_readlane_b32 s60, v254, 6
	s_ashr_i32 s5, s4, 31
	v_readlane_b32 s66, v254, 12
	v_readlane_b32 s67, v254, 13
	s_lshl_b64 s[4:5], s[4:5], 2
	s_mov_b64 s[22:23], s[66:67]
	s_add_u32 s4, s22, s4
	s_addc_u32 s5, s23, s5
	v_ashrrev_i32_e32 v149, 31, v148
	v_lshl_add_u64 v[68:69], v[148:149], 2, s[4:5]
	global_load_dwordx4 v[136:139], v[68:69], off offset:16
	global_load_dwordx4 v[140:143], v[68:69], off
	global_load_dwordx4 v[128:131], v[68:69], off offset:528
	global_load_dwordx4 v[132:135], v[68:69], off offset:512
	s_and_b64 vcc, exec, s[100:101]
	s_cbranch_vccnz .Lpfm3_none
	v_mbcnt_lo_u32_b32 v176, -1, 0
	v_mbcnt_hi_u32_b32 v176, -1, v176
	s_ashr_i32 s13, s12, 31
	v_or_b32_e32 v68, s87, v176
	v_bfe_u32 v178, v176, 3, 3
	v_readfirstlane_b32 s4, v68
	s_ashr_i32 s15, s4, 6
	s_lshl_b32 s4, s15, 3
	v_lshrrev_b32_e32 v177, 3, v176
	v_or_b32_e32 v179, s4, v178
	v_xor_b32_e32 v176, v177, v176
	s_lshl_b32 s5, s15, 1
	v_lshlrev_b32_e32 v177, 1, v179
	v_mov_b32_e32 v179, 0x63
	s_and_b32 s5, s5, 4
	v_and_b32_e32 v177, 24, v177
	v_bitop3_b32 v178, s4, v179, v178 bitop3:0xc8
	v_lshlrev_b32_e32 v176, 4, v176
	v_or3_b32 v177, s5, v178, v177
	v_and_b32_e32 v176, 0x70, v176
	s_lshl_b32 s4, s44, 19
	v_lshlrev_b32_e32 v177, 11, v177
	v_lshl_add_u32 v68, v68, 2, 0
	v_or3_b32 v176, v177, s4, v176
	s_lshl_b64 s[4:5], s[12:13], 22
	v_add_u32_e32 v70, 0x22410, v68
	s_add_u32 s4, s52, s4
	ds_read2st64_b32 v[68:69], v70 offset1:8
	ds_read2st64_b32 v[70:71], v70 offset0:16 offset1:24
	s_addc_u32 s5, s53, s5
	s_lshl_b32 s13, s15, 10
	s_add_i32 s13, s13, 0
	s_and_b32 s5, s5, 0xffff
	s_add_i32 s15, s13, 0x10010
	s_mov_b32 m0, s15
	s_nop 0
	buffer_load_dwordx4 v176, s[4:7], s31 offen lds
	s_add_i32 s15, s13, 0x12010
	s_mov_b32 m0, s15
	s_nop 0
	buffer_load_dwordx4 v176, s[4:7], s7 offen lds
	s_add_i32 s15, s13, 16
	s_waitcnt lgkmcnt(1)
	s_mov_b32 m0, s15
	s_nop 0
	buffer_load_dwordx4 v68, s[8:11], s31 offen lds
	s_add_i32 s15, s13, 0x2010
	s_mov_b32 m0, s15
	s_nop 0
	buffer_load_dwordx4 v69, s[8:11], s31 offen lds
	s_add_i32 s15, s13, 0x14010
	s_mov_b32 m0, s15
	s_nop 0
	buffer_load_dwordx4 v176, s[4:7], s34 offen lds
	s_add_i32 s15, s13, 0x16010
	s_mov_b32 m0, s15
	s_nop 0
	buffer_load_dwordx4 v176, s[4:7], s35 offen lds
	s_add_i32 s15, s13, 0x4010
	s_waitcnt lgkmcnt(0)
	s_mov_b32 m0, s15
	s_nop 0
	buffer_load_dwordx4 v70, s[8:11], s31 offen lds
	s_add_i32 s15, s13, 0x6010
	s_mov_b32 m0, s15
	s_nop 0
	buffer_load_dwordx4 v71, s[8:11], s31 offen lds
	s_add_i32 s15, s13, 0x18010
	s_mov_b32 m0, s15
	s_nop 0
	buffer_load_dwordx4 v176, s[4:7], s33 offen lds
	s_add_i32 s15, s13, 0x1a010
	s_mov_b32 m0, s15
	s_nop 0
	buffer_load_dwordx4 v176, s[4:7], s36 offen lds
	s_add_i32 s15, s13, 0x8010
	s_mov_b32 m0, s15
	s_nop 0
	buffer_load_dwordx4 v68, s[8:11], s33 offen lds
	s_add_i32 s15, s13, 0xa010
	s_mov_b32 m0, s15
	s_nop 0
	buffer_load_dwordx4 v69, s[8:11], s33 offen lds
	s_add_i32 s15, s13, 0x1c010
	s_mov_b32 m0, s15
	s_nop 0
	buffer_load_dwordx4 v176, s[4:7], s37 offen lds
	s_add_i32 s13, s13, 0x1e010
	s_mov_b32 m0, s13
	s_nop 0
	buffer_load_dwordx4 v176, s[4:7], s42 offen lds
	s_branch .Lpfm3_done

;   DI void epi_t(const RowTok& t, const ColCtx& c, const f32x4& v0, const f32x4& v1) const {
;     if (t.a < 0) return;
;     const f32x4 x0 = (v0 + c.b0) * t.gt, x1 = (v1 + c.b1) * t.gt;
;     u32x4 pk; pk.x = pack2(x0[0], x0[1]); pk.y = pack2(x0[2], x0[3]); pk.z = pack2(x1[0], x1[1]); pk.w = pack2(x1[2], x1[3]);
;     *(u32x4*)(p.yb + (size_t)t.a * 2048 + c.gc) = pk;
;   }
.Lpfm3_done:
	v_cmp_gt_i32_e32 vcc, s43, v144
	v_readlane_b32 s61, v254, 7
	v_readlane_b32 s62, v254, 8
	v_readlane_b32 s63, v254, 9
	v_readlane_b32 s64, v254, 10
	v_readlane_b32 s65, v254, 11
	s_waitcnt vmcnt(25)
	v_cndmask_b32_e32 v252, -1, v162, vcc
	v_cmp_lt_i32_e32 vcc, -1, v252
	s_and_saveexec_b64 s[4:5], vcc
	s_cbranch_execz .LBB0_1681
	s_waitcnt vmcnt(16)
	v_pk_add_f32 v[68:69], v[126:127], v[142:143]
	v_pk_add_f32 v[70:71], v[124:125], v[140:141]
	v_lshlrev_b64 v[144:145], 12, v[252:253]
	v_pk_mul_f32 v[124:125], v[162:163], v[68:69] op_sel:[1,0]
	v_pk_mul_f32 v[68:69], v[162:163], v[70:71] op_sel:[1,0]
	v_pk_add_f32 v[70:71], v[122:123], v[138:139]
	v_pk_add_f32 v[120:121], v[120:121], v[136:137]
	v_pk_mul_f32 v[122:123], v[162:163], v[70:71] op_sel:[1,0]
	v_pk_mul_f32 v[70:71], v[162:163], v[120:121] op_sel:[1,0]
	v_lshl_add_u64 v[120:121], s[40:41], 0, v[144:145]
	v_cvt_pk_bf16_f32 v68, v68, v69
	v_cvt_pk_bf16_f32 v69, v124, v125
	v_cvt_pk_bf16_f32 v70, v70, v71
	v_cvt_pk_bf16_f32 v71, v122, v123
	v_lshl_add_u64 v[120:121], v[148:149], 1, v[120:121]
	global_store_dwordx4 v[120:121], v[68:71], off
	s_waitcnt vmcnt(16)
	v_pk_add_f32 v[112:113], v[112:113], v[128:129]
	s_waitcnt vmcnt(15)
	v_pk_add_f32 v[68:69], v[118:119], v[134:135]
	v_pk_add_f32 v[70:71], v[116:117], v[132:133]
	v_pk_mul_f32 v[116:117], v[162:163], v[68:69] op_sel:[1,0]
	v_pk_mul_f32 v[68:69], v[162:163], v[70:71] op_sel:[1,0]
	v_pk_add_f32 v[70:71], v[114:115], v[130:131]
	v_cvt_pk_bf16_f32 v68, v68, v69
	v_pk_mul_f32 v[114:115], v[162:163], v[70:71] op_sel:[1,0]
	v_pk_mul_f32 v[70:71], v[162:163], v[112:113] op_sel:[1,0]
	v_cvt_pk_bf16_f32 v69, v116, v117
	v_cvt_pk_bf16_f32 v70, v70, v71
	v_cvt_pk_bf16_f32 v71, v114, v115
	global_store_dwordx4 v[120:121], v[68:71], off offset:256
.LBB0_1681:
	s_or_b64 exec, exec, s[4:5]
	v_cmp_gt_i32_e32 vcc, s43, v173
	s_waitcnt vmcnt(24)
	s_nop 0
	v_cndmask_b32_e32 v252, -1, v160, vcc
	v_cmp_lt_i32_e32 vcc, -1, v252
	s_and_saveexec_b64 s[4:5], vcc
	s_cbranch_execz .LBB0_1683
	s_waitcnt vmcnt(16)
	v_pk_add_f32 v[68:69], v[110:111], v[142:143]
	v_pk_add_f32 v[70:71], v[108:109], v[140:141]
	v_lshlrev_b64 v[112:113], 12, v[252:253]
	v_pk_mul_f32 v[108:109], v[160:161], v[68:69] op_sel:[1,0]
	v_pk_mul_f32 v[68:69], v[160:161], v[70:71] op_sel:[1,0]
	v_pk_add_f32 v[70:71], v[102:103], v[138:139]
	v_pk_add_f32 v[100:101], v[100:101], v[136:137]
	v_pk_mul_f32 v[102:103], v[160:161], v[70:71] op_sel:[1,0]
	v_pk_mul_f32 v[70:71], v[160:161], v[100:101] op_sel:[1,0]
	v_lshl_add_u64 v[100:101], s[40:41], 0, v[112:113]
	v_cvt_pk_bf16_f32 v68, v68, v69
	v_cvt_pk_bf16_f32 v69, v108, v109
	v_cvt_pk_bf16_f32 v70, v70, v71
	v_cvt_pk_bf16_f32 v71, v102, v103
	v_lshl_add_u64 v[100:101], v[148:149], 1, v[100:101]
	global_store_dwordx4 v[100:101], v[68:71], off
	s_waitcnt vmcnt(16)
	v_pk_add_f32 v[96:97], v[96:97], v[128:129]
	s_waitcnt vmcnt(15)
	v_pk_add_f32 v[68:69], v[106:107], v[134:135]
	v_pk_add_f32 v[70:71], v[104:105], v[132:133]
	v_pk_mul_f32 v[102:103], v[160:161], v[68:69] op_sel:[1,0]
	v_pk_mul_f32 v[68:69], v[160:161], v[70:71] op_sel:[1,0]
	v_pk_add_f32 v[70:71], v[98:99], v[130:131]
	v_cvt_pk_bf16_f32 v68, v68, v69
	v_pk_mul_f32 v[98:99], v[160:161], v[70:71] op_sel:[1,0]
	v_pk_mul_f32 v[70:71], v[160:161], v[96:97] op_sel:[1,0]
	v_cvt_pk_bf16_f32 v69, v102, v103
	v_cvt_pk_bf16_f32 v70, v70, v71
	v_cvt_pk_bf16_f32 v71, v98, v99
	global_store_dwordx4 v[100:101], v[68:71], off offset:256
.LBB0_1683:
	s_or_b64 exec, exec, s[4:5]
	v_cmp_gt_i32_e32 vcc, s43, v172
	s_waitcnt vmcnt(23)
	s_nop 0
	v_cndmask_b32_e32 v252, -1, v158, vcc
	v_cmp_lt_i32_e32 vcc, -1, v252
	s_and_saveexec_b64 s[4:5], vcc
	s_cbranch_execz .LBB0_1685
	s_waitcnt vmcnt(16)
	v_pk_add_f32 v[68:69], v[86:87], v[142:143]
	v_pk_add_f32 v[70:71], v[84:85], v[140:141]
	v_lshlrev_b64 v[96:97], 12, v[252:253]
	v_pk_mul_f32 v[84:85], v[158:159], v[68:69] op_sel:[1,0]
	v_pk_mul_f32 v[68:69], v[158:159], v[70:71] op_sel:[1,0]
	v_pk_add_f32 v[70:71], v[82:83], v[138:139]
	v_pk_add_f32 v[80:81], v[80:81], v[136:137]
	v_pk_mul_f32 v[82:83], v[158:159], v[70:71] op_sel:[1,0]
	v_pk_mul_f32 v[70:71], v[158:159], v[80:81] op_sel:[1,0]
	v_lshl_add_u64 v[80:81], s[40:41], 0, v[96:97]
	v_cvt_pk_bf16_f32 v68, v68, v69
	v_cvt_pk_bf16_f32 v69, v84, v85
	v_cvt_pk_bf16_f32 v70, v70, v71
	v_cvt_pk_bf16_f32 v71, v82, v83
	v_lshl_add_u64 v[80:81], v[148:149], 1, v[80:81]
	global_store_dwordx4 v[80:81], v[68:71], off
	s_waitcnt vmcnt(16)
	v_pk_add_f32 v[84:85], v[88:89], v[128:129]
	s_waitcnt vmcnt(15)
	v_pk_add_f32 v[68:69], v[94:95], v[134:135]
	v_pk_add_f32 v[70:71], v[92:93], v[132:133]
	v_pk_mul_f32 v[82:83], v[158:159], v[68:69] op_sel:[1,0]
	v_pk_mul_f32 v[68:69], v[158:159], v[70:71] op_sel:[1,0]
	v_pk_add_f32 v[70:71], v[90:91], v[130:131]
	v_cvt_pk_bf16_f32 v68, v68, v69
	v_pk_mul_f32 v[86:87], v[158:159], v[70:71] op_sel:[1,0]
	v_pk_mul_f32 v[70:71], v[158:159], v[84:85] op_sel:[1,0]
	v_cvt_pk_bf16_f32 v69, v82, v83
	v_cvt_pk_bf16_f32 v70, v70, v71
	v_cvt_pk_bf16_f32 v71, v86, v87
	global_store_dwordx4 v[80:81], v[68:71], off offset:256
;   DI void epi_t(const RowTok& t, const ColCtx& c, const f32x4& v0, const f32x4& v1) const {
;     if (t.a < 0) return;
;     const f32x4 x0 = (v0 + c.b0) * t.gt, x1 = (v1 + c.b1) * t.gt;
;     u32x4 pk; pk.x = pack2(x0[0], x0[1]); pk.y = pack2(x0[2], x0[3]); pk.z = pack2(x1[0], x1[1]); pk.w = pack2(x1[2], x1[3]);
;     *(u32x4*)(p.yb + (size_t)t.a * 2048 + c.gc) = pk;
;   }
.LBB0_1685:
	s_or_b64 exec, exec, s[4:5]
	v_cmp_gt_i32_e32 vcc, s43, v171
	s_waitcnt vmcnt(22)
	s_nop 0
	v_cndmask_b32_e32 v252, -1, v156, vcc
	v_cmp_lt_i32_e32 vcc, -1, v252
	s_and_saveexec_b64 s[4:5], vcc
	s_cbranch_execz .LBB0_1687
	v_lshlrev_b64 v[68:69], 12, v[252:253]
	s_waitcnt vmcnt(16)
	v_pk_add_f32 v[70:71], v[222:223], v[142:143]
	v_pk_add_f32 v[80:81], v[220:221], v[140:141]
	v_pk_add_f32 v[50:51], v[50:51], v[138:139]
	v_pk_add_f32 v[48:49], v[48:49], v[136:137]
	v_pk_mul_f32 v[70:71], v[156:157], v[70:71] op_sel:[1,0]
	v_pk_mul_f32 v[80:81], v[156:157], v[80:81] op_sel:[1,0]
	v_pk_mul_f32 v[82:83], v[156:157], v[50:51] op_sel:[1,0]
	v_pk_mul_f32 v[50:51], v[156:157], v[48:49] op_sel:[1,0]
	v_lshl_add_u64 v[68:69], s[40:41], 0, v[68:69]
	v_cvt_pk_bf16_f32 v48, v80, v81
	v_cvt_pk_bf16_f32 v49, v70, v71
	v_cvt_pk_bf16_f32 v50, v50, v51
	v_cvt_pk_bf16_f32 v51, v82, v83
	v_lshl_add_u64 v[68:69], v[148:149], 1, v[68:69]
	global_store_dwordx4 v[68:69], v[48:51], off
	s_waitcnt vmcnt(16)
	v_pk_add_f32 v[72:73], v[72:73], v[128:129]
	s_waitcnt vmcnt(15)
	v_pk_add_f32 v[48:49], v[78:79], v[134:135]
	v_pk_add_f32 v[50:51], v[76:77], v[132:133]
	v_pk_mul_f32 v[70:71], v[156:157], v[48:49] op_sel:[1,0]
	v_pk_mul_f32 v[48:49], v[156:157], v[50:51] op_sel:[1,0]
	v_pk_add_f32 v[50:51], v[74:75], v[130:131]
	v_cvt_pk_bf16_f32 v48, v48, v49
	v_pk_mul_f32 v[74:75], v[156:157], v[50:51] op_sel:[1,0]
	v_pk_mul_f32 v[50:51], v[156:157], v[72:73] op_sel:[1,0]
	v_cvt_pk_bf16_f32 v49, v70, v71
	v_cvt_pk_bf16_f32 v50, v50, v51
	v_cvt_pk_bf16_f32 v51, v74, v75
	global_store_dwordx4 v[68:69], v[48:51], off offset:256
.LBB0_1687:
	s_or_b64 exec, exec, s[4:5]
	v_cmp_gt_i32_e32 vcc, s43, v170
	s_waitcnt vmcnt(21)
	s_nop 0
	v_cndmask_b32_e32 v252, -1, v154, vcc
	v_cmp_lt_i32_e32 vcc, -1, v252
	s_and_saveexec_b64 s[4:5], vcc
	s_cbranch_execz .LBB0_1689
	s_waitcnt vmcnt(16)
	v_pk_add_f32 v[48:49], v[58:59], v[142:143]
	v_pk_add_f32 v[50:51], v[56:57], v[140:141]
	v_lshlrev_b64 v[68:69], 12, v[252:253]
	v_pk_mul_f32 v[56:57], v[154:155], v[48:49] op_sel:[1,0]
	v_pk_mul_f32 v[48:49], v[154:155], v[50:51] op_sel:[1,0]
	v_pk_add_f32 v[50:51], v[54:55], v[138:139]
	v_pk_add_f32 v[52:53], v[52:53], v[136:137]
	v_pk_mul_f32 v[54:55], v[154:155], v[50:51] op_sel:[1,0]
	v_pk_mul_f32 v[50:51], v[154:155], v[52:53] op_sel:[1,0]
	v_lshl_add_u64 v[52:53], s[40:41], 0, v[68:69]
	v_cvt_pk_bf16_f32 v48, v48, v49
	v_cvt_pk_bf16_f32 v49, v56, v57
	v_cvt_pk_bf16_f32 v50, v50, v51
	v_cvt_pk_bf16_f32 v51, v54, v55
	v_lshl_add_u64 v[52:53], v[148:149], 1, v[52:53]
	global_store_dwordx4 v[52:53], v[48:51], off
	s_waitcnt vmcnt(16)
	v_pk_add_f32 v[56:57], v[60:61], v[128:129]
	s_waitcnt vmcnt(15)
	v_pk_add_f32 v[48:49], v[66:67], v[134:135]
	v_pk_add_f32 v[50:51], v[64:65], v[132:133]
	v_pk_mul_f32 v[54:55], v[154:155], v[48:49] op_sel:[1,0]
	v_pk_mul_f32 v[48:49], v[154:155], v[50:51] op_sel:[1,0]
	v_pk_add_f32 v[50:51], v[62:63], v[130:131]
	v_cvt_pk_bf16_f32 v48, v48, v49
	v_pk_mul_f32 v[58:59], v[154:155], v[50:51] op_sel:[1,0]
	v_pk_mul_f32 v[50:51], v[154:155], v[56:57] op_sel:[1,0]
	v_cvt_pk_bf16_f32 v49, v54, v55
	v_cvt_pk_bf16_f32 v50, v50, v51
	v_cvt_pk_bf16_f32 v51, v58, v59
	global_store_dwordx4 v[52:53], v[48:51], off offset:256
;   DI void epi_t(const RowTok& t, const ColCtx& c, const f32x4& v0, const f32x4& v1) const {
;     if (t.a < 0) return;
;     const f32x4 x0 = (v0 + c.b0) * t.gt, x1 = (v1 + c.b1) * t.gt;
;     u32x4 pk; pk.x = pack2(x0[0], x0[1]); pk.y = pack2(x0[2], x0[3]); pk.z = pack2(x1[0], x1[1]); pk.w = pack2(x1[2], x1[3]);
;     *(u32x4*)(p.yb + (size_t)t.a * 2048 + c.gc) = pk;
;   }
.LBB0_1689:
	s_or_b64 exec, exec, s[4:5]
	v_cmp_gt_i32_e32 vcc, s43, v169
	s_waitcnt vmcnt(20)
	s_nop 0
	v_cndmask_b32_e32 v252, -1, v152, vcc
	v_cmp_lt_i32_e32 vcc, -1, v252
	s_and_saveexec_b64 s[4:5], vcc
	s_cbranch_execz .LBB0_1691
	s_waitcnt vmcnt(16)
	v_pk_add_f32 v[36:37], v[36:37], v[140:141]
	v_lshlrev_b64 v[48:49], 12, v[252:253]
	v_pk_add_f32 v[38:39], v[38:39], v[142:143]
	v_pk_mul_f32 v[36:37], v[36:37], v[152:153] op_sel:[0,1]
	v_pk_add_f32 v[34:35], v[34:35], v[138:139]
	v_pk_add_f32 v[32:33], v[32:33], v[136:137]
	v_pk_mul_f32 v[38:39], v[38:39], v[152:153] op_sel:[0,1]
	v_pk_mul_f32 v[50:51], v[152:153], v[34:35] op_sel:[1,0]
	v_pk_mul_f32 v[34:35], v[152:153], v[32:33] op_sel:[1,0]
	v_cvt_pk_bf16_f32 v32, v36, v37
	v_lshl_add_u64 v[36:37], s[40:41], 0, v[48:49]
	v_cvt_pk_bf16_f32 v33, v38, v39
	v_cvt_pk_bf16_f32 v34, v34, v35
	v_cvt_pk_bf16_f32 v35, v50, v51
	v_lshl_add_u64 v[36:37], v[148:149], 1, v[36:37]
	global_store_dwordx4 v[36:37], v[32:35], off
	s_waitcnt vmcnt(16)
	v_pk_add_f32 v[40:41], v[40:41], v[128:129]
	s_waitcnt vmcnt(15)
	v_pk_add_f32 v[32:33], v[46:47], v[134:135]
	v_pk_add_f32 v[34:35], v[44:45], v[132:133]
	v_pk_mul_f32 v[38:39], v[152:153], v[32:33] op_sel:[1,0]
	v_pk_mul_f32 v[32:33], v[152:153], v[34:35] op_sel:[1,0]
	v_pk_add_f32 v[34:35], v[42:43], v[130:131]
	v_cvt_pk_bf16_f32 v32, v32, v33
	v_pk_mul_f32 v[42:43], v[152:153], v[34:35] op_sel:[1,0]
	v_pk_mul_f32 v[34:35], v[152:153], v[40:41] op_sel:[1,0]
	v_cvt_pk_bf16_f32 v33, v38, v39
	v_cvt_pk_bf16_f32 v34, v34, v35
	v_cvt_pk_bf16_f32 v35, v42, v43
	global_store_dwordx4 v[36:37], v[32:35], off offset:256
.LBB0_1691:
	s_or_b64 exec, exec, s[4:5]
	v_cmp_gt_i32_e32 vcc, s43, v168
	s_waitcnt vmcnt(19)
	s_nop 0
	v_cndmask_b32_e32 v252, -1, v150, vcc
	v_cmp_lt_i32_e32 vcc, -1, v252
	s_and_saveexec_b64 s[4:5], vcc
	s_cbranch_execz .LBB0_1693
	s_waitcnt vmcnt(16)
	v_pk_add_f32 v[20:21], v[20:21], v[140:141]
	v_lshlrev_b64 v[32:33], 12, v[252:253]
	v_pk_add_f32 v[22:23], v[22:23], v[142:143]
	v_pk_mul_f32 v[20:21], v[20:21], v[150:151] op_sel:[0,1]
	v_pk_add_f32 v[18:19], v[18:19], v[138:139]
	v_pk_add_f32 v[16:17], v[16:17], v[136:137]
	v_pk_mul_f32 v[22:23], v[22:23], v[150:151] op_sel:[0,1]
	v_pk_mul_f32 v[34:35], v[18:19], v[150:151] op_sel:[0,1]
	v_pk_mul_f32 v[18:19], v[16:17], v[150:151] op_sel:[0,1]
	v_cvt_pk_bf16_f32 v16, v20, v21
	v_lshl_add_u64 v[20:21], s[40:41], 0, v[32:33]
	v_cvt_pk_bf16_f32 v17, v22, v23
	v_cvt_pk_bf16_f32 v18, v18, v19
	v_cvt_pk_bf16_f32 v19, v34, v35
	v_lshl_add_u64 v[20:21], v[148:149], 1, v[20:21]
	global_store_dwordx4 v[20:21], v[16:19], off
	s_waitcnt vmcnt(16)
	v_pk_add_f32 v[24:25], v[24:25], v[128:129]
	s_waitcnt vmcnt(15)
	v_pk_add_f32 v[16:17], v[30:31], v[134:135]
	v_pk_add_f32 v[18:19], v[28:29], v[132:133]
	v_pk_mul_f32 v[22:23], v[150:151], v[16:17] op_sel:[1,0]
	v_pk_mul_f32 v[16:17], v[150:151], v[18:19] op_sel:[1,0]
	v_pk_add_f32 v[18:19], v[26:27], v[130:131]
	v_cvt_pk_bf16_f32 v16, v16, v17
	v_pk_mul_f32 v[26:27], v[150:151], v[18:19] op_sel:[1,0]
	v_pk_mul_f32 v[18:19], v[150:151], v[24:25] op_sel:[1,0]
	v_cvt_pk_bf16_f32 v17, v22, v23
	v_cvt_pk_bf16_f32 v18, v18, v19
	v_cvt_pk_bf16_f32 v19, v26, v27
	global_store_dwordx4 v[20:21], v[16:19], off offset:256
.LBB0_1693:
	s_or_b64 exec, exec, s[4:5]
	v_cmp_gt_i32_e32 vcc, s43, v167
	s_waitcnt vmcnt(18)
	s_nop 0
	v_cndmask_b32_e32 v252, -1, v146, vcc
	v_cmp_lt_i32_e32 vcc, -1, v252
	s_and_saveexec_b64 s[4:5], vcc
	s_cbranch_execz .LBB0_1695
	s_waitcnt vmcnt(16)
	v_pk_add_f32 v[4:5], v[4:5], v[140:141]
	v_lshlrev_b64 v[16:17], 12, v[252:253]
	v_pk_add_f32 v[6:7], v[6:7], v[142:143]
	v_pk_mul_f32 v[4:5], v[4:5], v[146:147] op_sel:[0,1]
	v_pk_add_f32 v[2:3], v[2:3], v[138:139]
	v_pk_add_f32 v[0:1], v[0:1], v[136:137]
	v_pk_mul_f32 v[6:7], v[6:7], v[146:147] op_sel:[0,1]
	v_pk_mul_f32 v[18:19], v[2:3], v[146:147] op_sel:[0,1]
	v_pk_mul_f32 v[2:3], v[0:1], v[146:147] op_sel:[0,1]
	v_cvt_pk_bf16_f32 v0, v4, v5
	v_lshl_add_u64 v[4:5], s[40:41], 0, v[16:17]
	v_cvt_pk_bf16_f32 v1, v6, v7
	v_cvt_pk_bf16_f32 v2, v2, v3
	v_cvt_pk_bf16_f32 v3, v18, v19
	v_lshl_add_u64 v[4:5], v[148:149], 1, v[4:5]
	global_store_dwordx4 v[4:5], v[0:3], off
	s_waitcnt vmcnt(16)
	v_pk_add_f32 v[8:9], v[8:9], v[128:129]
	s_waitcnt vmcnt(15)
	v_pk_add_f32 v[0:1], v[14:15], v[134:135]
	v_pk_add_f32 v[2:3], v[12:13], v[132:133]
	v_pk_mul_f32 v[6:7], v[0:1], v[146:147] op_sel:[0,1]
	v_pk_mul_f32 v[0:1], v[2:3], v[146:147] op_sel:[0,1]
	v_pk_add_f32 v[2:3], v[10:11], v[130:131]
	v_cvt_pk_bf16_f32 v0, v0, v1
	v_pk_mul_f32 v[10:11], v[146:147], v[2:3] op_sel:[1,0]
	v_pk_mul_f32 v[2:3], v[146:147], v[8:9] op_sel:[1,0]
	v_cvt_pk_bf16_f32 v1, v6, v7
	v_cvt_pk_bf16_f32 v2, v2, v3
	v_cvt_pk_bf16_f32 v3, v10, v11
	global_store_dwordx4 v[4:5], v[0:3], off offset:256

; __global__ void __launch_bounds__(NTHREADS, 2) k_forward(Params p_in) {
;   Params p = p_in;
;   p.wid0 = __builtin_amdgcn_readfirstlane((int)(threadIdx.x >> 6));
	.amdhsa_kernel _Z9k_forward6Params
		.amdhsa_group_segment_fixed_size 0
		.amdhsa_private_segment_fixed_size 0
		.amdhsa_kernarg_size 712
		.amdhsa_user_sgpr_count 2
		.amdhsa_user_sgpr_dispatch_ptr 0
		.amdhsa_user_sgpr_queue_ptr 0
		.amdhsa_user_sgpr_kernarg_segment_ptr 1
		.amdhsa_user_sgpr_dispatch_id 0
		.amdhsa_user_sgpr_kernarg_preload_length 0
		.amdhsa_user_sgpr_kernarg_preload_offset 0
		.amdhsa_user_sgpr_private_segment_size 0
		.amdhsa_uses_dynamic_stack 0
		.amdhsa_enable_private_segment 0
		.amdhsa_system_sgpr_workgroup_id_x 1
		.amdhsa_system_sgpr_workgroup_id_y 0
		.amdhsa_system_sgpr_workgroup_id_z 0
		.amdhsa_system_sgpr_workgroup_info 0
		.amdhsa_system_vgpr_workitem_id 0
		.amdhsa_next_free_vgpr 256
		.amdhsa_next_free_sgpr 102
		.amdhsa_accum_offset 256
		.amdhsa_reserve_vcc 1
		.amdhsa_float_round_mode_32 0
		.amdhsa_float_round_mode_16_64 0
		.amdhsa_float_denorm_mode_32 3
		.amdhsa_float_denorm_mode_16_64 3
		.amdhsa_dx10_clamp 1
		.amdhsa_ieee_mode 1
		.amdhsa_fp16_overflow 0
		.amdhsa_tg_split 0
		.amdhsa_exception_fp_ieee_invalid_op 0
		.amdhsa_exception_fp_denorm_src 0
		.amdhsa_exception_fp_ieee_div_zero 0
		.amdhsa_exception_fp_ieee_overflow 0
		.amdhsa_exception_fp_ieee_underflow 0
		.amdhsa_exception_fp_ieee_inexact 0
		.amdhsa_exception_int_div_zero 0
	.end_amdhsa_kernel

; __global__ void __launch_bounds__(NTHREADS, 2) k_forward(Params p_in) {
;   Params p = p_in;
;   p.wid0 = __builtin_amdgcn_readfirstlane((int)(threadIdx.x >> 6));
amdhsa.kernels:
  - .agpr_count:     0
    .args:
      - .offset:         0
        .size:           456
        .value_kind:     by_value
      - .offset:         456
        .size:           4
        .value_kind:     hidden_block_count_x
      - .offset:         460
        .size:           4
        .value_kind:     hidden_block_count_y
      - .offset:         464
        .size:           4
        .value_kind:     hidden_block_count_z
      - .offset:         468
        .size:           2
        .value_kind:     hidden_group_size_x
      - .offset:         470
        .size:           2
        .value_kind:     hidden_group_size_y
      - .offset:         472
        .size:           2
        .value_kind:     hidden_group_size_z
      - .offset:         474
        .size:           2
        .value_kind:     hidden_remainder_x
      - .offset:         476
        .size:           2
        .value_kind:     hidden_remainder_y
      - .offset:         478
        .size:           2
        .value_kind:     hidden_remainder_z
      - .offset:         496
        .size:           8
        .value_kind:     hidden_global_offset_x
      - .offset:         504
        .size:           8
        .value_kind:     hidden_global_offset_y
      - .offset:         512
        .size:           8
        .value_kind:     hidden_global_offset_z
      - .offset:         520
        .size:           2
        .value_kind:     hidden_grid_dims
      - .offset:         576
        .size:           4
        .value_kind:     hidden_dynamic_lds_size
    .group_segment_fixed_size: 0
    .kernarg_segment_align: 8
    .kernarg_segment_size: 712
    .language:       OpenCL C
    .language_version:
      - 2
      - 0
    .max_flat_workgroup_size: 512
    .name:           _Z9k_forward6Params
    .private_segment_fixed_size: 0
    .sgpr_count:     108
    .sgpr_spill_count: 161
    .symbol:         _Z9k_forward6Params.kd
    .uniform_work_group_size: 1
    .uses_dynamic_stack: false
    .vgpr_count:     256
    .vgpr_spill_count: 0
    .wavefront_size: 64
